# context-row partial sums: gate vector loads hoisted ahead of the partial-product loads (one memory round trip per slice)
# baseline (speedup 1.0000x reference)
.LBB0_961:
	s_add_i32 s26, s88, s80
	s_cmpk_lt_i32 s26, 0x4400
	s_cselect_b64 s[10:11], -1, 0
	s_and_b64 s[8:9], s[10:11], exec
	s_cselect_b32 s8, s26, s80
	s_ashr_i32 s9, s8, 31
	v_readlane_b32 s3, v254, 8
	s_lshl_b64 s[8:9], s[8:9], 11
	s_add_i32 s20, s3, s80
	s_cmpk_lt_i32 s20, 0x4400
	s_cselect_b64 s[22:23], -1, 0
	v_lshl_add_u64 v[20:21], v[52:53], 0, s[8:9]
	s_and_b64 s[8:9], s[22:23], exec
	s_cselect_b32 s8, s20, s80
	s_ashr_i32 s9, s8, 31
	v_readlane_b32 s3, v255, 10
	s_lshl_b64 s[8:9], s[8:9], 11
	s_add_i32 s12, s3, s80
	s_cmpk_lt_i32 s12, 0x4400
	s_cselect_b64 s[18:19], -1, 0
	global_load_dwordx2 v[104:105], v[20:21], off
	global_load_dwordx2 v[102:103], v[20:21], off offset:512
	global_load_dwordx2 v[100:101], v[20:21], off offset:1024
	global_load_dwordx2 v[98:99], v[20:21], off offset:1536
	v_lshl_add_u64 v[20:21], v[52:53], 0, s[8:9]
	s_and_b64 s[8:9], s[18:19], exec
	s_cselect_b32 s8, s12, s80
	s_mov_b32 s3, 0xfbc00000
	global_load_dwordx2 v[96:97], v[20:21], off
	global_load_dwordx2 v[94:95], v[20:21], off offset:512
	global_load_dwordx2 v[92:93], v[20:21], off offset:1024
	global_load_dwordx2 v[90:91], v[20:21], off offset:1536
	s_ashr_i32 s9, s8, 31
	v_add_co_u32_e32 v20, vcc, s3, v72
	s_lshl_b64 s[8:9], s[8:9], 11
	s_nop 0
	v_addc_co_u32_e32 v21, vcc, -1, v73, vcc
	global_load_dwordx2 v[108:109], v[20:21], off
	global_load_dwordx2 v[106:107], v[20:21], off offset:-512
	global_load_dwordx2 v[114:115], v[20:21], off offset:-1024
	global_load_dwordx2 v[110:111], v[20:21], off offset:-1536
	v_lshl_add_u64 v[20:21], v[52:53], 0, s[8:9]
	v_readlane_b32 s8, v255, 18
	s_add_i32 s8, s8, s80
	s_cmpk_lt_i32 s8, 0x4400
	s_cselect_b64 s[14:15], -1, 0
	s_and_b64 s[36:37], s[14:15], exec
	s_cselect_b32 s36, s8, s80
	s_ashr_i32 s37, s36, 31
	s_lshl_b64 s[36:37], s[36:37], 11
	global_load_dwordx2 v[88:89], v[20:21], off
	global_load_dwordx2 v[86:87], v[20:21], off offset:512
	global_load_dwordx2 v[84:85], v[20:21], off offset:1024
	global_load_dwordx2 v[82:83], v[20:21], off offset:1536
	v_lshl_add_u64 v[20:21], v[52:53], 0, s[36:37]
	global_load_dwordx2 v[80:81], v[20:21], off
	global_load_dwordx2 v[78:79], v[20:21], off offset:512
	global_load_dwordx2 v[76:77], v[20:21], off offset:1024
	global_load_dwordx2 v[74:75], v[20:21], off offset:1536
	s_min_i32 s3, s80, 0x4000
	s_and_b32 s3, s3, 0xfffff000
	v_readlane_b32 s9, v255, 19
	s_add_i32 s3, s3, 0
	s_add_i32 s9, s3, 0xa000
	v_add_u32_e32 v1, s3, v54
	v_add_u32_e32 v2, s9, v54
	ds_read_b128 v[44:47], v1 offset:45056
	ds_read_b128 v[36:39], v1 offset:46080
	ds_read_b128 v[48:51], v2 offset:24576
	ds_read_b128 v[40:43], v2 offset:25600
	ds_read_b128 v[28:31], v1 offset:47104
	ds_read_b128 v[20:23], v1 offset:48128
	ds_read_b128 v[32:35], v2 offset:26624
	ds_read_b128 v[24:27], v2 offset:27648
	s_cmpk_lt_i32 s80, 0x4000
	s_waitcnt vmcnt(10)
	v_lshlrev_b32_e32 v116, 16, v107
	s_waitcnt vmcnt(9)
	v_lshlrev_b32_e32 v120, 16, v114
	s_waitcnt vmcnt(8)
	v_lshlrev_b32_e32 v112, 16, v110
	v_and_b32_e32 v113, 0xffff0000, v110
	v_lshlrev_b32_e32 v110, 16, v111
	v_and_b32_e32 v111, 0xffff0000, v111
	v_and_b32_e32 v121, 0xffff0000, v114
	v_lshlrev_b32_e32 v118, 16, v115
	v_and_b32_e32 v119, 0xffff0000, v115
	v_lshlrev_b32_e32 v114, 16, v106
	v_and_b32_e32 v115, 0xffff0000, v106
	v_and_b32_e32 v117, 0xffff0000, v107
	v_lshlrev_b32_e32 v106, 16, v108
	v_and_b32_e32 v107, 0xffff0000, v108
	v_lshlrev_b32_e32 v108, 16, v109
	v_and_b32_e32 v109, 0xffff0000, v109
	s_cbranch_scc1 .LBB0_963
	global_load_dwordx4 v[236:239], v[58:59], off
	global_load_dwordx4 v[240:243], v[62:63], off
	global_load_dwordx4 v[244:247], v[66:67], off
	global_load_dwordx4 v[248:251], v[70:71], off
	s_mov_b32 s3, s81
	s_lshl_b64 s[38:39], s[80:81], 11
	s_lshl_b64 s[36:37], s[2:3], 2
	s_add_u32 s3, s0, s36
	s_addc_u32 s9, s1, s37
	s_add_u32 s40, s3, 0x420f8000
	s_addc_u32 s41, s9, 0
	v_lshlrev_b32_e32 v2, 4, v0
	v_lshl_add_u64 v[130:131], s[40:41], 0, v[2:3]
	s_mov_b32 s3, 0x400000
	v_add_co_u32_e32 v122, vcc, s3, v130
	s_mov_b32 s13, 0x800000
	s_nop 0
	v_addc_co_u32_e32 v123, vcc, 0, v131, vcc
	v_add_co_u32_e32 v126, vcc, s13, v130
	global_load_dwordx4 v[122:125], v[122:123], off
	s_nop 0
	v_addc_co_u32_e32 v127, vcc, 0, v131, vcc
	s_mov_b32 s9, 0xc00000
	v_mov_b32_e32 v1, v134
	global_load_dwordx4 v[134:137], v2, s[40:41]
	v_add_co_u32_e32 v130, vcc, s9, v130
	global_load_dwordx4 v[126:129], v[126:127], off
	s_nop 0
	v_addc_co_u32_e32 v131, vcc, 0, v131, vcc
	global_load_dwordx4 v[130:133], v[130:131], off
	v_lshlrev_b32_e32 v2, 4, v60
	s_waitcnt vmcnt(2)
	v_pk_add_f32 v[136:137], v[136:137], 0 op_sel_hi:[1,0]
	v_pk_add_f32 v[134:135], v[134:135], 0 op_sel_hi:[1,0]
	v_pk_add_f32 v[124:125], v[124:125], v[136:137]
	v_pk_add_f32 v[122:123], v[122:123], v[134:135]
	s_waitcnt vmcnt(1)
	v_pk_add_f32 v[124:125], v[128:129], v[124:125]
	v_pk_add_f32 v[122:123], v[126:127], v[122:123]
	s_waitcnt vmcnt(0)
	v_pk_add_f32 v[126:127], v[132:133], v[124:125]
	v_pk_add_f32 v[128:129], v[130:131], v[122:123]
	v_lshl_add_u64 v[130:131], s[40:41], 0, v[2:3]
	s_waitcnt vmcnt(0)
	v_pk_fma_f32 v[112:113], v[236:237], v[128:129], v[112:113]
	v_add_co_u32_e32 v122, vcc, s3, v130
	v_pk_fma_f32 v[110:111], v[238:239], v[126:127], v[110:111]
	s_nop 0
	v_addc_co_u32_e32 v123, vcc, 0, v131, vcc
	v_add_co_u32_e32 v126, vcc, s13, v130
	global_load_dwordx4 v[122:125], v[122:123], off
	s_nop 0
	v_addc_co_u32_e32 v127, vcc, 0, v131, vcc
	v_add_co_u32_e32 v130, vcc, s9, v130
	global_load_dwordx4 v[126:129], v[126:127], off
	s_nop 0
	v_addc_co_u32_e32 v131, vcc, 0, v131, vcc
	global_load_dwordx4 v[130:133], v[130:131], off
	s_nop 0
	global_load_dwordx4 v[134:137], v2, s[40:41]
	v_lshlrev_b32_e32 v2, 4, v64
	s_waitcnt vmcnt(0)
	v_pk_add_f32 v[136:137], v[136:137], 0 op_sel_hi:[1,0]
	v_pk_add_f32 v[134:135], v[134:135], 0 op_sel_hi:[1,0]
	v_pk_add_f32 v[124:125], v[124:125], v[136:137]
	v_pk_add_f32 v[122:123], v[122:123], v[134:135]
	v_pk_add_f32 v[124:125], v[128:129], v[124:125]
	v_pk_add_f32 v[122:123], v[126:127], v[122:123]
	v_pk_add_f32 v[126:127], v[132:133], v[124:125]
	v_pk_add_f32 v[128:129], v[130:131], v[122:123]
	v_lshl_add_u64 v[130:131], s[40:41], 0, v[2:3]
	s_waitcnt vmcnt(0)
	v_pk_fma_f32 v[120:121], v[240:241], v[128:129], v[120:121]
	v_add_co_u32_e32 v122, vcc, s3, v130
	v_pk_fma_f32 v[118:119], v[242:243], v[126:127], v[118:119]
	s_nop 0
	v_addc_co_u32_e32 v123, vcc, 0, v131, vcc
	v_add_co_u32_e32 v126, vcc, s13, v130
	global_load_dwordx4 v[122:125], v[122:123], off
	s_nop 0
	v_addc_co_u32_e32 v127, vcc, 0, v131, vcc
	v_add_co_u32_e32 v130, vcc, s9, v130
	global_load_dwordx4 v[126:129], v[126:127], off
	s_nop 0
	v_addc_co_u32_e32 v131, vcc, 0, v131, vcc
	global_load_dwordx4 v[130:133], v[130:131], off
	s_nop 0
	global_load_dwordx4 v[134:137], v2, s[40:41]
	v_lshlrev_b32_e32 v2, 4, v68
	s_waitcnt vmcnt(0)
	v_pk_add_f32 v[136:137], v[136:137], 0 op_sel_hi:[1,0]
	v_pk_add_f32 v[134:135], v[134:135], 0 op_sel_hi:[1,0]
	v_pk_add_f32 v[124:125], v[124:125], v[136:137]
	v_pk_add_f32 v[122:123], v[122:123], v[134:135]
	v_pk_add_f32 v[124:125], v[128:129], v[124:125]
	v_pk_add_f32 v[122:123], v[126:127], v[122:123]
	v_pk_add_f32 v[126:127], v[132:133], v[124:125]
	v_pk_add_f32 v[128:129], v[130:131], v[122:123]
	v_lshl_add_u64 v[130:131], s[40:41], 0, v[2:3]
	s_waitcnt vmcnt(0)
	v_pk_fma_f32 v[114:115], v[244:245], v[128:129], v[114:115]
	v_add_co_u32_e32 v122, vcc, s3, v130
	v_pk_fma_f32 v[116:117], v[246:247], v[126:127], v[116:117]
	s_nop 0
	v_addc_co_u32_e32 v123, vcc, 0, v131, vcc
	v_add_co_u32_e32 v126, vcc, s13, v130
	global_load_dwordx4 v[122:125], v[122:123], off
	s_nop 0
	v_addc_co_u32_e32 v127, vcc, 0, v131, vcc
	v_add_co_u32_e32 v130, vcc, s9, v130
	global_load_dwordx4 v[126:129], v[126:127], off
	s_nop 0
	v_addc_co_u32_e32 v131, vcc, 0, v131, vcc
	global_load_dwordx4 v[130:133], v[130:131], off
	s_nop 0
	global_load_dwordx4 v[134:137], v2, s[40:41]
	s_waitcnt vmcnt(0)
	v_pk_add_f32 v[136:137], v[136:137], 0 op_sel_hi:[1,0]
	v_pk_add_f32 v[134:135], v[134:135], 0 op_sel_hi:[1,0]
	v_pk_add_f32 v[124:125], v[124:125], v[136:137]
	v_pk_add_f32 v[122:123], v[122:123], v[134:135]
	v_pk_add_f32 v[124:125], v[128:129], v[124:125]
	v_pk_add_f32 v[122:123], v[126:127], v[122:123]
	v_pk_add_f32 v[126:127], v[132:133], v[124:125]
	v_pk_add_f32 v[128:129], v[130:131], v[122:123]
	v_mov_b32_e32 v134, v1
	s_waitcnt vmcnt(0)
	v_pk_fma_f32 v[108:109], v[250:251], v[126:127], v[108:109]
	v_pk_fma_f32 v[106:107], v[248:249], v[128:129], v[106:107]
	v_cvt_pk_bf16_f32 v122, v112, v113
	v_cvt_pk_bf16_f32 v123, v110, v111
	v_lshl_add_u64 v[124:125], v[52:53], 0, s[38:39]
	global_store_dwordx2 v[124:125], v[122:123], off
	v_lshlrev_b32_e32 v112, 16, v122
	v_and_b32_e32 v113, 0xffff0000, v122
	v_lshlrev_b32_e32 v110, 16, v123
	v_and_b32_e32 v111, 0xffff0000, v123
	v_cvt_pk_bf16_f32 v122, v120, v121
	v_cvt_pk_bf16_f32 v123, v118, v119
	global_store_dwordx2 v[124:125], v[122:123], off offset:512
	v_lshlrev_b32_e32 v120, 16, v122
	v_and_b32_e32 v121, 0xffff0000, v122
	v_lshlrev_b32_e32 v118, 16, v123
	v_and_b32_e32 v119, 0xffff0000, v123
	v_cvt_pk_bf16_f32 v122, v114, v115
	v_cvt_pk_bf16_f32 v123, v116, v117
	global_store_dwordx2 v[124:125], v[122:123], off offset:1024
	v_lshlrev_b32_e32 v114, 16, v122
	v_and_b32_e32 v115, 0xffff0000, v122
	v_lshlrev_b32_e32 v116, 16, v123
	v_and_b32_e32 v117, 0xffff0000, v123
	v_cvt_pk_bf16_f32 v122, v106, v107
	v_cvt_pk_bf16_f32 v123, v108, v109
	v_lshlrev_b32_e32 v106, 16, v122
	v_and_b32_e32 v107, 0xffff0000, v122
	v_lshlrev_b32_e32 v108, 16, v123
	v_and_b32_e32 v109, 0xffff0000, v123
	global_store_dwordx2 v[124:125], v[122:123], off offset:1536
	s_branch .LBB0_964

.LBB0_968:
	s_min_i32 s3, s26, 0x4000
	s_and_b32 s3, s3, 0xfffff000
	s_add_i32 s3, s3, 0
	s_add_i32 s9, s3, 0xa000
	v_add_u32_e32 v1, s3, v54
	v_add_u32_e32 v2, s9, v54
	ds_read_b128 v[44:47], v1 offset:45056
	ds_read_b128 v[36:39], v1 offset:46080
	ds_read_b128 v[48:51], v2 offset:24576
	ds_read_b128 v[40:43], v2 offset:25600
	ds_read_b128 v[28:31], v1 offset:47104
	ds_read_b128 v[20:23], v1 offset:48128
	ds_read_b128 v[32:35], v2 offset:26624
	ds_read_b128 v[24:27], v2 offset:27648
	v_lshlrev_b32_e32 v114, 16, v104
	v_and_b32_e32 v115, 0xffff0000, v104
	v_lshlrev_b32_e32 v104, 16, v105
	v_and_b32_e32 v105, 0xffff0000, v105
	v_lshlrev_b32_e32 v112, 16, v102
	v_and_b32_e32 v113, 0xffff0000, v102
	v_lshlrev_b32_e32 v110, 16, v103
	v_and_b32_e32 v111, 0xffff0000, v103
	v_lshlrev_b32_e32 v106, 16, v100
	v_and_b32_e32 v107, 0xffff0000, v100
	v_lshlrev_b32_e32 v108, 16, v101
	v_and_b32_e32 v109, 0xffff0000, v101
	v_lshlrev_b32_e32 v100, 16, v98
	v_and_b32_e32 v101, 0xffff0000, v98
	v_lshlrev_b32_e32 v98, 16, v99
	s_cmpk_lt_i32 s26, 0x4000
	v_and_b32_e32 v99, 0xffff0000, v99
	s_cbranch_scc1 .LBB0_970
	global_load_dwordx4 v[236:239], v[58:59], off
	global_load_dwordx4 v[240:243], v[62:63], off
	global_load_dwordx4 v[244:247], v[66:67], off
	global_load_dwordx4 v[248:251], v[70:71], off
	v_readlane_b32 s3, v255, 15
	s_mov_b32 s27, s81
	s_add_i32 s36, s3, s2
	s_mov_b32 s37, s81
	s_lshl_b64 s[10:11], s[26:27], 11
	s_lshl_b64 s[36:37], s[36:37], 2
	s_add_u32 s3, s0, s36
	s_addc_u32 s9, s1, s37
	s_add_u32 s38, s3, 0x420f8000
	s_addc_u32 s39, s9, 0
	v_lshlrev_b32_e32 v2, 4, v0
	v_lshl_add_u64 v[102:103], s[38:39], 0, v[2:3]
	s_mov_b32 s9, 0x400000
	v_add_co_u32_e32 v116, vcc, s9, v102
	s_mov_b32 s3, 0x800000
	s_nop 0
	v_addc_co_u32_e32 v117, vcc, 0, v103, vcc
	v_add_co_u32_e32 v120, vcc, s3, v102
	s_mov_b32 s13, 0xc00000
	s_nop 0
	v_addc_co_u32_e32 v121, vcc, 0, v103, vcc
	v_add_co_u32_e32 v102, vcc, s13, v102
	global_load_dwordx4 v[116:119], v[116:117], off
	s_nop 0
	v_addc_co_u32_e32 v103, vcc, 0, v103, vcc
	global_load_dwordx4 v[120:123], v[120:121], off
	s_nop 0
	global_load_dwordx4 v[124:127], v[102:103], off
	global_load_dwordx4 v[128:131], v2, s[38:39]
	v_lshlrev_b32_e32 v2, 4, v60
	s_waitcnt vmcnt(0)
	v_pk_add_f32 v[128:129], v[128:129], 0 op_sel_hi:[1,0]
	s_nop 0
	v_pk_add_f32 v[116:117], v[116:117], v[128:129]
	v_pk_add_f32 v[102:103], v[130:131], 0 op_sel_hi:[1,0]
	v_pk_add_f32 v[116:117], v[120:121], v[116:117]
	v_pk_add_f32 v[102:103], v[118:119], v[102:103]
	v_pk_add_f32 v[120:121], v[124:125], v[116:117]
	v_pk_add_f32 v[102:103], v[122:123], v[102:103]
	v_lshl_add_u64 v[122:123], s[38:39], 0, v[2:3]
	v_pk_add_f32 v[102:103], v[126:127], v[102:103]
	s_waitcnt vmcnt(0)
	v_pk_fma_f32 v[102:103], v[238:239], v[102:103], v[104:105]
	v_pk_fma_f32 v[104:105], v[236:237], v[120:121], v[114:115]
	v_add_co_u32_e32 v114, vcc, s9, v122
	v_cvt_pk_bf16_f32 v104, v104, v105
	s_nop 0
	v_addc_co_u32_e32 v115, vcc, 0, v123, vcc
	v_add_co_u32_e32 v118, vcc, s3, v122
	global_load_dwordx4 v[114:117], v[114:115], off
	s_nop 0
	v_addc_co_u32_e32 v119, vcc, 0, v123, vcc
	v_add_co_u32_e32 v122, vcc, s13, v122
	global_load_dwordx4 v[118:121], v[118:119], off
	s_nop 0
	v_addc_co_u32_e32 v123, vcc, 0, v123, vcc
	global_load_dwordx4 v[122:125], v[122:123], off
	s_nop 0
	global_load_dwordx4 v[126:129], v2, s[38:39]
	v_lshlrev_b32_e32 v2, 4, v64
	v_cvt_pk_bf16_f32 v105, v102, v103
	v_lshl_add_u64 v[102:103], v[52:53], 0, s[10:11]
	s_waitcnt vmcnt(0)
	v_pk_add_f32 v[128:129], v[128:129], 0 op_sel_hi:[1,0]
	v_pk_add_f32 v[126:127], v[126:127], 0 op_sel_hi:[1,0]
	v_pk_add_f32 v[116:117], v[116:117], v[128:129]
	v_pk_add_f32 v[114:115], v[114:115], v[126:127]
	v_pk_add_f32 v[116:117], v[120:121], v[116:117]
	v_pk_add_f32 v[114:115], v[118:119], v[114:115]
	v_pk_add_f32 v[118:119], v[124:125], v[116:117]
	v_pk_add_f32 v[120:121], v[122:123], v[114:115]
	v_lshl_add_u64 v[122:123], s[38:39], 0, v[2:3]
	s_waitcnt vmcnt(0)
	v_pk_fma_f32 v[112:113], v[240:241], v[120:121], v[112:113]
	v_add_co_u32_e32 v114, vcc, s9, v122
	v_pk_fma_f32 v[110:111], v[242:243], v[118:119], v[110:111]
	s_nop 0
	v_addc_co_u32_e32 v115, vcc, 0, v123, vcc
	v_add_co_u32_e32 v118, vcc, s3, v122
	global_load_dwordx4 v[114:117], v[114:115], off
	s_nop 0
	v_addc_co_u32_e32 v119, vcc, 0, v123, vcc
	v_add_co_u32_e32 v122, vcc, s13, v122
	global_load_dwordx4 v[118:121], v[118:119], off
	s_nop 0
	v_addc_co_u32_e32 v123, vcc, 0, v123, vcc
	global_load_dwordx4 v[122:125], v[122:123], off
	s_nop 0
	global_load_dwordx4 v[126:129], v2, s[38:39]
	v_lshlrev_b32_e32 v2, 4, v68
	s_waitcnt vmcnt(0)
	v_pk_add_f32 v[128:129], v[128:129], 0 op_sel_hi:[1,0]
	v_pk_add_f32 v[126:127], v[126:127], 0 op_sel_hi:[1,0]
	v_pk_add_f32 v[116:117], v[116:117], v[128:129]
	v_pk_add_f32 v[114:115], v[114:115], v[126:127]
	v_pk_add_f32 v[116:117], v[120:121], v[116:117]
	v_pk_add_f32 v[114:115], v[118:119], v[114:115]
	v_pk_add_f32 v[118:119], v[124:125], v[116:117]
	v_pk_add_f32 v[120:121], v[122:123], v[114:115]
	v_lshl_add_u64 v[122:123], s[38:39], 0, v[2:3]
	s_waitcnt vmcnt(0)
	v_pk_fma_f32 v[106:107], v[244:245], v[120:121], v[106:107]
	v_add_co_u32_e32 v114, vcc, s9, v122
	v_pk_fma_f32 v[108:109], v[246:247], v[118:119], v[108:109]
	s_nop 0
	v_addc_co_u32_e32 v115, vcc, 0, v123, vcc
	v_add_co_u32_e32 v118, vcc, s3, v122
	global_load_dwordx4 v[114:117], v[114:115], off
	s_nop 0
	v_addc_co_u32_e32 v119, vcc, 0, v123, vcc
	v_add_co_u32_e32 v122, vcc, s13, v122
	global_load_dwordx4 v[118:121], v[118:119], off
	s_nop 0
	v_addc_co_u32_e32 v123, vcc, 0, v123, vcc
	global_load_dwordx4 v[122:125], v[122:123], off
	s_nop 0
	global_load_dwordx4 v[126:129], v2, s[38:39]
	s_waitcnt vmcnt(0)
	v_pk_add_f32 v[128:129], v[128:129], 0 op_sel_hi:[1,0]
	v_pk_add_f32 v[126:127], v[126:127], 0 op_sel_hi:[1,0]
	v_pk_add_f32 v[116:117], v[116:117], v[128:129]
	v_pk_add_f32 v[114:115], v[114:115], v[126:127]
	v_pk_add_f32 v[116:117], v[120:121], v[116:117]
	v_pk_add_f32 v[114:115], v[118:119], v[114:115]
	v_pk_add_f32 v[118:119], v[124:125], v[116:117]
	v_pk_add_f32 v[120:121], v[122:123], v[114:115]
	s_waitcnt vmcnt(0)
	v_pk_fma_f32 v[98:99], v[250:251], v[118:119], v[98:99]
	v_cvt_pk_bf16_f32 v116, v112, v113
	v_cvt_pk_bf16_f32 v117, v110, v111
	v_pk_fma_f32 v[100:101], v[248:249], v[120:121], v[100:101]
	global_store_dwordx2 v[102:103], v[116:117], off offset:512
	v_lshlrev_b32_e32 v112, 16, v116
	v_and_b32_e32 v113, 0xffff0000, v116
	v_lshlrev_b32_e32 v110, 16, v117
	v_and_b32_e32 v111, 0xffff0000, v117
	v_cvt_pk_bf16_f32 v116, v106, v107
	v_cvt_pk_bf16_f32 v117, v108, v109
	global_store_dwordx2 v[102:103], v[116:117], off offset:1024
	v_lshlrev_b32_e32 v106, 16, v116
	v_and_b32_e32 v107, 0xffff0000, v116
	v_lshlrev_b32_e32 v108, 16, v117
	v_and_b32_e32 v109, 0xffff0000, v117
	v_cvt_pk_bf16_f32 v116, v100, v101
	v_cvt_pk_bf16_f32 v117, v98, v99
	global_store_dwordx2 v[102:103], v[104:105], off
	v_lshlrev_b32_e32 v114, 16, v104
	v_and_b32_e32 v115, 0xffff0000, v104
	v_lshlrev_b32_e32 v104, 16, v105
	v_and_b32_e32 v105, 0xffff0000, v105
	v_lshlrev_b32_e32 v100, 16, v116
	v_and_b32_e32 v101, 0xffff0000, v116
	v_lshlrev_b32_e32 v98, 16, v117
	v_and_b32_e32 v99, 0xffff0000, v117
	global_store_dwordx2 v[102:103], v[116:117], off offset:1536

.LBB0_971:
	s_min_i32 s3, s20, 0x4000
	s_and_b32 s3, s3, 0xfffff000
	s_add_i32 s3, s3, 0
	s_add_i32 s9, s3, 0xa000
	v_add_u32_e32 v1, s3, v54
	v_add_u32_e32 v2, s9, v54
	ds_read_b128 v[44:47], v1 offset:45056
	ds_read_b128 v[36:39], v1 offset:46080
	ds_read_b128 v[48:51], v2 offset:24576
	ds_read_b128 v[40:43], v2 offset:25600
	ds_read_b128 v[28:31], v1 offset:47104
	ds_read_b128 v[20:23], v1 offset:48128
	ds_read_b128 v[32:35], v2 offset:26624
	ds_read_b128 v[24:27], v2 offset:27648
	v_lshlrev_b32_e32 v106, 16, v96
	v_and_b32_e32 v107, 0xffff0000, v96
	v_lshlrev_b32_e32 v96, 16, v97
	v_and_b32_e32 v97, 0xffff0000, v97
	v_lshlrev_b32_e32 v104, 16, v94
	v_and_b32_e32 v105, 0xffff0000, v94
	v_lshlrev_b32_e32 v102, 16, v95
	v_and_b32_e32 v103, 0xffff0000, v95
	v_lshlrev_b32_e32 v98, 16, v92
	v_and_b32_e32 v99, 0xffff0000, v92
	v_lshlrev_b32_e32 v100, 16, v93
	v_and_b32_e32 v101, 0xffff0000, v93
	v_lshlrev_b32_e32 v92, 16, v90
	v_and_b32_e32 v93, 0xffff0000, v90
	v_lshlrev_b32_e32 v90, 16, v91
	s_cmpk_lt_i32 s20, 0x4000
	v_and_b32_e32 v91, 0xffff0000, v91
	s_cbranch_scc1 .LBB0_973
	global_load_dwordx4 v[236:239], v[58:59], off
	global_load_dwordx4 v[240:243], v[62:63], off
	global_load_dwordx4 v[244:247], v[66:67], off
	global_load_dwordx4 v[248:251], v[70:71], off
	v_readlane_b32 s3, v255, 12
	s_mov_b32 s21, s81
	s_add_i32 s22, s3, s2
	s_mov_b32 s23, s81
	s_lshl_b64 s[10:11], s[20:21], 11
	s_lshl_b64 s[22:23], s[22:23], 2
	s_add_u32 s3, s0, s22
	s_addc_u32 s9, s1, s23
	s_add_u32 s22, s3, 0x420f8000
	s_addc_u32 s23, s9, 0
	v_lshlrev_b32_e32 v2, 4, v0
	v_lshl_add_u64 v[94:95], s[22:23], 0, v[2:3]
	s_mov_b32 s9, 0x400000
	v_add_co_u32_e32 v108, vcc, s9, v94
	s_mov_b32 s3, 0x800000
	s_nop 0
	v_addc_co_u32_e32 v109, vcc, 0, v95, vcc
	v_add_co_u32_e32 v112, vcc, s3, v94
	s_mov_b32 s13, 0xc00000
	s_nop 0
	v_addc_co_u32_e32 v113, vcc, 0, v95, vcc
	v_add_co_u32_e32 v94, vcc, s13, v94
	global_load_dwordx4 v[108:111], v[108:109], off
	s_nop 0
	v_addc_co_u32_e32 v95, vcc, 0, v95, vcc
	global_load_dwordx4 v[112:115], v[112:113], off
	s_nop 0
	global_load_dwordx4 v[116:119], v[94:95], off
	global_load_dwordx4 v[120:123], v2, s[22:23]
	v_lshlrev_b32_e32 v2, 4, v60
	s_waitcnt vmcnt(0)
	v_pk_add_f32 v[120:121], v[120:121], 0 op_sel_hi:[1,0]
	s_nop 0
	v_pk_add_f32 v[108:109], v[108:109], v[120:121]
	v_pk_add_f32 v[94:95], v[122:123], 0 op_sel_hi:[1,0]
	v_pk_add_f32 v[108:109], v[112:113], v[108:109]
	v_pk_add_f32 v[94:95], v[110:111], v[94:95]
	v_pk_add_f32 v[112:113], v[116:117], v[108:109]
	v_pk_add_f32 v[94:95], v[114:115], v[94:95]
	v_lshl_add_u64 v[114:115], s[22:23], 0, v[2:3]
	v_pk_add_f32 v[94:95], v[118:119], v[94:95]
	s_waitcnt vmcnt(0)
	v_pk_fma_f32 v[94:95], v[238:239], v[94:95], v[96:97]
	v_pk_fma_f32 v[96:97], v[236:237], v[112:113], v[106:107]
	v_add_co_u32_e32 v106, vcc, s9, v114
	v_cvt_pk_bf16_f32 v96, v96, v97
	s_nop 0
	v_addc_co_u32_e32 v107, vcc, 0, v115, vcc
	v_add_co_u32_e32 v110, vcc, s3, v114
	global_load_dwordx4 v[106:109], v[106:107], off
	s_nop 0
	v_addc_co_u32_e32 v111, vcc, 0, v115, vcc
	v_add_co_u32_e32 v114, vcc, s13, v114
	global_load_dwordx4 v[110:113], v[110:111], off
	s_nop 0
	v_addc_co_u32_e32 v115, vcc, 0, v115, vcc
	global_load_dwordx4 v[114:117], v[114:115], off
	s_nop 0
	global_load_dwordx4 v[118:121], v2, s[22:23]
	v_lshlrev_b32_e32 v2, 4, v64
	v_cvt_pk_bf16_f32 v97, v94, v95
	v_lshl_add_u64 v[94:95], v[52:53], 0, s[10:11]
	s_waitcnt vmcnt(0)
	v_pk_add_f32 v[120:121], v[120:121], 0 op_sel_hi:[1,0]
	v_pk_add_f32 v[118:119], v[118:119], 0 op_sel_hi:[1,0]
	v_pk_add_f32 v[108:109], v[108:109], v[120:121]
	v_pk_add_f32 v[106:107], v[106:107], v[118:119]
	v_pk_add_f32 v[108:109], v[112:113], v[108:109]
	v_pk_add_f32 v[106:107], v[110:111], v[106:107]
	v_pk_add_f32 v[110:111], v[116:117], v[108:109]
	v_pk_add_f32 v[112:113], v[114:115], v[106:107]
	v_lshl_add_u64 v[114:115], s[22:23], 0, v[2:3]
	s_waitcnt vmcnt(0)
	v_pk_fma_f32 v[104:105], v[240:241], v[112:113], v[104:105]
	v_add_co_u32_e32 v106, vcc, s9, v114
	v_pk_fma_f32 v[102:103], v[242:243], v[110:111], v[102:103]
	s_nop 0
	v_addc_co_u32_e32 v107, vcc, 0, v115, vcc
	v_add_co_u32_e32 v110, vcc, s3, v114
	global_load_dwordx4 v[106:109], v[106:107], off
	s_nop 0
	v_addc_co_u32_e32 v111, vcc, 0, v115, vcc
	v_add_co_u32_e32 v114, vcc, s13, v114
	global_load_dwordx4 v[110:113], v[110:111], off
	s_nop 0
	v_addc_co_u32_e32 v115, vcc, 0, v115, vcc
	global_load_dwordx4 v[114:117], v[114:115], off
	s_nop 0
	global_load_dwordx4 v[118:121], v2, s[22:23]
	v_lshlrev_b32_e32 v2, 4, v68
	s_waitcnt vmcnt(0)
	v_pk_add_f32 v[120:121], v[120:121], 0 op_sel_hi:[1,0]
	v_pk_add_f32 v[118:119], v[118:119], 0 op_sel_hi:[1,0]
	v_pk_add_f32 v[108:109], v[108:109], v[120:121]
	v_pk_add_f32 v[106:107], v[106:107], v[118:119]
	v_pk_add_f32 v[108:109], v[112:113], v[108:109]
	v_pk_add_f32 v[106:107], v[110:111], v[106:107]
	v_pk_add_f32 v[110:111], v[116:117], v[108:109]
	v_pk_add_f32 v[112:113], v[114:115], v[106:107]
	v_lshl_add_u64 v[114:115], s[22:23], 0, v[2:3]
	s_waitcnt vmcnt(0)
	v_pk_fma_f32 v[98:99], v[244:245], v[112:113], v[98:99]
	v_add_co_u32_e32 v106, vcc, s9, v114
	v_pk_fma_f32 v[100:101], v[246:247], v[110:111], v[100:101]
	s_nop 0
	v_addc_co_u32_e32 v107, vcc, 0, v115, vcc
	v_add_co_u32_e32 v110, vcc, s3, v114
	global_load_dwordx4 v[106:109], v[106:107], off
	s_nop 0
	v_addc_co_u32_e32 v111, vcc, 0, v115, vcc
	v_add_co_u32_e32 v114, vcc, s13, v114
	global_load_dwordx4 v[110:113], v[110:111], off
	s_nop 0
	v_addc_co_u32_e32 v115, vcc, 0, v115, vcc
	global_load_dwordx4 v[114:117], v[114:115], off
	s_nop 0
	global_load_dwordx4 v[118:121], v2, s[22:23]
	s_waitcnt vmcnt(0)
	v_pk_add_f32 v[120:121], v[120:121], 0 op_sel_hi:[1,0]
	v_pk_add_f32 v[118:119], v[118:119], 0 op_sel_hi:[1,0]
	v_pk_add_f32 v[108:109], v[108:109], v[120:121]
	v_pk_add_f32 v[106:107], v[106:107], v[118:119]
	v_pk_add_f32 v[108:109], v[112:113], v[108:109]
	v_pk_add_f32 v[106:107], v[110:111], v[106:107]
	v_pk_add_f32 v[110:111], v[116:117], v[108:109]
	v_pk_add_f32 v[112:113], v[114:115], v[106:107]
	s_waitcnt vmcnt(0)
	v_pk_fma_f32 v[90:91], v[250:251], v[110:111], v[90:91]
	v_cvt_pk_bf16_f32 v108, v104, v105
	v_cvt_pk_bf16_f32 v109, v102, v103
	v_pk_fma_f32 v[92:93], v[248:249], v[112:113], v[92:93]
	global_store_dwordx2 v[94:95], v[108:109], off offset:512
	v_lshlrev_b32_e32 v104, 16, v108
	v_and_b32_e32 v105, 0xffff0000, v108
	v_lshlrev_b32_e32 v102, 16, v109
	v_and_b32_e32 v103, 0xffff0000, v109
	v_cvt_pk_bf16_f32 v108, v98, v99
	v_cvt_pk_bf16_f32 v109, v100, v101
	global_store_dwordx2 v[94:95], v[108:109], off offset:1024
	v_lshlrev_b32_e32 v98, 16, v108
	v_and_b32_e32 v99, 0xffff0000, v108
	v_lshlrev_b32_e32 v100, 16, v109
	v_and_b32_e32 v101, 0xffff0000, v109
	v_cvt_pk_bf16_f32 v108, v92, v93
	v_cvt_pk_bf16_f32 v109, v90, v91
	global_store_dwordx2 v[94:95], v[96:97], off
	v_lshlrev_b32_e32 v106, 16, v96
	v_and_b32_e32 v107, 0xffff0000, v96
	v_lshlrev_b32_e32 v96, 16, v97
	v_and_b32_e32 v97, 0xffff0000, v97
	v_lshlrev_b32_e32 v92, 16, v108
	v_and_b32_e32 v93, 0xffff0000, v108
	v_lshlrev_b32_e32 v90, 16, v109
	v_and_b32_e32 v91, 0xffff0000, v109
	global_store_dwordx2 v[94:95], v[108:109], off offset:1536

.LBB0_974:
	s_min_i32 s3, s12, 0x4000
	s_and_b32 s3, s3, 0xfffff000
	s_add_i32 s3, s3, 0
	s_add_i32 s9, s3, 0xa000
	v_add_u32_e32 v1, s3, v54
	v_add_u32_e32 v2, s9, v54
	ds_read_b128 v[44:47], v1 offset:45056
	ds_read_b128 v[36:39], v1 offset:46080
	ds_read_b128 v[48:51], v2 offset:24576
	ds_read_b128 v[40:43], v2 offset:25600
	ds_read_b128 v[28:31], v1 offset:47104
	ds_read_b128 v[20:23], v1 offset:48128
	ds_read_b128 v[32:35], v2 offset:26624
	ds_read_b128 v[24:27], v2 offset:27648
	s_waitcnt vmcnt(11)
	v_lshlrev_b32_e32 v98, 16, v88
	v_and_b32_e32 v99, 0xffff0000, v88
	v_lshlrev_b32_e32 v88, 16, v89
	v_and_b32_e32 v89, 0xffff0000, v89
	s_waitcnt vmcnt(10)
	v_lshlrev_b32_e32 v96, 16, v86
	v_and_b32_e32 v97, 0xffff0000, v86
	v_lshlrev_b32_e32 v94, 16, v87
	v_and_b32_e32 v95, 0xffff0000, v87
	s_waitcnt vmcnt(9)
	v_lshlrev_b32_e32 v90, 16, v84
	v_and_b32_e32 v91, 0xffff0000, v84
	v_lshlrev_b32_e32 v92, 16, v85
	v_and_b32_e32 v93, 0xffff0000, v85
	s_waitcnt vmcnt(8)
	v_lshlrev_b32_e32 v84, 16, v82
	v_and_b32_e32 v85, 0xffff0000, v82
	v_lshlrev_b32_e32 v82, 16, v83
	s_cmpk_lt_i32 s12, 0x4000
	v_and_b32_e32 v83, 0xffff0000, v83
	s_cbranch_scc1 .LBB0_976
	global_load_dwordx4 v[236:239], v[58:59], off
	global_load_dwordx4 v[240:243], v[62:63], off
	global_load_dwordx4 v[244:247], v[66:67], off
	global_load_dwordx4 v[248:251], v[70:71], off
	v_readlane_b32 s3, v255, 13
	s_mov_b32 s13, s81
	s_add_i32 s18, s3, s2
	s_mov_b32 s19, s81
	s_lshl_b64 s[10:11], s[12:13], 11
	s_lshl_b64 s[18:19], s[18:19], 2
	s_add_u32 s3, s0, s18
	s_addc_u32 s9, s1, s19
	s_add_u32 s18, s3, 0x420f8000
	s_addc_u32 s19, s9, 0
	v_lshlrev_b32_e32 v2, 4, v0
	v_lshl_add_u64 v[86:87], s[18:19], 0, v[2:3]
	s_mov_b32 s9, 0x400000
	v_add_co_u32_e32 v100, vcc, s9, v86
	s_mov_b32 s3, 0x800000
	s_nop 0
	v_addc_co_u32_e32 v101, vcc, 0, v87, vcc
	v_add_co_u32_e32 v104, vcc, s3, v86
	s_mov_b32 s13, 0xc00000
	s_nop 0
	v_addc_co_u32_e32 v105, vcc, 0, v87, vcc
	v_add_co_u32_e32 v86, vcc, s13, v86
	global_load_dwordx4 v[100:103], v[100:101], off
	s_nop 0
	v_addc_co_u32_e32 v87, vcc, 0, v87, vcc
	global_load_dwordx4 v[104:107], v[104:105], off
	s_nop 0
	global_load_dwordx4 v[108:111], v[86:87], off
	global_load_dwordx4 v[112:115], v2, s[18:19]
	v_lshlrev_b32_e32 v2, 4, v60
	s_waitcnt vmcnt(0)
	v_pk_add_f32 v[112:113], v[112:113], 0 op_sel_hi:[1,0]
	s_nop 0
	v_pk_add_f32 v[100:101], v[100:101], v[112:113]
	v_pk_add_f32 v[86:87], v[114:115], 0 op_sel_hi:[1,0]
	v_pk_add_f32 v[100:101], v[104:105], v[100:101]
	v_pk_add_f32 v[86:87], v[102:103], v[86:87]
	v_pk_add_f32 v[104:105], v[108:109], v[100:101]
	v_pk_add_f32 v[86:87], v[106:107], v[86:87]
	v_lshl_add_u64 v[106:107], s[18:19], 0, v[2:3]
	v_pk_add_f32 v[86:87], v[110:111], v[86:87]
	s_waitcnt vmcnt(0)
	v_pk_fma_f32 v[86:87], v[238:239], v[86:87], v[88:89]
	v_pk_fma_f32 v[88:89], v[236:237], v[104:105], v[98:99]
	v_add_co_u32_e32 v98, vcc, s9, v106
	v_cvt_pk_bf16_f32 v88, v88, v89
	s_nop 0
	v_addc_co_u32_e32 v99, vcc, 0, v107, vcc
	v_add_co_u32_e32 v102, vcc, s3, v106
	global_load_dwordx4 v[98:101], v[98:99], off
	s_nop 0
	v_addc_co_u32_e32 v103, vcc, 0, v107, vcc
	v_add_co_u32_e32 v106, vcc, s13, v106
	global_load_dwordx4 v[102:105], v[102:103], off
	s_nop 0
	v_addc_co_u32_e32 v107, vcc, 0, v107, vcc
	global_load_dwordx4 v[106:109], v[106:107], off
	s_nop 0
	global_load_dwordx4 v[110:113], v2, s[18:19]
	v_lshlrev_b32_e32 v2, 4, v64
	v_cvt_pk_bf16_f32 v89, v86, v87
	v_lshl_add_u64 v[86:87], v[52:53], 0, s[10:11]
	s_waitcnt vmcnt(0)
	v_pk_add_f32 v[112:113], v[112:113], 0 op_sel_hi:[1,0]
	v_pk_add_f32 v[110:111], v[110:111], 0 op_sel_hi:[1,0]
	v_pk_add_f32 v[100:101], v[100:101], v[112:113]
	v_pk_add_f32 v[98:99], v[98:99], v[110:111]
	v_pk_add_f32 v[100:101], v[104:105], v[100:101]
	v_pk_add_f32 v[98:99], v[102:103], v[98:99]
	v_pk_add_f32 v[102:103], v[108:109], v[100:101]
	v_pk_add_f32 v[104:105], v[106:107], v[98:99]
	v_lshl_add_u64 v[106:107], s[18:19], 0, v[2:3]
	s_waitcnt vmcnt(0)
	v_pk_fma_f32 v[96:97], v[240:241], v[104:105], v[96:97]
	v_add_co_u32_e32 v98, vcc, s9, v106
	v_pk_fma_f32 v[94:95], v[242:243], v[102:103], v[94:95]
	s_nop 0
	v_addc_co_u32_e32 v99, vcc, 0, v107, vcc
	v_add_co_u32_e32 v102, vcc, s3, v106
	global_load_dwordx4 v[98:101], v[98:99], off
	s_nop 0
	v_addc_co_u32_e32 v103, vcc, 0, v107, vcc
	v_add_co_u32_e32 v106, vcc, s13, v106
	global_load_dwordx4 v[102:105], v[102:103], off
	s_nop 0
	v_addc_co_u32_e32 v107, vcc, 0, v107, vcc
	global_load_dwordx4 v[106:109], v[106:107], off
	s_nop 0
	global_load_dwordx4 v[110:113], v2, s[18:19]
	v_lshlrev_b32_e32 v2, 4, v68
	s_waitcnt vmcnt(0)
	v_pk_add_f32 v[112:113], v[112:113], 0 op_sel_hi:[1,0]
	v_pk_add_f32 v[110:111], v[110:111], 0 op_sel_hi:[1,0]
	v_pk_add_f32 v[100:101], v[100:101], v[112:113]
	v_pk_add_f32 v[98:99], v[98:99], v[110:111]
	v_pk_add_f32 v[100:101], v[104:105], v[100:101]
	v_pk_add_f32 v[98:99], v[102:103], v[98:99]
	v_pk_add_f32 v[102:103], v[108:109], v[100:101]
	v_pk_add_f32 v[104:105], v[106:107], v[98:99]
	v_lshl_add_u64 v[106:107], s[18:19], 0, v[2:3]
	s_waitcnt vmcnt(0)
	v_pk_fma_f32 v[90:91], v[244:245], v[104:105], v[90:91]
	v_add_co_u32_e32 v98, vcc, s9, v106
	v_pk_fma_f32 v[92:93], v[246:247], v[102:103], v[92:93]
	s_nop 0
	v_addc_co_u32_e32 v99, vcc, 0, v107, vcc
	v_add_co_u32_e32 v102, vcc, s3, v106
	global_load_dwordx4 v[98:101], v[98:99], off
	s_nop 0
	v_addc_co_u32_e32 v103, vcc, 0, v107, vcc
	v_add_co_u32_e32 v106, vcc, s13, v106
	global_load_dwordx4 v[102:105], v[102:103], off
	s_nop 0
	v_addc_co_u32_e32 v107, vcc, 0, v107, vcc
	global_load_dwordx4 v[106:109], v[106:107], off
	s_nop 0
	global_load_dwordx4 v[110:113], v2, s[18:19]
	s_waitcnt vmcnt(0)
	v_pk_add_f32 v[112:113], v[112:113], 0 op_sel_hi:[1,0]
	v_pk_add_f32 v[110:111], v[110:111], 0 op_sel_hi:[1,0]
	v_pk_add_f32 v[100:101], v[100:101], v[112:113]
	v_pk_add_f32 v[98:99], v[98:99], v[110:111]
	v_pk_add_f32 v[100:101], v[104:105], v[100:101]
	v_pk_add_f32 v[98:99], v[102:103], v[98:99]
	v_pk_add_f32 v[102:103], v[108:109], v[100:101]
	v_pk_add_f32 v[104:105], v[106:107], v[98:99]
	s_waitcnt vmcnt(0)
	v_pk_fma_f32 v[82:83], v[250:251], v[102:103], v[82:83]
	v_cvt_pk_bf16_f32 v100, v96, v97
	v_cvt_pk_bf16_f32 v101, v94, v95
	v_pk_fma_f32 v[84:85], v[248:249], v[104:105], v[84:85]
	global_store_dwordx2 v[86:87], v[100:101], off offset:512
	v_lshlrev_b32_e32 v96, 16, v100
	v_and_b32_e32 v97, 0xffff0000, v100
	v_lshlrev_b32_e32 v94, 16, v101
	v_and_b32_e32 v95, 0xffff0000, v101
	v_cvt_pk_bf16_f32 v100, v90, v91
	v_cvt_pk_bf16_f32 v101, v92, v93
	global_store_dwordx2 v[86:87], v[100:101], off offset:1024
	v_lshlrev_b32_e32 v90, 16, v100
	v_and_b32_e32 v91, 0xffff0000, v100
	v_lshlrev_b32_e32 v92, 16, v101
	v_and_b32_e32 v93, 0xffff0000, v101
	v_cvt_pk_bf16_f32 v100, v84, v85
	v_cvt_pk_bf16_f32 v101, v82, v83
	global_store_dwordx2 v[86:87], v[88:89], off
	v_lshlrev_b32_e32 v98, 16, v88
	v_and_b32_e32 v99, 0xffff0000, v88
	v_lshlrev_b32_e32 v88, 16, v89
	v_and_b32_e32 v89, 0xffff0000, v89
	v_lshlrev_b32_e32 v84, 16, v100
	v_and_b32_e32 v85, 0xffff0000, v100
	v_lshlrev_b32_e32 v82, 16, v101
	v_and_b32_e32 v83, 0xffff0000, v101
	global_store_dwordx2 v[86:87], v[100:101], off offset:1536

.LBB0_977:
	s_min_i32 s3, s8, 0x4000
	s_and_b32 s3, s3, 0xfffff000
	s_add_i32 s3, s3, 0
	s_add_i32 s9, s3, 0xa000
	v_add_u32_e32 v1, s3, v54
	v_add_u32_e32 v2, s9, v54
	ds_read_b128 v[44:47], v1 offset:45056
	ds_read_b128 v[36:39], v1 offset:46080
	ds_read_b128 v[48:51], v2 offset:24576
	ds_read_b128 v[40:43], v2 offset:25600
	ds_read_b128 v[28:31], v1 offset:47104
	ds_read_b128 v[20:23], v1 offset:48128
	ds_read_b128 v[32:35], v2 offset:26624
	ds_read_b128 v[24:27], v2 offset:27648
	s_waitcnt vmcnt(7)
	v_lshlrev_b32_e32 v90, 16, v80
	v_and_b32_e32 v91, 0xffff0000, v80
	v_lshlrev_b32_e32 v80, 16, v81
	v_and_b32_e32 v81, 0xffff0000, v81
	s_waitcnt vmcnt(6)
	v_lshlrev_b32_e32 v88, 16, v78
	v_and_b32_e32 v89, 0xffff0000, v78
	v_lshlrev_b32_e32 v86, 16, v79
	v_and_b32_e32 v87, 0xffff0000, v79
	s_waitcnt vmcnt(5)
	v_lshlrev_b32_e32 v82, 16, v76
	v_and_b32_e32 v83, 0xffff0000, v76
	v_lshlrev_b32_e32 v84, 16, v77
	v_and_b32_e32 v85, 0xffff0000, v77
	s_waitcnt vmcnt(4)
	v_lshlrev_b32_e32 v76, 16, v74
	v_and_b32_e32 v77, 0xffff0000, v74
	v_lshlrev_b32_e32 v74, 16, v75
	s_cmpk_lt_i32 s8, 0x4000
	v_and_b32_e32 v75, 0xffff0000, v75
	s_cbranch_scc1 .LBB0_959
	global_load_dwordx4 v[236:239], v[58:59], off
	global_load_dwordx4 v[240:243], v[62:63], off
	global_load_dwordx4 v[244:247], v[66:67], off
	global_load_dwordx4 v[248:251], v[70:71], off
	v_readlane_b32 s3, v255, 14
	s_mov_b32 s9, s81
	s_add_i32 s12, s3, s2
	s_mov_b32 s13, s81
	s_lshl_b64 s[10:11], s[8:9], 11
	s_lshl_b64 s[12:13], s[12:13], 2
	s_add_u32 s3, s0, s12
	s_addc_u32 s9, s1, s13
	s_add_u32 s12, s3, 0x420f8000
	s_addc_u32 s13, s9, 0
	v_lshlrev_b32_e32 v2, 4, v0
	v_lshl_add_u64 v[78:79], s[12:13], 0, v[2:3]
	s_mov_b32 s9, 0x400000
	v_add_co_u32_e32 v92, vcc, s9, v78
	s_mov_b32 s3, 0x800000
	s_nop 0
	v_addc_co_u32_e32 v93, vcc, 0, v79, vcc
	v_add_co_u32_e32 v96, vcc, s3, v78
	s_mov_b32 s14, 0xc00000
	s_nop 0
	v_addc_co_u32_e32 v97, vcc, 0, v79, vcc
	v_add_co_u32_e32 v78, vcc, s14, v78
	global_load_dwordx4 v[92:95], v[92:93], off
	s_nop 0
	v_addc_co_u32_e32 v79, vcc, 0, v79, vcc
	global_load_dwordx4 v[96:99], v[96:97], off
	s_nop 0
	global_load_dwordx4 v[100:103], v[78:79], off
	global_load_dwordx4 v[104:107], v2, s[12:13]
	v_lshlrev_b32_e32 v2, 4, v60
	s_waitcnt vmcnt(0)
	v_pk_add_f32 v[104:105], v[104:105], 0 op_sel_hi:[1,0]
	s_nop 0
	v_pk_add_f32 v[92:93], v[92:93], v[104:105]
	v_pk_add_f32 v[78:79], v[106:107], 0 op_sel_hi:[1,0]
	v_pk_add_f32 v[92:93], v[96:97], v[92:93]
	v_pk_add_f32 v[78:79], v[94:95], v[78:79]
	v_pk_add_f32 v[96:97], v[100:101], v[92:93]
	v_pk_add_f32 v[78:79], v[98:99], v[78:79]
	v_lshl_add_u64 v[98:99], s[12:13], 0, v[2:3]
	v_pk_add_f32 v[78:79], v[102:103], v[78:79]
	s_waitcnt vmcnt(0)
	v_pk_fma_f32 v[78:79], v[238:239], v[78:79], v[80:81]
	v_pk_fma_f32 v[80:81], v[236:237], v[96:97], v[90:91]
	v_add_co_u32_e32 v90, vcc, s9, v98
	v_cvt_pk_bf16_f32 v80, v80, v81
	s_nop 0
	v_addc_co_u32_e32 v91, vcc, 0, v99, vcc
	v_add_co_u32_e32 v94, vcc, s3, v98
	global_load_dwordx4 v[90:93], v[90:91], off
	s_nop 0
	v_addc_co_u32_e32 v95, vcc, 0, v99, vcc
	v_add_co_u32_e32 v98, vcc, s14, v98
	global_load_dwordx4 v[94:97], v[94:95], off
	s_nop 0
	v_addc_co_u32_e32 v99, vcc, 0, v99, vcc
	global_load_dwordx4 v[98:101], v[98:99], off
	s_nop 0
	global_load_dwordx4 v[102:105], v2, s[12:13]
	v_lshlrev_b32_e32 v2, 4, v64
	v_cvt_pk_bf16_f32 v81, v78, v79
	v_lshl_add_u64 v[78:79], v[52:53], 0, s[10:11]
	s_waitcnt vmcnt(0)
	v_pk_add_f32 v[104:105], v[104:105], 0 op_sel_hi:[1,0]
	v_pk_add_f32 v[102:103], v[102:103], 0 op_sel_hi:[1,0]
	v_pk_add_f32 v[92:93], v[92:93], v[104:105]
	v_pk_add_f32 v[90:91], v[90:91], v[102:103]
	v_pk_add_f32 v[92:93], v[96:97], v[92:93]
	v_pk_add_f32 v[90:91], v[94:95], v[90:91]
	v_pk_add_f32 v[94:95], v[100:101], v[92:93]
	v_pk_add_f32 v[96:97], v[98:99], v[90:91]
	v_lshl_add_u64 v[98:99], s[12:13], 0, v[2:3]
	s_waitcnt vmcnt(0)
	v_pk_fma_f32 v[88:89], v[240:241], v[96:97], v[88:89]
	v_add_co_u32_e32 v90, vcc, s9, v98
	v_pk_fma_f32 v[86:87], v[242:243], v[94:95], v[86:87]
	s_nop 0
	v_addc_co_u32_e32 v91, vcc, 0, v99, vcc
	v_add_co_u32_e32 v94, vcc, s3, v98
	global_load_dwordx4 v[90:93], v[90:91], off
	s_nop 0
	v_addc_co_u32_e32 v95, vcc, 0, v99, vcc
	v_add_co_u32_e32 v98, vcc, s14, v98
	global_load_dwordx4 v[94:97], v[94:95], off
	s_nop 0
	v_addc_co_u32_e32 v99, vcc, 0, v99, vcc
	global_load_dwordx4 v[98:101], v[98:99], off
	s_nop 0
	global_load_dwordx4 v[102:105], v2, s[12:13]
	v_lshlrev_b32_e32 v2, 4, v68
	s_waitcnt vmcnt(0)
	v_pk_add_f32 v[104:105], v[104:105], 0 op_sel_hi:[1,0]
	v_pk_add_f32 v[102:103], v[102:103], 0 op_sel_hi:[1,0]
	v_pk_add_f32 v[92:93], v[92:93], v[104:105]
	v_pk_add_f32 v[90:91], v[90:91], v[102:103]
	v_pk_add_f32 v[92:93], v[96:97], v[92:93]
	v_pk_add_f32 v[90:91], v[94:95], v[90:91]
	v_pk_add_f32 v[94:95], v[100:101], v[92:93]
	v_pk_add_f32 v[96:97], v[98:99], v[90:91]
	v_lshl_add_u64 v[98:99], s[12:13], 0, v[2:3]
	s_waitcnt vmcnt(0)
	v_pk_fma_f32 v[82:83], v[244:245], v[96:97], v[82:83]
	v_add_co_u32_e32 v90, vcc, s9, v98
	v_pk_fma_f32 v[84:85], v[246:247], v[94:95], v[84:85]
	s_nop 0
	v_addc_co_u32_e32 v91, vcc, 0, v99, vcc
	v_add_co_u32_e32 v94, vcc, s3, v98
	global_load_dwordx4 v[90:93], v[90:91], off
	s_nop 0
	v_addc_co_u32_e32 v95, vcc, 0, v99, vcc
	v_add_co_u32_e32 v98, vcc, s14, v98
	global_load_dwordx4 v[94:97], v[94:95], off
	s_nop 0
	v_addc_co_u32_e32 v99, vcc, 0, v99, vcc
	global_load_dwordx4 v[98:101], v[98:99], off
	s_nop 0
	global_load_dwordx4 v[102:105], v2, s[12:13]
	s_waitcnt vmcnt(0)
	v_pk_add_f32 v[104:105], v[104:105], 0 op_sel_hi:[1,0]
	v_pk_add_f32 v[102:103], v[102:103], 0 op_sel_hi:[1,0]
	v_pk_add_f32 v[92:93], v[92:93], v[104:105]
	v_pk_add_f32 v[90:91], v[90:91], v[102:103]
	v_pk_add_f32 v[92:93], v[96:97], v[92:93]
	v_pk_add_f32 v[90:91], v[94:95], v[90:91]
	v_pk_add_f32 v[94:95], v[100:101], v[92:93]
	v_pk_add_f32 v[96:97], v[98:99], v[90:91]
	s_waitcnt vmcnt(0)
	v_pk_fma_f32 v[74:75], v[250:251], v[94:95], v[74:75]
	v_cvt_pk_bf16_f32 v92, v88, v89
	v_cvt_pk_bf16_f32 v93, v86, v87
	v_pk_fma_f32 v[76:77], v[248:249], v[96:97], v[76:77]
	global_store_dwordx2 v[78:79], v[92:93], off offset:512
	v_lshlrev_b32_e32 v88, 16, v92
	v_and_b32_e32 v89, 0xffff0000, v92
	v_lshlrev_b32_e32 v86, 16, v93
	v_and_b32_e32 v87, 0xffff0000, v93
	v_cvt_pk_bf16_f32 v92, v82, v83
	v_cvt_pk_bf16_f32 v93, v84, v85
	global_store_dwordx2 v[78:79], v[92:93], off offset:1024
	v_lshlrev_b32_e32 v82, 16, v92
	v_and_b32_e32 v83, 0xffff0000, v92
	v_lshlrev_b32_e32 v84, 16, v93
	v_and_b32_e32 v85, 0xffff0000, v93
	v_cvt_pk_bf16_f32 v92, v76, v77
	v_cvt_pk_bf16_f32 v93, v74, v75
	global_store_dwordx2 v[78:79], v[80:81], off
	v_lshlrev_b32_e32 v90, 16, v80
	v_and_b32_e32 v91, 0xffff0000, v80
	v_lshlrev_b32_e32 v80, 16, v81
	v_and_b32_e32 v81, 0xffff0000, v81
	v_lshlrev_b32_e32 v76, 16, v92
	v_and_b32_e32 v77, 0xffff0000, v92
	v_lshlrev_b32_e32 v74, 16, v93
	v_and_b32_e32 v75, 0xffff0000, v93
	global_store_dwordx2 v[78:79], v[92:93], off offset:1536
	s_branch .LBB0_959

.LBB0_1247:
	s_add_i32 s8, s88, s80
	s_cmpk_lt_i32 s8, 0x4400
	s_cselect_b64 s[12:13], -1, 0
	s_and_b64 s[2:3], s[12:13], exec
	s_cselect_b32 s2, s8, s80
	s_ashr_i32 s3, s2, 31
	s_lshl_b64 s[2:3], s[2:3], 11
	v_lshl_add_u64 v[20:21], v[56:57], 0, s[2:3]
	v_readlane_b32 s2, v254, 8
	s_add_i32 s50, s2, s80
	s_cmpk_lt_i32 s50, 0x4400
	s_cselect_b64 s[2:3], -1, 0
	s_and_b64 s[10:11], s[2:3], exec
	s_cselect_b32 s10, s50, s80
	s_ashr_i32 s11, s10, 31
	v_readlane_b32 s9, v255, 10
	s_lshl_b64 s[10:11], s[10:11], 11
	s_add_i32 s40, s9, s80
	s_cmpk_lt_i32 s40, 0x4400
	s_cselect_b64 s[46:47], -1, 0
	global_load_dwordx2 v[108:109], v[20:21], off
	global_load_dwordx2 v[106:107], v[20:21], off offset:512
	global_load_dwordx2 v[104:105], v[20:21], off offset:1024
	global_load_dwordx2 v[102:103], v[20:21], off offset:1536
	v_lshl_add_u64 v[20:21], v[56:57], 0, s[10:11]
	s_and_b64 s[10:11], s[46:47], exec
	s_cselect_b32 s10, s40, s80
	s_mov_b32 s9, 0xfbc00000
	global_load_dwordx2 v[100:101], v[20:21], off
	global_load_dwordx2 v[98:99], v[20:21], off offset:512
	global_load_dwordx2 v[96:97], v[20:21], off offset:1024
	global_load_dwordx2 v[94:95], v[20:21], off offset:1536
	s_ashr_i32 s11, s10, 31
	v_add_co_u32_e32 v20, vcc, s9, v76
	s_lshl_b64 s[10:11], s[10:11], 11
	s_nop 0
	v_addc_co_u32_e32 v21, vcc, -1, v77, vcc
	global_load_dwordx2 v[112:113], v[20:21], off
	global_load_dwordx2 v[54:55], v[20:21], off offset:-512
	global_load_dwordx2 v[52:53], v[20:21], off offset:-1024
	global_load_dwordx2 v[110:111], v[20:21], off offset:-1536
	v_lshl_add_u64 v[20:21], v[56:57], 0, s[10:11]
	v_readlane_b32 s10, v255, 18
	s_add_i32 s38, s10, s80
	s_cmpk_lt_i32 s38, 0x4400
	v_readlane_b32 s11, v255, 19
	s_cselect_b64 s[42:43], -1, 0
	s_and_b64 s[10:11], s[42:43], exec
	s_cselect_b32 s10, s38, s80
	s_ashr_i32 s11, s10, 31
	s_lshl_b64 s[10:11], s[10:11], 11
	global_load_dwordx2 v[92:93], v[20:21], off
	global_load_dwordx2 v[90:91], v[20:21], off offset:512
	global_load_dwordx2 v[88:89], v[20:21], off offset:1024
	global_load_dwordx2 v[86:87], v[20:21], off offset:1536
	v_lshl_add_u64 v[20:21], v[56:57], 0, s[10:11]
	global_load_dwordx2 v[84:85], v[20:21], off
	global_load_dwordx2 v[82:83], v[20:21], off offset:512
	global_load_dwordx2 v[80:81], v[20:21], off offset:1024
	global_load_dwordx2 v[78:79], v[20:21], off offset:1536
	s_min_i32 s9, s80, 0x4000
	s_and_b32 s9, s9, 0xfffff000
	s_add_i32 s9, s9, 0
	s_add_i32 s10, s9, 0xa000
	v_add_u32_e32 v1, s9, v58
	v_add_u32_e32 v2, s10, v58
	ds_read_b128 v[44:47], v1 offset:45056
	ds_read_b128 v[36:39], v1 offset:46080
	ds_read_b128 v[48:51], v2 offset:24576
	ds_read_b128 v[40:43], v2 offset:25600
	ds_read_b128 v[28:31], v1 offset:47104
	ds_read_b128 v[20:23], v1 offset:48128
	ds_read_b128 v[32:35], v2 offset:26624
	ds_read_b128 v[24:27], v2 offset:27648
	s_cmpk_lt_i32 s80, 0x4000
	s_waitcnt vmcnt(9)
	v_lshlrev_b32_e32 v120, 16, v52
	s_waitcnt vmcnt(8)
	v_lshlrev_b32_e32 v116, 16, v110
	v_and_b32_e32 v117, 0xffff0000, v110
	v_lshlrev_b32_e32 v114, 16, v111
	v_and_b32_e32 v115, 0xffff0000, v111
	v_and_b32_e32 v121, 0xffff0000, v52
	v_lshlrev_b32_e32 v118, 16, v53
	v_and_b32_e32 v119, 0xffff0000, v53
	v_lshlrev_b32_e32 v52, 16, v54
	v_and_b32_e32 v53, 0xffff0000, v54
	v_lshlrev_b32_e32 v54, 16, v55
	v_and_b32_e32 v55, 0xffff0000, v55
	v_lshlrev_b32_e32 v110, 16, v112
	v_and_b32_e32 v111, 0xffff0000, v112
	v_lshlrev_b32_e32 v112, 16, v113
	v_and_b32_e32 v113, 0xffff0000, v113
	s_cbranch_scc1 .LBB0_1249
	global_load_dwordx4 v[236:239], v[62:63], off
	global_load_dwordx4 v[240:243], v[66:67], off
	global_load_dwordx4 v[244:247], v[70:71], off
	global_load_dwordx4 v[248:251], v[74:75], off
	s_mov_b32 s17, s81
	s_lshl_b64 s[14:15], s[80:81], 11
	s_lshl_b64 s[10:11], s[16:17], 2
	s_add_u32 s9, s0, s10
	s_addc_u32 s11, s1, s11
	s_add_u32 s10, s9, 0x420f8000
	s_addc_u32 s11, s11, 0
	v_lshlrev_b32_e32 v2, 4, v0
	v_lshl_add_u64 v[162:163], s[10:11], 0, v[2:3]
	s_mov_b32 s9, 0x400000
	v_add_co_u32_e32 v126, vcc, s9, v162
	s_mov_b32 s17, 0x800000
	s_nop 0
	v_addc_co_u32_e32 v127, vcc, 0, v163, vcc
	v_add_co_u32_e32 v130, vcc, s17, v162
	s_mov_b32 s18, 0xc00000
	s_nop 0
	v_addc_co_u32_e32 v131, vcc, 0, v163, vcc
	v_mov_b32_e32 v1, v134
	v_add_co_u32_e32 v134, vcc, s18, v162
	s_mov_b32 s19, 0x1000000
	s_nop 0
	v_addc_co_u32_e32 v135, vcc, 0, v163, vcc
	v_add_co_u32_e32 v138, vcc, s19, v162
	s_mov_b32 s20, 0x1400000
	s_nop 0
	v_addc_co_u32_e32 v139, vcc, 0, v163, vcc
	v_add_co_u32_e32 v142, vcc, s20, v162
	s_mov_b32 s21, 0x1800000
	s_nop 0
	v_addc_co_u32_e32 v143, vcc, 0, v163, vcc
	global_load_dwordx4 v[122:125], v2, s[10:11]
	v_add_co_u32_e32 v146, vcc, s21, v162
	global_load_dwordx4 v[126:129], v[126:127], off
	s_nop 0
	v_addc_co_u32_e32 v147, vcc, 0, v163, vcc
	s_mov_b32 s22, 0x1c00000
	global_load_dwordx4 v[130:133], v[130:131], off
	v_add_co_u32_e32 v150, vcc, s22, v162
	global_load_dwordx4 v[134:137], v[134:135], off
	s_nop 0
	v_addc_co_u32_e32 v151, vcc, 0, v163, vcc
	s_brev_b32 s23, 64
	global_load_dwordx4 v[138:141], v[138:139], off
	v_add_co_u32_e32 v154, vcc, s23, v162
	global_load_dwordx4 v[142:145], v[142:143], off
	s_nop 0
	v_addc_co_u32_e32 v155, vcc, 0, v163, vcc
	s_mov_b32 s24, 0x2400000
	global_load_dwordx4 v[146:149], v[146:147], off
	v_add_co_u32_e32 v158, vcc, s24, v162
	global_load_dwordx4 v[150:153], v[150:151], off
	s_nop 0
	v_addc_co_u32_e32 v159, vcc, 0, v163, vcc
	s_mov_b32 s25, 0x2800000
	global_load_dwordx4 v[154:157], v[154:155], off
	v_add_co_u32_e32 v162, vcc, s25, v162
	global_load_dwordx4 v[158:161], v[158:159], off
	s_nop 0
	v_addc_co_u32_e32 v163, vcc, 0, v163, vcc
	global_load_dwordx4 v[162:165], v[162:163], off
	v_lshlrev_b32_e32 v2, 4, v64
	s_waitcnt vmcnt(10)
	v_pk_add_f32 v[124:125], v[124:125], 0 op_sel_hi:[1,0]
	v_pk_add_f32 v[122:123], v[122:123], 0 op_sel_hi:[1,0]
	s_waitcnt vmcnt(9)
	v_pk_add_f32 v[124:125], v[124:125], v[128:129]
	v_pk_add_f32 v[122:123], v[122:123], v[126:127]
	s_waitcnt vmcnt(8)
	v_pk_add_f32 v[124:125], v[124:125], v[132:133]
	v_pk_add_f32 v[122:123], v[122:123], v[130:131]
	s_waitcnt vmcnt(7)
	v_pk_add_f32 v[124:125], v[124:125], v[136:137]
	v_pk_add_f32 v[122:123], v[122:123], v[134:135]
	s_waitcnt vmcnt(6)
	v_pk_add_f32 v[124:125], v[124:125], v[140:141]
	v_pk_add_f32 v[122:123], v[122:123], v[138:139]
	s_waitcnt vmcnt(5)
	v_pk_add_f32 v[124:125], v[124:125], v[144:145]
	v_pk_add_f32 v[122:123], v[122:123], v[142:143]
	s_waitcnt vmcnt(4)
	v_pk_add_f32 v[124:125], v[124:125], v[148:149]
	v_pk_add_f32 v[122:123], v[122:123], v[146:147]
	s_waitcnt vmcnt(3)
	v_pk_add_f32 v[124:125], v[124:125], v[152:153]
	v_pk_add_f32 v[122:123], v[122:123], v[150:151]
	s_waitcnt vmcnt(2)
	v_pk_add_f32 v[124:125], v[124:125], v[156:157]
	v_pk_add_f32 v[122:123], v[122:123], v[154:155]
	s_waitcnt vmcnt(1)
	v_pk_add_f32 v[124:125], v[124:125], v[160:161]
	v_pk_add_f32 v[122:123], v[122:123], v[158:159]
	s_waitcnt vmcnt(0)
	v_pk_add_f32 v[126:127], v[124:125], v[164:165]
	v_pk_add_f32 v[128:129], v[122:123], v[162:163]
	v_lshl_add_u64 v[162:163], s[10:11], 0, v[2:3]
	s_waitcnt vmcnt(0)
	v_pk_fma_f32 v[114:115], v[126:127], v[238:239], v[114:115]
	v_add_co_u32_e32 v126, vcc, s9, v162
	v_pk_fma_f32 v[116:117], v[128:129], v[236:237], v[116:117]
	s_nop 0
	v_addc_co_u32_e32 v127, vcc, 0, v163, vcc
	v_add_co_u32_e32 v130, vcc, s17, v162
	global_load_dwordx4 v[122:125], v2, s[10:11]
	s_nop 0
	v_addc_co_u32_e32 v131, vcc, 0, v163, vcc
	v_add_co_u32_e32 v134, vcc, s18, v162
	global_load_dwordx4 v[126:129], v[126:127], off
	s_nop 0
	v_addc_co_u32_e32 v135, vcc, 0, v163, vcc
	v_add_co_u32_e32 v138, vcc, s19, v162
	global_load_dwordx4 v[130:133], v[130:131], off
	s_nop 0
	v_addc_co_u32_e32 v139, vcc, 0, v163, vcc
	v_add_co_u32_e32 v142, vcc, s20, v162
	global_load_dwordx4 v[134:137], v[134:135], off
	s_nop 0
	v_addc_co_u32_e32 v143, vcc, 0, v163, vcc
	v_add_co_u32_e32 v146, vcc, s21, v162
	global_load_dwordx4 v[138:141], v[138:139], off
	s_nop 0
	v_addc_co_u32_e32 v147, vcc, 0, v163, vcc
	v_add_co_u32_e32 v150, vcc, s22, v162
	global_load_dwordx4 v[142:145], v[142:143], off
	s_nop 0
	v_addc_co_u32_e32 v151, vcc, 0, v163, vcc
	v_add_co_u32_e32 v154, vcc, s23, v162
	global_load_dwordx4 v[146:149], v[146:147], off
	s_nop 0
	v_addc_co_u32_e32 v155, vcc, 0, v163, vcc
	v_add_co_u32_e32 v158, vcc, s24, v162
	global_load_dwordx4 v[150:153], v[150:151], off
	s_nop 0
	v_addc_co_u32_e32 v159, vcc, 0, v163, vcc
	global_load_dwordx4 v[154:157], v[154:155], off
	v_add_co_u32_e32 v162, vcc, s25, v162
	global_load_dwordx4 v[158:161], v[158:159], off
	s_nop 0
	v_addc_co_u32_e32 v163, vcc, 0, v163, vcc
	global_load_dwordx4 v[162:165], v[162:163], off
	v_lshlrev_b32_e32 v2, 4, v68
	s_waitcnt vmcnt(10)
	v_pk_add_f32 v[124:125], v[124:125], 0 op_sel_hi:[1,0]
	v_pk_add_f32 v[122:123], v[122:123], 0 op_sel_hi:[1,0]
	s_waitcnt vmcnt(9)
	v_pk_add_f32 v[124:125], v[124:125], v[128:129]
	v_pk_add_f32 v[122:123], v[122:123], v[126:127]
	s_waitcnt vmcnt(8)
	v_pk_add_f32 v[124:125], v[124:125], v[132:133]
	v_pk_add_f32 v[122:123], v[122:123], v[130:131]
	s_waitcnt vmcnt(7)
	v_pk_add_f32 v[124:125], v[124:125], v[136:137]
	v_pk_add_f32 v[122:123], v[122:123], v[134:135]
	s_waitcnt vmcnt(6)
	v_pk_add_f32 v[124:125], v[124:125], v[140:141]
	v_pk_add_f32 v[122:123], v[122:123], v[138:139]
	s_waitcnt vmcnt(5)
	v_pk_add_f32 v[124:125], v[124:125], v[144:145]
	v_pk_add_f32 v[122:123], v[122:123], v[142:143]
	s_waitcnt vmcnt(4)
	v_pk_add_f32 v[124:125], v[124:125], v[148:149]
	v_pk_add_f32 v[122:123], v[122:123], v[146:147]
	s_waitcnt vmcnt(3)
	v_pk_add_f32 v[124:125], v[124:125], v[152:153]
	v_pk_add_f32 v[122:123], v[122:123], v[150:151]
	s_waitcnt vmcnt(2)
	v_pk_add_f32 v[124:125], v[124:125], v[156:157]
	v_pk_add_f32 v[122:123], v[122:123], v[154:155]
	s_waitcnt vmcnt(1)
	v_pk_add_f32 v[124:125], v[124:125], v[160:161]
	v_pk_add_f32 v[122:123], v[122:123], v[158:159]
	s_waitcnt vmcnt(0)
	v_pk_add_f32 v[126:127], v[124:125], v[164:165]
	v_pk_add_f32 v[128:129], v[122:123], v[162:163]
	v_lshl_add_u64 v[162:163], s[10:11], 0, v[2:3]
	s_waitcnt vmcnt(0)
	v_pk_fma_f32 v[118:119], v[126:127], v[242:243], v[118:119]
	v_add_co_u32_e32 v126, vcc, s9, v162
	v_pk_fma_f32 v[120:121], v[128:129], v[240:241], v[120:121]
	s_nop 0
	v_addc_co_u32_e32 v127, vcc, 0, v163, vcc
	v_add_co_u32_e32 v130, vcc, s17, v162
	global_load_dwordx4 v[122:125], v2, s[10:11]
	s_nop 0
	v_addc_co_u32_e32 v131, vcc, 0, v163, vcc
	v_add_co_u32_e32 v134, vcc, s18, v162
	global_load_dwordx4 v[126:129], v[126:127], off
	s_nop 0
	v_addc_co_u32_e32 v135, vcc, 0, v163, vcc
	v_add_co_u32_e32 v138, vcc, s19, v162
	global_load_dwordx4 v[130:133], v[130:131], off
	s_nop 0
	v_addc_co_u32_e32 v139, vcc, 0, v163, vcc
	v_add_co_u32_e32 v142, vcc, s20, v162
	global_load_dwordx4 v[134:137], v[134:135], off
	s_nop 0
	v_addc_co_u32_e32 v143, vcc, 0, v163, vcc
	v_add_co_u32_e32 v146, vcc, s21, v162
	global_load_dwordx4 v[138:141], v[138:139], off
	s_nop 0
	v_addc_co_u32_e32 v147, vcc, 0, v163, vcc
	v_add_co_u32_e32 v150, vcc, s22, v162
	global_load_dwordx4 v[142:145], v[142:143], off
	s_nop 0
	v_addc_co_u32_e32 v151, vcc, 0, v163, vcc
	v_add_co_u32_e32 v154, vcc, s23, v162
	global_load_dwordx4 v[146:149], v[146:147], off
	s_nop 0
	v_addc_co_u32_e32 v155, vcc, 0, v163, vcc
	v_add_co_u32_e32 v158, vcc, s24, v162
	global_load_dwordx4 v[150:153], v[150:151], off
	s_nop 0
	v_addc_co_u32_e32 v159, vcc, 0, v163, vcc
	global_load_dwordx4 v[154:157], v[154:155], off
	v_add_co_u32_e32 v162, vcc, s25, v162
	global_load_dwordx4 v[158:161], v[158:159], off
	s_nop 0
	v_addc_co_u32_e32 v163, vcc, 0, v163, vcc
	global_load_dwordx4 v[162:165], v[162:163], off
	v_lshlrev_b32_e32 v2, 4, v72
	s_waitcnt vmcnt(10)
	v_pk_add_f32 v[124:125], v[124:125], 0 op_sel_hi:[1,0]
	v_pk_add_f32 v[122:123], v[122:123], 0 op_sel_hi:[1,0]
	s_waitcnt vmcnt(9)
	v_pk_add_f32 v[124:125], v[124:125], v[128:129]
	v_pk_add_f32 v[122:123], v[122:123], v[126:127]
	s_waitcnt vmcnt(8)
	v_pk_add_f32 v[124:125], v[124:125], v[132:133]
	v_pk_add_f32 v[122:123], v[122:123], v[130:131]
	s_waitcnt vmcnt(7)
	v_pk_add_f32 v[124:125], v[124:125], v[136:137]
	v_pk_add_f32 v[122:123], v[122:123], v[134:135]
	s_waitcnt vmcnt(6)
	v_pk_add_f32 v[124:125], v[124:125], v[140:141]
	v_pk_add_f32 v[122:123], v[122:123], v[138:139]
	s_waitcnt vmcnt(5)
	v_pk_add_f32 v[124:125], v[124:125], v[144:145]
	v_pk_add_f32 v[122:123], v[122:123], v[142:143]
	s_waitcnt vmcnt(4)
	v_pk_add_f32 v[124:125], v[124:125], v[148:149]
	v_pk_add_f32 v[122:123], v[122:123], v[146:147]
	s_waitcnt vmcnt(3)
	v_pk_add_f32 v[124:125], v[124:125], v[152:153]
	v_pk_add_f32 v[122:123], v[122:123], v[150:151]
	s_waitcnt vmcnt(2)
	v_pk_add_f32 v[124:125], v[124:125], v[156:157]
	v_pk_add_f32 v[122:123], v[122:123], v[154:155]
	s_waitcnt vmcnt(1)
	v_pk_add_f32 v[124:125], v[124:125], v[160:161]
	v_pk_add_f32 v[122:123], v[122:123], v[158:159]
	s_waitcnt vmcnt(0)
	v_pk_add_f32 v[128:129], v[124:125], v[164:165]
	v_pk_add_f32 v[130:131], v[122:123], v[162:163]
	s_waitcnt vmcnt(0)
	v_pk_fma_f32 v[122:123], v[128:129], v[246:247], v[54:55]
	v_lshl_add_u64 v[126:127], s[10:11], 0, v[2:3]
	v_add_co_u32_e32 v128, vcc, s9, v126
	v_pk_fma_f32 v[124:125], v[130:131], v[244:245], v[52:53]
	s_nop 0
	v_addc_co_u32_e32 v129, vcc, 0, v127, vcc
	v_add_co_u32_e32 v132, vcc, s17, v126
	global_load_dwordx4 v[52:55], v2, s[10:11]
	s_nop 0
	v_addc_co_u32_e32 v133, vcc, 0, v127, vcc
	v_add_co_u32_e32 v136, vcc, s18, v126
	global_load_dwordx4 v[128:131], v[128:129], off
	s_nop 0
	v_addc_co_u32_e32 v137, vcc, 0, v127, vcc
	v_add_co_u32_e32 v140, vcc, s19, v126
	global_load_dwordx4 v[132:135], v[132:133], off
	s_nop 0
	v_addc_co_u32_e32 v141, vcc, 0, v127, vcc
	v_add_co_u32_e32 v144, vcc, s20, v126
	global_load_dwordx4 v[136:139], v[136:137], off
	s_nop 0
	v_addc_co_u32_e32 v145, vcc, 0, v127, vcc
	v_add_co_u32_e32 v148, vcc, s21, v126
	global_load_dwordx4 v[140:143], v[140:141], off
	s_nop 0
	v_addc_co_u32_e32 v149, vcc, 0, v127, vcc
	v_add_co_u32_e32 v152, vcc, s22, v126
	global_load_dwordx4 v[144:147], v[144:145], off
	s_nop 0
	v_addc_co_u32_e32 v153, vcc, 0, v127, vcc
	v_add_co_u32_e32 v156, vcc, s23, v126
	global_load_dwordx4 v[148:151], v[148:149], off
	s_nop 0
	v_addc_co_u32_e32 v157, vcc, 0, v127, vcc
	v_add_co_u32_e32 v160, vcc, s24, v126
	global_load_dwordx4 v[152:155], v[152:153], off
	s_nop 0
	v_addc_co_u32_e32 v161, vcc, 0, v127, vcc
	global_load_dwordx4 v[156:159], v[156:157], off
	v_add_co_u32_e32 v126, vcc, s25, v126
	global_load_dwordx4 v[160:163], v[160:161], off
	s_nop 0
	v_addc_co_u32_e32 v127, vcc, 0, v127, vcc
	global_load_dwordx4 v[164:167], v[126:127], off
	s_waitcnt vmcnt(10)
	v_pk_add_f32 v[54:55], v[54:55], 0 op_sel_hi:[1,0]
	v_pk_add_f32 v[52:53], v[52:53], 0 op_sel_hi:[1,0]
	s_waitcnt vmcnt(9)
	v_pk_add_f32 v[54:55], v[54:55], v[130:131]
	v_pk_add_f32 v[52:53], v[52:53], v[128:129]
	s_waitcnt vmcnt(8)
	v_pk_add_f32 v[54:55], v[54:55], v[134:135]
	v_pk_add_f32 v[52:53], v[52:53], v[132:133]
	v_mov_b32_e32 v134, v1
	s_waitcnt vmcnt(7)
	v_pk_add_f32 v[54:55], v[54:55], v[138:139]
	v_pk_add_f32 v[52:53], v[52:53], v[136:137]
	s_waitcnt vmcnt(6)
	v_pk_add_f32 v[54:55], v[54:55], v[142:143]
	v_pk_add_f32 v[52:53], v[52:53], v[140:141]
	s_waitcnt vmcnt(5)
	v_pk_add_f32 v[54:55], v[54:55], v[146:147]
	v_pk_add_f32 v[52:53], v[52:53], v[144:145]
	s_waitcnt vmcnt(4)
	v_pk_add_f32 v[54:55], v[54:55], v[150:151]
	v_pk_add_f32 v[52:53], v[52:53], v[148:149]
	s_waitcnt vmcnt(3)
	v_pk_add_f32 v[54:55], v[54:55], v[154:155]
	v_pk_add_f32 v[52:53], v[52:53], v[152:153]
	s_waitcnt vmcnt(2)
	v_pk_add_f32 v[54:55], v[54:55], v[158:159]
	v_pk_add_f32 v[52:53], v[52:53], v[156:157]
	s_waitcnt vmcnt(1)
	v_pk_add_f32 v[54:55], v[54:55], v[162:163]
	v_pk_add_f32 v[52:53], v[52:53], v[160:161]
	s_waitcnt vmcnt(0)
	v_pk_add_f32 v[128:129], v[54:55], v[166:167]
	v_pk_add_f32 v[126:127], v[52:53], v[164:165]
	s_waitcnt vmcnt(0)
	v_pk_fma_f32 v[112:113], v[128:129], v[250:251], v[112:113]
	v_pk_fma_f32 v[110:111], v[126:127], v[248:249], v[110:111]
	v_cvt_pk_bf16_f32 v52, v116, v117
	v_cvt_pk_bf16_f32 v53, v114, v115
	v_lshl_add_u64 v[126:127], v[56:57], 0, s[14:15]
	global_store_dwordx2 v[126:127], v[52:53], off
	v_lshlrev_b32_e32 v116, 16, v52
	v_and_b32_e32 v117, 0xffff0000, v52
	v_lshlrev_b32_e32 v114, 16, v53
	v_and_b32_e32 v115, 0xffff0000, v53
	v_cvt_pk_bf16_f32 v52, v120, v121
	v_cvt_pk_bf16_f32 v53, v118, v119
	v_cvt_pk_bf16_f32 v54, v124, v125
	v_cvt_pk_bf16_f32 v55, v122, v123
	v_cvt_pk_bf16_f32 v122, v110, v111
	v_cvt_pk_bf16_f32 v123, v112, v113
	global_store_dwordx2 v[126:127], v[52:53], off offset:512
	v_lshlrev_b32_e32 v120, 16, v52
	v_and_b32_e32 v121, 0xffff0000, v52
	v_lshlrev_b32_e32 v118, 16, v53
	v_and_b32_e32 v119, 0xffff0000, v53
	global_store_dwordx2 v[126:127], v[54:55], off offset:1024
	v_lshlrev_b32_e32 v52, 16, v54
	v_and_b32_e32 v53, 0xffff0000, v54
	v_lshlrev_b32_e32 v54, 16, v55
	v_and_b32_e32 v55, 0xffff0000, v55
	v_lshlrev_b32_e32 v110, 16, v122
	v_and_b32_e32 v111, 0xffff0000, v122
	v_lshlrev_b32_e32 v112, 16, v123
	v_and_b32_e32 v113, 0xffff0000, v123
	global_store_dwordx2 v[126:127], v[122:123], off offset:1536
	s_branch .LBB0_1250

.LBB0_1254:
	s_min_i32 s9, s8, 0x4000
	s_and_b32 s9, s9, 0xfffff000
	s_add_i32 s9, s9, 0
	s_add_i32 s10, s9, 0xa000
	v_add_u32_e32 v1, s9, v58
	v_add_u32_e32 v2, s10, v58
	ds_read_b128 v[44:47], v1 offset:45056
	ds_read_b128 v[36:39], v1 offset:46080
	ds_read_b128 v[48:51], v2 offset:24576
	ds_read_b128 v[40:43], v2 offset:25600
	ds_read_b128 v[28:31], v1 offset:47104
	ds_read_b128 v[20:23], v1 offset:48128
	ds_read_b128 v[32:35], v2 offset:26624
	ds_read_b128 v[24:27], v2 offset:27648
	v_lshlrev_b32_e32 v118, 16, v108
	v_and_b32_e32 v119, 0xffff0000, v108
	v_lshlrev_b32_e32 v108, 16, v109
	v_and_b32_e32 v109, 0xffff0000, v109
	v_lshlrev_b32_e32 v112, 16, v106
	v_and_b32_e32 v113, 0xffff0000, v106
	v_lshlrev_b32_e32 v110, 16, v107
	v_and_b32_e32 v111, 0xffff0000, v107
	v_lshlrev_b32_e32 v52, 16, v104
	v_and_b32_e32 v53, 0xffff0000, v104
	v_lshlrev_b32_e32 v54, 16, v105
	v_and_b32_e32 v55, 0xffff0000, v105
	v_lshlrev_b32_e32 v104, 16, v102
	v_and_b32_e32 v105, 0xffff0000, v102
	v_lshlrev_b32_e32 v102, 16, v103
	s_cmpk_lt_i32 s8, 0x4000
	v_and_b32_e32 v103, 0xffff0000, v103
	s_cbranch_scc1 .LBB0_1256
	global_load_dwordx4 v[236:239], v[62:63], off
	global_load_dwordx4 v[240:243], v[66:67], off
	global_load_dwordx4 v[244:247], v[70:71], off
	global_load_dwordx4 v[248:251], v[74:75], off
	s_mov_b32 s9, s81
	s_lshl_b64 s[12:13], s[8:9], 11
	v_readlane_b32 s9, v255, 15
	s_add_i32 s10, s9, s16
	s_mov_b32 s11, s81
	s_lshl_b64 s[10:11], s[10:11], 2
	s_add_u32 s9, s0, s10
	s_addc_u32 s11, s1, s11
	s_add_u32 s10, s9, 0x420f8000
	s_addc_u32 s11, s11, 0
	v_lshlrev_b32_e32 v2, 4, v0
	v_lshl_add_u64 v[106:107], s[10:11], 0, v[2:3]
	s_mov_b32 s14, 0x400000
	v_add_co_u32_e32 v120, vcc, s14, v106
	s_mov_b32 s9, 0x800000
	s_nop 0
	v_addc_co_u32_e32 v121, vcc, 0, v107, vcc
	v_add_co_u32_e32 v124, vcc, s9, v106
	s_mov_b32 s15, 0xc00000
	s_nop 0
	v_addc_co_u32_e32 v125, vcc, 0, v107, vcc
	v_add_co_u32_e32 v128, vcc, s15, v106
	s_mov_b32 s17, 0x1000000
	s_nop 0
	v_addc_co_u32_e32 v129, vcc, 0, v107, vcc
	v_add_co_u32_e32 v132, vcc, s17, v106
	s_mov_b32 s18, 0x1400000
	s_nop 0
	v_addc_co_u32_e32 v133, vcc, 0, v107, vcc
	v_add_co_u32_e32 v136, vcc, s18, v106
	s_mov_b32 s19, 0x1800000
	s_nop 0
	v_addc_co_u32_e32 v137, vcc, 0, v107, vcc
	global_load_dwordx4 v[114:117], v2, s[10:11]
	v_add_co_u32_e32 v140, vcc, s19, v106
	global_load_dwordx4 v[120:123], v[120:121], off
	s_nop 0
	v_addc_co_u32_e32 v141, vcc, 0, v107, vcc
	s_mov_b32 s20, 0x1c00000
	global_load_dwordx4 v[124:127], v[124:125], off
	v_add_co_u32_e32 v144, vcc, s20, v106
	global_load_dwordx4 v[128:131], v[128:129], off
	s_nop 0
	v_addc_co_u32_e32 v145, vcc, 0, v107, vcc
	s_brev_b32 s21, 64
	v_mov_b32_e32 v1, v134
	global_load_dwordx4 v[132:135], v[132:133], off
	v_add_co_u32_e32 v148, vcc, s21, v106
	global_load_dwordx4 v[136:139], v[136:137], off
	s_nop 0
	v_addc_co_u32_e32 v149, vcc, 0, v107, vcc
	s_mov_b32 s22, 0x2400000
	global_load_dwordx4 v[140:143], v[140:141], off
	v_add_co_u32_e32 v152, vcc, s22, v106
	global_load_dwordx4 v[144:147], v[144:145], off
	s_nop 0
	v_addc_co_u32_e32 v153, vcc, 0, v107, vcc
	s_mov_b32 s23, 0x2800000
	global_load_dwordx4 v[148:151], v[148:149], off
	v_add_co_u32_e32 v106, vcc, s23, v106
	global_load_dwordx4 v[152:155], v[152:153], off
	s_nop 0
	v_addc_co_u32_e32 v107, vcc, 0, v107, vcc
	global_load_dwordx4 v[156:159], v[106:107], off
	v_lshlrev_b32_e32 v2, 4, v64
	s_waitcnt vmcnt(10)
	v_pk_add_f32 v[114:115], v[114:115], 0 op_sel_hi:[1,0]
	v_pk_add_f32 v[106:107], v[116:117], 0 op_sel_hi:[1,0]
	s_waitcnt vmcnt(9)
	v_pk_add_f32 v[114:115], v[114:115], v[120:121]
	v_pk_add_f32 v[106:107], v[106:107], v[122:123]
	s_waitcnt vmcnt(8)
	v_pk_add_f32 v[114:115], v[114:115], v[124:125]
	v_pk_add_f32 v[106:107], v[106:107], v[126:127]
	s_waitcnt vmcnt(7)
	v_pk_add_f32 v[114:115], v[114:115], v[128:129]
	v_pk_add_f32 v[106:107], v[106:107], v[130:131]
	s_waitcnt vmcnt(6)
	v_pk_add_f32 v[114:115], v[114:115], v[132:133]
	v_pk_add_f32 v[106:107], v[106:107], v[134:135]
	s_waitcnt vmcnt(5)
	v_pk_add_f32 v[114:115], v[114:115], v[136:137]
	v_pk_add_f32 v[106:107], v[106:107], v[138:139]
	s_waitcnt vmcnt(4)
	v_pk_add_f32 v[114:115], v[114:115], v[140:141]
	v_pk_add_f32 v[106:107], v[106:107], v[142:143]
	s_waitcnt vmcnt(3)
	v_pk_add_f32 v[114:115], v[114:115], v[144:145]
	v_pk_add_f32 v[106:107], v[106:107], v[146:147]
	s_waitcnt vmcnt(2)
	v_pk_add_f32 v[114:115], v[114:115], v[148:149]
	v_pk_add_f32 v[106:107], v[106:107], v[150:151]
	s_waitcnt vmcnt(1)
	v_pk_add_f32 v[114:115], v[114:115], v[152:153]
	v_pk_add_f32 v[106:107], v[106:107], v[154:155]
	v_lshl_add_u64 v[154:155], s[10:11], 0, v[2:3]
	s_waitcnt vmcnt(0)
	v_pk_add_f32 v[120:121], v[114:115], v[156:157]
	v_pk_add_f32 v[106:107], v[106:107], v[158:159]
	s_waitcnt vmcnt(0)
	v_pk_fma_f32 v[106:107], v[106:107], v[238:239], v[108:109]
	v_pk_fma_f32 v[108:109], v[120:121], v[236:237], v[118:119]
	v_add_co_u32_e32 v118, vcc, s14, v154
	global_load_dwordx4 v[114:117], v2, s[10:11]
	s_nop 0
	v_addc_co_u32_e32 v119, vcc, 0, v155, vcc
	v_add_co_u32_e32 v122, vcc, s9, v154
	global_load_dwordx4 v[118:121], v[118:119], off
	s_nop 0
	v_addc_co_u32_e32 v123, vcc, 0, v155, vcc
	v_add_co_u32_e32 v126, vcc, s15, v154
	global_load_dwordx4 v[122:125], v[122:123], off
	s_nop 0
	v_addc_co_u32_e32 v127, vcc, 0, v155, vcc
	v_add_co_u32_e32 v130, vcc, s17, v154
	global_load_dwordx4 v[126:129], v[126:127], off
	s_nop 0
	v_addc_co_u32_e32 v131, vcc, 0, v155, vcc
	v_add_co_u32_e32 v134, vcc, s18, v154
	global_load_dwordx4 v[130:133], v[130:131], off
	s_nop 0
	v_addc_co_u32_e32 v135, vcc, 0, v155, vcc
	v_add_co_u32_e32 v138, vcc, s19, v154
	global_load_dwordx4 v[134:137], v[134:135], off
	s_nop 0
	v_addc_co_u32_e32 v139, vcc, 0, v155, vcc
	v_add_co_u32_e32 v142, vcc, s20, v154
	global_load_dwordx4 v[138:141], v[138:139], off
	s_nop 0
	v_addc_co_u32_e32 v143, vcc, 0, v155, vcc
	v_add_co_u32_e32 v146, vcc, s21, v154
	global_load_dwordx4 v[142:145], v[142:143], off
	s_nop 0
	v_addc_co_u32_e32 v147, vcc, 0, v155, vcc
	v_add_co_u32_e32 v150, vcc, s22, v154
	global_load_dwordx4 v[146:149], v[146:147], off
	s_nop 0
	v_addc_co_u32_e32 v151, vcc, 0, v155, vcc
	v_add_co_u32_e32 v154, vcc, s23, v154
	global_load_dwordx4 v[150:153], v[150:151], off
	s_nop 0
	v_addc_co_u32_e32 v155, vcc, 0, v155, vcc
	global_load_dwordx4 v[154:157], v[154:155], off
	v_lshlrev_b32_e32 v2, 4, v68
	s_waitcnt vmcnt(10)
	v_pk_add_f32 v[116:117], v[116:117], 0 op_sel_hi:[1,0]
	v_pk_add_f32 v[114:115], v[114:115], 0 op_sel_hi:[1,0]
	s_waitcnt vmcnt(9)
	v_pk_add_f32 v[116:117], v[116:117], v[120:121]
	v_pk_add_f32 v[114:115], v[114:115], v[118:119]
	s_waitcnt vmcnt(8)
	v_pk_add_f32 v[116:117], v[116:117], v[124:125]
	v_pk_add_f32 v[114:115], v[114:115], v[122:123]
	s_waitcnt vmcnt(7)
	v_pk_add_f32 v[116:117], v[116:117], v[128:129]
	v_pk_add_f32 v[114:115], v[114:115], v[126:127]
	s_waitcnt vmcnt(6)
	v_pk_add_f32 v[116:117], v[116:117], v[132:133]
	v_pk_add_f32 v[114:115], v[114:115], v[130:131]
	s_waitcnt vmcnt(5)
	v_pk_add_f32 v[116:117], v[116:117], v[136:137]
	v_pk_add_f32 v[114:115], v[114:115], v[134:135]
	s_waitcnt vmcnt(4)
	v_pk_add_f32 v[116:117], v[116:117], v[140:141]
	v_pk_add_f32 v[114:115], v[114:115], v[138:139]
	s_waitcnt vmcnt(3)
	v_pk_add_f32 v[116:117], v[116:117], v[144:145]
	v_pk_add_f32 v[114:115], v[114:115], v[142:143]
	s_waitcnt vmcnt(2)
	v_pk_add_f32 v[116:117], v[116:117], v[148:149]
	v_pk_add_f32 v[114:115], v[114:115], v[146:147]
	s_waitcnt vmcnt(1)
	v_pk_add_f32 v[116:117], v[116:117], v[152:153]
	v_pk_add_f32 v[114:115], v[114:115], v[150:151]
	s_waitcnt vmcnt(0)
	v_pk_add_f32 v[118:119], v[116:117], v[156:157]
	v_pk_add_f32 v[120:121], v[114:115], v[154:155]
	v_lshl_add_u64 v[154:155], s[10:11], 0, v[2:3]
	s_waitcnt vmcnt(0)
	v_pk_fma_f32 v[110:111], v[118:119], v[242:243], v[110:111]
	v_add_co_u32_e32 v118, vcc, s14, v154
	v_pk_fma_f32 v[112:113], v[120:121], v[240:241], v[112:113]
	s_nop 0
	v_addc_co_u32_e32 v119, vcc, 0, v155, vcc
	v_add_co_u32_e32 v122, vcc, s9, v154
	global_load_dwordx4 v[114:117], v2, s[10:11]
	s_nop 0
	v_addc_co_u32_e32 v123, vcc, 0, v155, vcc
	v_add_co_u32_e32 v126, vcc, s15, v154
	global_load_dwordx4 v[118:121], v[118:119], off
	s_nop 0
	v_addc_co_u32_e32 v127, vcc, 0, v155, vcc
	v_add_co_u32_e32 v130, vcc, s17, v154
	global_load_dwordx4 v[122:125], v[122:123], off
	s_nop 0
	v_addc_co_u32_e32 v131, vcc, 0, v155, vcc
	v_add_co_u32_e32 v134, vcc, s18, v154
	global_load_dwordx4 v[126:129], v[126:127], off
	s_nop 0
	v_addc_co_u32_e32 v135, vcc, 0, v155, vcc
	v_add_co_u32_e32 v138, vcc, s19, v154
	global_load_dwordx4 v[130:133], v[130:131], off
	s_nop 0
	v_addc_co_u32_e32 v139, vcc, 0, v155, vcc
	v_add_co_u32_e32 v142, vcc, s20, v154
	global_load_dwordx4 v[134:137], v[134:135], off
	s_nop 0
	v_addc_co_u32_e32 v143, vcc, 0, v155, vcc
	v_add_co_u32_e32 v146, vcc, s21, v154
	global_load_dwordx4 v[138:141], v[138:139], off
	s_nop 0
	v_addc_co_u32_e32 v147, vcc, 0, v155, vcc
	v_add_co_u32_e32 v150, vcc, s22, v154
	global_load_dwordx4 v[142:145], v[142:143], off
	s_nop 0
	v_addc_co_u32_e32 v151, vcc, 0, v155, vcc
	global_load_dwordx4 v[146:149], v[146:147], off
	v_add_co_u32_e32 v154, vcc, s23, v154
	global_load_dwordx4 v[150:153], v[150:151], off
	s_nop 0
	v_addc_co_u32_e32 v155, vcc, 0, v155, vcc
	global_load_dwordx4 v[154:157], v[154:155], off
	v_lshlrev_b32_e32 v2, 4, v72
	s_waitcnt vmcnt(10)
	v_pk_add_f32 v[116:117], v[116:117], 0 op_sel_hi:[1,0]
	v_pk_add_f32 v[114:115], v[114:115], 0 op_sel_hi:[1,0]
	s_waitcnt vmcnt(9)
	v_pk_add_f32 v[116:117], v[116:117], v[120:121]
	v_pk_add_f32 v[114:115], v[114:115], v[118:119]
	s_waitcnt vmcnt(8)
	v_pk_add_f32 v[116:117], v[116:117], v[124:125]
	v_pk_add_f32 v[114:115], v[114:115], v[122:123]
	s_waitcnt vmcnt(7)
	v_pk_add_f32 v[116:117], v[116:117], v[128:129]
	v_pk_add_f32 v[114:115], v[114:115], v[126:127]
	s_waitcnt vmcnt(6)
	v_pk_add_f32 v[116:117], v[116:117], v[132:133]
	v_pk_add_f32 v[114:115], v[114:115], v[130:131]
	s_waitcnt vmcnt(5)
	v_pk_add_f32 v[116:117], v[116:117], v[136:137]
	v_pk_add_f32 v[114:115], v[114:115], v[134:135]
	s_waitcnt vmcnt(4)
	v_pk_add_f32 v[116:117], v[116:117], v[140:141]
	v_pk_add_f32 v[114:115], v[114:115], v[138:139]
	s_waitcnt vmcnt(3)
	v_pk_add_f32 v[116:117], v[116:117], v[144:145]
	v_pk_add_f32 v[114:115], v[114:115], v[142:143]
	s_waitcnt vmcnt(2)
	v_pk_add_f32 v[116:117], v[116:117], v[148:149]
	v_pk_add_f32 v[114:115], v[114:115], v[146:147]
	s_waitcnt vmcnt(1)
	v_pk_add_f32 v[116:117], v[116:117], v[152:153]
	v_pk_add_f32 v[114:115], v[114:115], v[150:151]
	s_waitcnt vmcnt(0)
	v_pk_add_f32 v[120:121], v[116:117], v[156:157]
	v_pk_add_f32 v[122:123], v[114:115], v[154:155]
	s_waitcnt vmcnt(0)
	v_pk_fma_f32 v[114:115], v[120:121], v[246:247], v[54:55]
	v_lshl_add_u64 v[118:119], s[10:11], 0, v[2:3]
	v_add_co_u32_e32 v120, vcc, s14, v118
	v_pk_fma_f32 v[116:117], v[122:123], v[244:245], v[52:53]
	s_nop 0
	v_addc_co_u32_e32 v121, vcc, 0, v119, vcc
	v_add_co_u32_e32 v124, vcc, s9, v118
	global_load_dwordx4 v[52:55], v2, s[10:11]
	s_nop 0
	v_addc_co_u32_e32 v125, vcc, 0, v119, vcc
	v_add_co_u32_e32 v128, vcc, s15, v118
	global_load_dwordx4 v[120:123], v[120:121], off
	s_nop 0
	v_addc_co_u32_e32 v129, vcc, 0, v119, vcc
	v_add_co_u32_e32 v132, vcc, s17, v118
	global_load_dwordx4 v[124:127], v[124:125], off
	s_nop 0
	v_addc_co_u32_e32 v133, vcc, 0, v119, vcc
	v_add_co_u32_e32 v136, vcc, s18, v118
	global_load_dwordx4 v[128:131], v[128:129], off
	s_nop 0
	v_addc_co_u32_e32 v137, vcc, 0, v119, vcc
	v_add_co_u32_e32 v140, vcc, s19, v118
	global_load_dwordx4 v[132:135], v[132:133], off
	s_nop 0
	v_addc_co_u32_e32 v141, vcc, 0, v119, vcc
	v_add_co_u32_e32 v144, vcc, s20, v118
	global_load_dwordx4 v[136:139], v[136:137], off
	s_nop 0
	v_addc_co_u32_e32 v145, vcc, 0, v119, vcc
	v_add_co_u32_e32 v148, vcc, s21, v118
	global_load_dwordx4 v[140:143], v[140:141], off
	s_nop 0
	v_addc_co_u32_e32 v149, vcc, 0, v119, vcc
	v_add_co_u32_e32 v152, vcc, s22, v118
	global_load_dwordx4 v[144:147], v[144:145], off
	s_nop 0
	v_addc_co_u32_e32 v153, vcc, 0, v119, vcc
	global_load_dwordx4 v[148:151], v[148:149], off
	v_add_co_u32_e32 v118, vcc, s23, v118
	global_load_dwordx4 v[152:155], v[152:153], off
	s_nop 0
	v_addc_co_u32_e32 v119, vcc, 0, v119, vcc
	global_load_dwordx4 v[156:159], v[118:119], off
	s_waitcnt vmcnt(10)
	v_pk_add_f32 v[54:55], v[54:55], 0 op_sel_hi:[1,0]
	v_pk_add_f32 v[52:53], v[52:53], 0 op_sel_hi:[1,0]
	s_waitcnt vmcnt(9)
	v_pk_add_f32 v[54:55], v[54:55], v[122:123]
	v_pk_add_f32 v[52:53], v[52:53], v[120:121]
	s_waitcnt vmcnt(8)
	v_pk_add_f32 v[54:55], v[54:55], v[126:127]
	v_pk_add_f32 v[52:53], v[52:53], v[124:125]
	s_waitcnt vmcnt(7)
	v_pk_add_f32 v[54:55], v[54:55], v[130:131]
	v_pk_add_f32 v[52:53], v[52:53], v[128:129]
	s_waitcnt vmcnt(6)
	v_pk_add_f32 v[54:55], v[54:55], v[134:135]
	v_pk_add_f32 v[52:53], v[52:53], v[132:133]
	v_mov_b32_e32 v134, v1
	s_waitcnt vmcnt(5)
	v_pk_add_f32 v[54:55], v[54:55], v[138:139]
	v_pk_add_f32 v[52:53], v[52:53], v[136:137]
	s_waitcnt vmcnt(4)
	v_pk_add_f32 v[54:55], v[54:55], v[142:143]
	v_pk_add_f32 v[52:53], v[52:53], v[140:141]
	s_waitcnt vmcnt(3)
	v_pk_add_f32 v[54:55], v[54:55], v[146:147]
	v_pk_add_f32 v[52:53], v[52:53], v[144:145]
	s_waitcnt vmcnt(2)
	v_pk_add_f32 v[54:55], v[54:55], v[150:151]
	v_pk_add_f32 v[52:53], v[52:53], v[148:149]
	s_waitcnt vmcnt(1)
	v_pk_add_f32 v[54:55], v[54:55], v[154:155]
	v_pk_add_f32 v[52:53], v[52:53], v[152:153]
	s_waitcnt vmcnt(0)
	v_pk_add_f32 v[120:121], v[54:55], v[158:159]
	v_pk_add_f32 v[118:119], v[52:53], v[156:157]
	s_waitcnt vmcnt(0)
	v_pk_fma_f32 v[102:103], v[120:121], v[250:251], v[102:103]
	v_pk_fma_f32 v[104:105], v[118:119], v[248:249], v[104:105]
	v_cvt_pk_bf16_f32 v52, v108, v109
	v_cvt_pk_bf16_f32 v53, v106, v107
	v_lshl_add_u64 v[106:107], v[56:57], 0, s[12:13]
	global_store_dwordx2 v[106:107], v[52:53], off
	v_lshlrev_b32_e32 v118, 16, v52
	v_and_b32_e32 v119, 0xffff0000, v52
	v_lshlrev_b32_e32 v108, 16, v53
	v_and_b32_e32 v109, 0xffff0000, v53
	v_cvt_pk_bf16_f32 v52, v112, v113
	v_cvt_pk_bf16_f32 v53, v110, v111
	v_cvt_pk_bf16_f32 v54, v116, v117
	v_cvt_pk_bf16_f32 v55, v114, v115
	v_cvt_pk_bf16_f32 v114, v104, v105
	v_cvt_pk_bf16_f32 v115, v102, v103
	global_store_dwordx2 v[106:107], v[52:53], off offset:512
	v_lshlrev_b32_e32 v112, 16, v52
	v_and_b32_e32 v113, 0xffff0000, v52
	v_lshlrev_b32_e32 v110, 16, v53
	v_and_b32_e32 v111, 0xffff0000, v53
	global_store_dwordx2 v[106:107], v[54:55], off offset:1024
	v_lshlrev_b32_e32 v52, 16, v54
	v_and_b32_e32 v53, 0xffff0000, v54
	v_lshlrev_b32_e32 v54, 16, v55
	v_and_b32_e32 v55, 0xffff0000, v55
	v_lshlrev_b32_e32 v104, 16, v114
	v_and_b32_e32 v105, 0xffff0000, v114
	v_lshlrev_b32_e32 v102, 16, v115
	v_and_b32_e32 v103, 0xffff0000, v115
	global_store_dwordx2 v[106:107], v[114:115], off offset:1536

.LBB0_1257:
	s_min_i32 s2, s50, 0x4000
	s_and_b32 s2, s2, 0xfffff000
	s_add_i32 s2, s2, 0
	s_add_i32 s3, s2, 0xa000
	v_add_u32_e32 v1, s2, v58
	v_add_u32_e32 v2, s3, v58
	ds_read_b128 v[44:47], v1 offset:45056
	ds_read_b128 v[36:39], v1 offset:46080
	ds_read_b128 v[48:51], v2 offset:24576
	ds_read_b128 v[40:43], v2 offset:25600
	ds_read_b128 v[28:31], v1 offset:47104
	ds_read_b128 v[20:23], v1 offset:48128
	ds_read_b128 v[32:35], v2 offset:26624
	ds_read_b128 v[24:27], v2 offset:27648
	v_lshlrev_b32_e32 v110, 16, v100
	v_and_b32_e32 v111, 0xffff0000, v100
	v_lshlrev_b32_e32 v100, 16, v101
	v_and_b32_e32 v101, 0xffff0000, v101
	v_lshlrev_b32_e32 v104, 16, v98
	v_and_b32_e32 v105, 0xffff0000, v98
	v_lshlrev_b32_e32 v102, 16, v99
	v_and_b32_e32 v103, 0xffff0000, v99
	v_lshlrev_b32_e32 v52, 16, v96
	v_and_b32_e32 v53, 0xffff0000, v96
	v_lshlrev_b32_e32 v54, 16, v97
	v_and_b32_e32 v55, 0xffff0000, v97
	v_lshlrev_b32_e32 v96, 16, v94
	v_and_b32_e32 v97, 0xffff0000, v94
	v_lshlrev_b32_e32 v94, 16, v95
	s_cmpk_lt_i32 s50, 0x4000
	v_and_b32_e32 v95, 0xffff0000, v95
	s_cbranch_scc1 .LBB0_1259
	global_load_dwordx4 v[236:239], v[62:63], off
	global_load_dwordx4 v[240:243], v[66:67], off
	global_load_dwordx4 v[244:247], v[70:71], off
	global_load_dwordx4 v[248:251], v[74:75], off
	v_readlane_b32 s8, v255, 12
	s_mov_b32 s51, s81
	s_add_i32 s8, s8, s16
	s_mov_b32 s9, s81
	s_lshl_b64 s[2:3], s[50:51], 11
	s_lshl_b64 s[8:9], s[8:9], 2
	s_add_u32 s8, s0, s8
	s_addc_u32 s9, s1, s9
	s_add_u32 s8, s8, 0x420f8000
	s_addc_u32 s9, s9, 0
	v_lshlrev_b32_e32 v2, 4, v0
	v_lshl_add_u64 v[98:99], s[8:9], 0, v[2:3]
	s_mov_b32 s11, 0x400000
	v_add_co_u32_e32 v112, vcc, s11, v98
	s_mov_b32 s10, 0x800000
	s_nop 0
	v_addc_co_u32_e32 v113, vcc, 0, v99, vcc
	v_add_co_u32_e32 v116, vcc, s10, v98
	s_mov_b32 s12, 0xc00000
	s_nop 0
	v_addc_co_u32_e32 v117, vcc, 0, v99, vcc
	v_add_co_u32_e32 v120, vcc, s12, v98
	s_mov_b32 s13, 0x1000000
	s_nop 0
	v_addc_co_u32_e32 v121, vcc, 0, v99, vcc
	v_add_co_u32_e32 v124, vcc, s13, v98
	s_mov_b32 s14, 0x1400000
	s_nop 0
	v_addc_co_u32_e32 v125, vcc, 0, v99, vcc
	v_add_co_u32_e32 v128, vcc, s14, v98
	s_mov_b32 s15, 0x1800000
	s_nop 0
	v_addc_co_u32_e32 v129, vcc, 0, v99, vcc
	global_load_dwordx4 v[106:109], v2, s[8:9]
	v_add_co_u32_e32 v132, vcc, s15, v98
	global_load_dwordx4 v[112:115], v[112:113], off
	s_nop 0
	v_addc_co_u32_e32 v133, vcc, 0, v99, vcc
	s_mov_b32 s17, 0x1c00000
	global_load_dwordx4 v[116:119], v[116:117], off
	v_add_co_u32_e32 v136, vcc, s17, v98
	global_load_dwordx4 v[120:123], v[120:121], off
	s_nop 0
	v_addc_co_u32_e32 v137, vcc, 0, v99, vcc
	s_brev_b32 s18, 64
	global_load_dwordx4 v[124:127], v[124:125], off
	v_add_co_u32_e32 v140, vcc, s18, v98
	global_load_dwordx4 v[128:131], v[128:129], off
	s_nop 0
	v_addc_co_u32_e32 v141, vcc, 0, v99, vcc
	s_mov_b32 s19, 0x2400000
	v_mov_b32_e32 v1, v134
	global_load_dwordx4 v[132:135], v[132:133], off
	v_add_co_u32_e32 v144, vcc, s19, v98
	global_load_dwordx4 v[136:139], v[136:137], off
	s_nop 0
	v_addc_co_u32_e32 v145, vcc, 0, v99, vcc
	s_mov_b32 s20, 0x2800000
	global_load_dwordx4 v[140:143], v[140:141], off
	v_add_co_u32_e32 v98, vcc, s20, v98
	global_load_dwordx4 v[144:147], v[144:145], off
	s_nop 0
	v_addc_co_u32_e32 v99, vcc, 0, v99, vcc
	global_load_dwordx4 v[148:151], v[98:99], off
	v_lshlrev_b32_e32 v2, 4, v64
	s_waitcnt vmcnt(10)
	v_pk_add_f32 v[106:107], v[106:107], 0 op_sel_hi:[1,0]
	v_pk_add_f32 v[98:99], v[108:109], 0 op_sel_hi:[1,0]
	s_waitcnt vmcnt(9)
	v_pk_add_f32 v[106:107], v[106:107], v[112:113]
	v_pk_add_f32 v[98:99], v[98:99], v[114:115]
	s_waitcnt vmcnt(8)
	v_pk_add_f32 v[106:107], v[106:107], v[116:117]
	v_pk_add_f32 v[98:99], v[98:99], v[118:119]
	s_waitcnt vmcnt(7)
	v_pk_add_f32 v[106:107], v[106:107], v[120:121]
	v_pk_add_f32 v[98:99], v[98:99], v[122:123]
	s_waitcnt vmcnt(6)
	v_pk_add_f32 v[106:107], v[106:107], v[124:125]
	v_pk_add_f32 v[98:99], v[98:99], v[126:127]
	s_waitcnt vmcnt(5)
	v_pk_add_f32 v[106:107], v[106:107], v[128:129]
	v_pk_add_f32 v[98:99], v[98:99], v[130:131]
	s_waitcnt vmcnt(4)
	v_pk_add_f32 v[106:107], v[106:107], v[132:133]
	v_pk_add_f32 v[98:99], v[98:99], v[134:135]
	s_waitcnt vmcnt(3)
	v_pk_add_f32 v[106:107], v[106:107], v[136:137]
	v_pk_add_f32 v[98:99], v[98:99], v[138:139]
	s_waitcnt vmcnt(2)
	v_pk_add_f32 v[106:107], v[106:107], v[140:141]
	v_pk_add_f32 v[98:99], v[98:99], v[142:143]
	s_waitcnt vmcnt(1)
	v_pk_add_f32 v[106:107], v[106:107], v[144:145]
	v_pk_add_f32 v[98:99], v[98:99], v[146:147]
	v_lshl_add_u64 v[146:147], s[8:9], 0, v[2:3]
	s_waitcnt vmcnt(0)
	v_pk_add_f32 v[112:113], v[106:107], v[148:149]
	v_pk_add_f32 v[98:99], v[98:99], v[150:151]
	s_waitcnt vmcnt(0)
	v_pk_fma_f32 v[98:99], v[98:99], v[238:239], v[100:101]
	v_pk_fma_f32 v[100:101], v[112:113], v[236:237], v[110:111]
	v_add_co_u32_e32 v110, vcc, s11, v146
	global_load_dwordx4 v[106:109], v2, s[8:9]
	s_nop 0
	v_addc_co_u32_e32 v111, vcc, 0, v147, vcc
	v_add_co_u32_e32 v114, vcc, s10, v146
	global_load_dwordx4 v[110:113], v[110:111], off
	s_nop 0
	v_addc_co_u32_e32 v115, vcc, 0, v147, vcc
	v_add_co_u32_e32 v118, vcc, s12, v146
	global_load_dwordx4 v[114:117], v[114:115], off
	s_nop 0
	v_addc_co_u32_e32 v119, vcc, 0, v147, vcc
	v_add_co_u32_e32 v122, vcc, s13, v146
	global_load_dwordx4 v[118:121], v[118:119], off
	s_nop 0
	v_addc_co_u32_e32 v123, vcc, 0, v147, vcc
	v_add_co_u32_e32 v126, vcc, s14, v146
	global_load_dwordx4 v[122:125], v[122:123], off
	s_nop 0
	v_addc_co_u32_e32 v127, vcc, 0, v147, vcc
	v_add_co_u32_e32 v130, vcc, s15, v146
	global_load_dwordx4 v[126:129], v[126:127], off
	s_nop 0
	v_addc_co_u32_e32 v131, vcc, 0, v147, vcc
	v_add_co_u32_e32 v134, vcc, s17, v146
	global_load_dwordx4 v[130:133], v[130:131], off
	s_nop 0
	v_addc_co_u32_e32 v135, vcc, 0, v147, vcc
	v_add_co_u32_e32 v138, vcc, s18, v146
	global_load_dwordx4 v[134:137], v[134:135], off
	s_nop 0
	v_addc_co_u32_e32 v139, vcc, 0, v147, vcc
	v_add_co_u32_e32 v142, vcc, s19, v146
	global_load_dwordx4 v[138:141], v[138:139], off
	s_nop 0
	v_addc_co_u32_e32 v143, vcc, 0, v147, vcc
	v_add_co_u32_e32 v146, vcc, s20, v146
	global_load_dwordx4 v[142:145], v[142:143], off
	s_nop 0
	v_addc_co_u32_e32 v147, vcc, 0, v147, vcc
	global_load_dwordx4 v[146:149], v[146:147], off
	v_lshlrev_b32_e32 v2, 4, v68
	s_waitcnt vmcnt(10)
	v_pk_add_f32 v[108:109], v[108:109], 0 op_sel_hi:[1,0]
	v_pk_add_f32 v[106:107], v[106:107], 0 op_sel_hi:[1,0]
	s_waitcnt vmcnt(9)
	v_pk_add_f32 v[108:109], v[108:109], v[112:113]
	v_pk_add_f32 v[106:107], v[106:107], v[110:111]
	s_waitcnt vmcnt(8)
	v_pk_add_f32 v[108:109], v[108:109], v[116:117]
	v_pk_add_f32 v[106:107], v[106:107], v[114:115]
	s_waitcnt vmcnt(7)
	v_pk_add_f32 v[108:109], v[108:109], v[120:121]
	v_pk_add_f32 v[106:107], v[106:107], v[118:119]
	s_waitcnt vmcnt(6)
	v_pk_add_f32 v[108:109], v[108:109], v[124:125]
	v_pk_add_f32 v[106:107], v[106:107], v[122:123]
	s_waitcnt vmcnt(5)
	v_pk_add_f32 v[108:109], v[108:109], v[128:129]
	v_pk_add_f32 v[106:107], v[106:107], v[126:127]
	s_waitcnt vmcnt(4)
	v_pk_add_f32 v[108:109], v[108:109], v[132:133]
	v_pk_add_f32 v[106:107], v[106:107], v[130:131]
	s_waitcnt vmcnt(3)
	v_pk_add_f32 v[108:109], v[108:109], v[136:137]
	v_pk_add_f32 v[106:107], v[106:107], v[134:135]
	s_waitcnt vmcnt(2)
	v_pk_add_f32 v[108:109], v[108:109], v[140:141]
	v_pk_add_f32 v[106:107], v[106:107], v[138:139]
	s_waitcnt vmcnt(1)
	v_pk_add_f32 v[108:109], v[108:109], v[144:145]
	v_pk_add_f32 v[106:107], v[106:107], v[142:143]
	s_waitcnt vmcnt(0)
	v_pk_add_f32 v[110:111], v[108:109], v[148:149]
	v_pk_add_f32 v[112:113], v[106:107], v[146:147]
	v_lshl_add_u64 v[146:147], s[8:9], 0, v[2:3]
	s_waitcnt vmcnt(0)
	v_pk_fma_f32 v[102:103], v[110:111], v[242:243], v[102:103]
	v_add_co_u32_e32 v110, vcc, s11, v146
	v_pk_fma_f32 v[104:105], v[112:113], v[240:241], v[104:105]
	s_nop 0
	v_addc_co_u32_e32 v111, vcc, 0, v147, vcc
	v_add_co_u32_e32 v114, vcc, s10, v146
	global_load_dwordx4 v[106:109], v2, s[8:9]
	s_nop 0
	v_addc_co_u32_e32 v115, vcc, 0, v147, vcc
	v_add_co_u32_e32 v118, vcc, s12, v146
	global_load_dwordx4 v[110:113], v[110:111], off
	s_nop 0
	v_addc_co_u32_e32 v119, vcc, 0, v147, vcc
	v_add_co_u32_e32 v122, vcc, s13, v146
	global_load_dwordx4 v[114:117], v[114:115], off
	s_nop 0
	v_addc_co_u32_e32 v123, vcc, 0, v147, vcc
	v_add_co_u32_e32 v126, vcc, s14, v146
	global_load_dwordx4 v[118:121], v[118:119], off
	s_nop 0
	v_addc_co_u32_e32 v127, vcc, 0, v147, vcc
	v_add_co_u32_e32 v130, vcc, s15, v146
	global_load_dwordx4 v[122:125], v[122:123], off
	s_nop 0
	v_addc_co_u32_e32 v131, vcc, 0, v147, vcc
	v_add_co_u32_e32 v134, vcc, s17, v146
	global_load_dwordx4 v[126:129], v[126:127], off
	s_nop 0
	v_addc_co_u32_e32 v135, vcc, 0, v147, vcc
	v_add_co_u32_e32 v138, vcc, s18, v146
	global_load_dwordx4 v[130:133], v[130:131], off
	s_nop 0
	v_addc_co_u32_e32 v139, vcc, 0, v147, vcc
	v_add_co_u32_e32 v142, vcc, s19, v146
	global_load_dwordx4 v[134:137], v[134:135], off
	s_nop 0
	v_addc_co_u32_e32 v143, vcc, 0, v147, vcc
	global_load_dwordx4 v[138:141], v[138:139], off
	v_add_co_u32_e32 v146, vcc, s20, v146
	global_load_dwordx4 v[142:145], v[142:143], off
	s_nop 0
	v_addc_co_u32_e32 v147, vcc, 0, v147, vcc
	global_load_dwordx4 v[146:149], v[146:147], off
	v_lshlrev_b32_e32 v2, 4, v72
	s_waitcnt vmcnt(10)
	v_pk_add_f32 v[108:109], v[108:109], 0 op_sel_hi:[1,0]
	v_pk_add_f32 v[106:107], v[106:107], 0 op_sel_hi:[1,0]
	s_waitcnt vmcnt(9)
	v_pk_add_f32 v[108:109], v[108:109], v[112:113]
	v_pk_add_f32 v[106:107], v[106:107], v[110:111]
	s_waitcnt vmcnt(8)
	v_pk_add_f32 v[108:109], v[108:109], v[116:117]
	v_pk_add_f32 v[106:107], v[106:107], v[114:115]
	s_waitcnt vmcnt(7)
	v_pk_add_f32 v[108:109], v[108:109], v[120:121]
	v_pk_add_f32 v[106:107], v[106:107], v[118:119]
	s_waitcnt vmcnt(6)
	v_pk_add_f32 v[108:109], v[108:109], v[124:125]
	v_pk_add_f32 v[106:107], v[106:107], v[122:123]
	s_waitcnt vmcnt(5)
	v_pk_add_f32 v[108:109], v[108:109], v[128:129]
	v_pk_add_f32 v[106:107], v[106:107], v[126:127]
	s_waitcnt vmcnt(4)
	v_pk_add_f32 v[108:109], v[108:109], v[132:133]
	v_pk_add_f32 v[106:107], v[106:107], v[130:131]
	s_waitcnt vmcnt(3)
	v_pk_add_f32 v[108:109], v[108:109], v[136:137]
	v_pk_add_f32 v[106:107], v[106:107], v[134:135]
	s_waitcnt vmcnt(2)
	v_pk_add_f32 v[108:109], v[108:109], v[140:141]
	v_pk_add_f32 v[106:107], v[106:107], v[138:139]
	s_waitcnt vmcnt(1)
	v_pk_add_f32 v[108:109], v[108:109], v[144:145]
	v_pk_add_f32 v[106:107], v[106:107], v[142:143]
	s_waitcnt vmcnt(0)
	v_pk_add_f32 v[112:113], v[108:109], v[148:149]
	v_pk_add_f32 v[114:115], v[106:107], v[146:147]
	s_waitcnt vmcnt(0)
	v_pk_fma_f32 v[106:107], v[112:113], v[246:247], v[54:55]
	v_lshl_add_u64 v[110:111], s[8:9], 0, v[2:3]
	v_add_co_u32_e32 v112, vcc, s11, v110
	v_pk_fma_f32 v[108:109], v[114:115], v[244:245], v[52:53]
	s_nop 0
	v_addc_co_u32_e32 v113, vcc, 0, v111, vcc
	v_add_co_u32_e32 v116, vcc, s10, v110
	global_load_dwordx4 v[52:55], v2, s[8:9]
	s_nop 0
	v_addc_co_u32_e32 v117, vcc, 0, v111, vcc
	v_add_co_u32_e32 v120, vcc, s12, v110
	global_load_dwordx4 v[112:115], v[112:113], off
	s_nop 0
	v_addc_co_u32_e32 v121, vcc, 0, v111, vcc
	v_add_co_u32_e32 v124, vcc, s13, v110
	global_load_dwordx4 v[116:119], v[116:117], off
	s_nop 0
	v_addc_co_u32_e32 v125, vcc, 0, v111, vcc
	v_add_co_u32_e32 v128, vcc, s14, v110
	global_load_dwordx4 v[120:123], v[120:121], off
	s_nop 0
	v_addc_co_u32_e32 v129, vcc, 0, v111, vcc
	v_add_co_u32_e32 v132, vcc, s15, v110
	global_load_dwordx4 v[124:127], v[124:125], off
	s_nop 0
	v_addc_co_u32_e32 v133, vcc, 0, v111, vcc
	v_add_co_u32_e32 v136, vcc, s17, v110
	global_load_dwordx4 v[128:131], v[128:129], off
	s_nop 0
	v_addc_co_u32_e32 v137, vcc, 0, v111, vcc
	v_add_co_u32_e32 v140, vcc, s18, v110
	global_load_dwordx4 v[132:135], v[132:133], off
	s_nop 0
	v_addc_co_u32_e32 v141, vcc, 0, v111, vcc
	v_add_co_u32_e32 v144, vcc, s19, v110
	global_load_dwordx4 v[136:139], v[136:137], off
	s_nop 0
	v_addc_co_u32_e32 v145, vcc, 0, v111, vcc
	global_load_dwordx4 v[140:143], v[140:141], off
	v_add_co_u32_e32 v110, vcc, s20, v110
	global_load_dwordx4 v[144:147], v[144:145], off
	s_nop 0
	v_addc_co_u32_e32 v111, vcc, 0, v111, vcc
	global_load_dwordx4 v[148:151], v[110:111], off
	s_waitcnt vmcnt(10)
	v_pk_add_f32 v[54:55], v[54:55], 0 op_sel_hi:[1,0]
	v_pk_add_f32 v[52:53], v[52:53], 0 op_sel_hi:[1,0]
	s_waitcnt vmcnt(9)
	v_pk_add_f32 v[54:55], v[54:55], v[114:115]
	v_pk_add_f32 v[52:53], v[52:53], v[112:113]
	s_waitcnt vmcnt(8)
	v_pk_add_f32 v[54:55], v[54:55], v[118:119]
	v_pk_add_f32 v[52:53], v[52:53], v[116:117]
	s_waitcnt vmcnt(7)
	v_pk_add_f32 v[54:55], v[54:55], v[122:123]
	v_pk_add_f32 v[52:53], v[52:53], v[120:121]
	s_waitcnt vmcnt(6)
	v_pk_add_f32 v[54:55], v[54:55], v[126:127]
	v_pk_add_f32 v[52:53], v[52:53], v[124:125]
	s_waitcnt vmcnt(5)
	v_pk_add_f32 v[54:55], v[54:55], v[130:131]
	v_pk_add_f32 v[52:53], v[52:53], v[128:129]
	s_waitcnt vmcnt(4)
	v_pk_add_f32 v[54:55], v[54:55], v[134:135]
	v_pk_add_f32 v[52:53], v[52:53], v[132:133]
	v_mov_b32_e32 v134, v1
	s_waitcnt vmcnt(3)
	v_pk_add_f32 v[54:55], v[54:55], v[138:139]
	v_pk_add_f32 v[52:53], v[52:53], v[136:137]
	s_waitcnt vmcnt(2)
	v_pk_add_f32 v[54:55], v[54:55], v[142:143]
	v_pk_add_f32 v[52:53], v[52:53], v[140:141]
	s_waitcnt vmcnt(1)
	v_pk_add_f32 v[54:55], v[54:55], v[146:147]
	v_pk_add_f32 v[52:53], v[52:53], v[144:145]
	s_waitcnt vmcnt(0)
	v_pk_add_f32 v[112:113], v[54:55], v[150:151]
	v_pk_add_f32 v[110:111], v[52:53], v[148:149]
	s_waitcnt vmcnt(0)
	v_pk_fma_f32 v[94:95], v[112:113], v[250:251], v[94:95]
	v_pk_fma_f32 v[96:97], v[110:111], v[248:249], v[96:97]
	v_cvt_pk_bf16_f32 v52, v100, v101
	v_cvt_pk_bf16_f32 v53, v98, v99
	v_lshl_add_u64 v[98:99], v[56:57], 0, s[2:3]
	global_store_dwordx2 v[98:99], v[52:53], off
	v_lshlrev_b32_e32 v110, 16, v52
	v_and_b32_e32 v111, 0xffff0000, v52
	v_lshlrev_b32_e32 v100, 16, v53
	v_and_b32_e32 v101, 0xffff0000, v53
	v_cvt_pk_bf16_f32 v52, v104, v105
	v_cvt_pk_bf16_f32 v53, v102, v103
	v_cvt_pk_bf16_f32 v54, v108, v109
	v_cvt_pk_bf16_f32 v55, v106, v107
	v_cvt_pk_bf16_f32 v106, v96, v97
	v_cvt_pk_bf16_f32 v107, v94, v95
	global_store_dwordx2 v[98:99], v[52:53], off offset:512
	v_lshlrev_b32_e32 v104, 16, v52
	v_and_b32_e32 v105, 0xffff0000, v52
	v_lshlrev_b32_e32 v102, 16, v53
	v_and_b32_e32 v103, 0xffff0000, v53
	global_store_dwordx2 v[98:99], v[54:55], off offset:1024
	v_lshlrev_b32_e32 v52, 16, v54
	v_and_b32_e32 v53, 0xffff0000, v54
	v_lshlrev_b32_e32 v54, 16, v55
	v_and_b32_e32 v55, 0xffff0000, v55
	v_lshlrev_b32_e32 v96, 16, v106
	v_and_b32_e32 v97, 0xffff0000, v106
	v_lshlrev_b32_e32 v94, 16, v107
	v_and_b32_e32 v95, 0xffff0000, v107
	global_store_dwordx2 v[98:99], v[106:107], off offset:1536

.LBB0_1260:
	s_min_i32 s2, s40, 0x4000
	s_and_b32 s2, s2, 0xfffff000
	s_add_i32 s2, s2, 0
	s_add_i32 s3, s2, 0xa000
	v_add_u32_e32 v1, s2, v58
	v_add_u32_e32 v2, s3, v58
	ds_read_b128 v[44:47], v1 offset:45056
	ds_read_b128 v[36:39], v1 offset:46080
	ds_read_b128 v[48:51], v2 offset:24576
	ds_read_b128 v[40:43], v2 offset:25600
	ds_read_b128 v[28:31], v1 offset:47104
	ds_read_b128 v[20:23], v1 offset:48128
	ds_read_b128 v[32:35], v2 offset:26624
	ds_read_b128 v[24:27], v2 offset:27648
	s_waitcnt vmcnt(11)
	v_lshlrev_b32_e32 v102, 16, v92
	v_and_b32_e32 v103, 0xffff0000, v92
	v_lshlrev_b32_e32 v92, 16, v93
	v_and_b32_e32 v93, 0xffff0000, v93
	s_waitcnt vmcnt(10)
	v_lshlrev_b32_e32 v96, 16, v90
	v_and_b32_e32 v97, 0xffff0000, v90
	v_lshlrev_b32_e32 v94, 16, v91
	v_and_b32_e32 v95, 0xffff0000, v91
	s_waitcnt vmcnt(9)
	v_lshlrev_b32_e32 v52, 16, v88
	v_and_b32_e32 v53, 0xffff0000, v88
	v_lshlrev_b32_e32 v54, 16, v89
	v_and_b32_e32 v55, 0xffff0000, v89
	s_waitcnt vmcnt(8)
	v_lshlrev_b32_e32 v88, 16, v86
	v_and_b32_e32 v89, 0xffff0000, v86
	v_lshlrev_b32_e32 v86, 16, v87
	s_cmpk_lt_i32 s40, 0x4000
	v_and_b32_e32 v87, 0xffff0000, v87
	s_cbranch_scc1 .LBB0_1262
	global_load_dwordx4 v[236:239], v[62:63], off
	global_load_dwordx4 v[240:243], v[66:67], off
	global_load_dwordx4 v[244:247], v[70:71], off
	global_load_dwordx4 v[248:251], v[74:75], off
	v_readlane_b32 s8, v255, 13
	s_mov_b32 s41, s81
	s_add_i32 s8, s8, s16
	s_mov_b32 s9, s81
	s_lshl_b64 s[2:3], s[40:41], 11
	s_lshl_b64 s[8:9], s[8:9], 2
	s_add_u32 s8, s0, s8
	s_addc_u32 s9, s1, s9
	s_add_u32 s8, s8, 0x420f8000
	s_addc_u32 s9, s9, 0
	v_lshlrev_b32_e32 v2, 4, v0
	v_lshl_add_u64 v[90:91], s[8:9], 0, v[2:3]
	s_mov_b32 s11, 0x400000
	v_add_co_u32_e32 v104, vcc, s11, v90
	s_mov_b32 s10, 0x800000
	s_nop 0
	v_addc_co_u32_e32 v105, vcc, 0, v91, vcc
	v_add_co_u32_e32 v108, vcc, s10, v90
	s_mov_b32 s12, 0xc00000
	s_nop 0
	v_addc_co_u32_e32 v109, vcc, 0, v91, vcc
	v_add_co_u32_e32 v112, vcc, s12, v90
	s_mov_b32 s13, 0x1000000
	s_nop 0
	v_addc_co_u32_e32 v113, vcc, 0, v91, vcc
	v_add_co_u32_e32 v116, vcc, s13, v90
	s_mov_b32 s14, 0x1400000
	s_nop 0
	v_addc_co_u32_e32 v117, vcc, 0, v91, vcc
	v_add_co_u32_e32 v120, vcc, s14, v90
	s_mov_b32 s15, 0x1800000
	s_nop 0
	v_addc_co_u32_e32 v121, vcc, 0, v91, vcc
	global_load_dwordx4 v[98:101], v2, s[8:9]
	v_add_co_u32_e32 v124, vcc, s15, v90
	global_load_dwordx4 v[104:107], v[104:105], off
	s_nop 0
	v_addc_co_u32_e32 v125, vcc, 0, v91, vcc
	s_mov_b32 s17, 0x1c00000
	global_load_dwordx4 v[108:111], v[108:109], off
	v_add_co_u32_e32 v128, vcc, s17, v90
	global_load_dwordx4 v[112:115], v[112:113], off
	s_nop 0
	v_addc_co_u32_e32 v129, vcc, 0, v91, vcc
	s_brev_b32 s18, 64
	global_load_dwordx4 v[116:119], v[116:117], off
	v_add_co_u32_e32 v132, vcc, s18, v90
	global_load_dwordx4 v[120:123], v[120:121], off
	s_nop 0
	v_addc_co_u32_e32 v133, vcc, 0, v91, vcc
	s_mov_b32 s19, 0x2400000
	global_load_dwordx4 v[124:127], v[124:125], off
	v_add_co_u32_e32 v136, vcc, s19, v90
	global_load_dwordx4 v[128:131], v[128:129], off
	s_nop 0
	v_addc_co_u32_e32 v137, vcc, 0, v91, vcc
	s_mov_b32 s20, 0x2800000
	v_mov_b32_e32 v1, v134
	global_load_dwordx4 v[132:135], v[132:133], off
	v_add_co_u32_e32 v90, vcc, s20, v90
	global_load_dwordx4 v[136:139], v[136:137], off
	s_nop 0
	v_addc_co_u32_e32 v91, vcc, 0, v91, vcc
	global_load_dwordx4 v[140:143], v[90:91], off
	v_lshlrev_b32_e32 v2, 4, v64
	s_waitcnt vmcnt(10)
	v_pk_add_f32 v[98:99], v[98:99], 0 op_sel_hi:[1,0]
	v_pk_add_f32 v[90:91], v[100:101], 0 op_sel_hi:[1,0]
	s_waitcnt vmcnt(9)
	v_pk_add_f32 v[98:99], v[98:99], v[104:105]
	v_pk_add_f32 v[90:91], v[90:91], v[106:107]
	s_waitcnt vmcnt(8)
	v_pk_add_f32 v[98:99], v[98:99], v[108:109]
	v_pk_add_f32 v[90:91], v[90:91], v[110:111]
	s_waitcnt vmcnt(7)
	v_pk_add_f32 v[98:99], v[98:99], v[112:113]
	v_pk_add_f32 v[90:91], v[90:91], v[114:115]
	s_waitcnt vmcnt(6)
	v_pk_add_f32 v[98:99], v[98:99], v[116:117]
	v_pk_add_f32 v[90:91], v[90:91], v[118:119]
	s_waitcnt vmcnt(5)
	v_pk_add_f32 v[98:99], v[98:99], v[120:121]
	v_pk_add_f32 v[90:91], v[90:91], v[122:123]
	s_waitcnt vmcnt(4)
	v_pk_add_f32 v[98:99], v[98:99], v[124:125]
	v_pk_add_f32 v[90:91], v[90:91], v[126:127]
	s_waitcnt vmcnt(3)
	v_pk_add_f32 v[98:99], v[98:99], v[128:129]
	v_pk_add_f32 v[90:91], v[90:91], v[130:131]
	s_waitcnt vmcnt(2)
	v_pk_add_f32 v[98:99], v[98:99], v[132:133]
	v_pk_add_f32 v[90:91], v[90:91], v[134:135]
	s_waitcnt vmcnt(1)
	v_pk_add_f32 v[98:99], v[98:99], v[136:137]
	v_pk_add_f32 v[90:91], v[90:91], v[138:139]
	v_lshl_add_u64 v[138:139], s[8:9], 0, v[2:3]
	s_waitcnt vmcnt(0)
	v_pk_add_f32 v[104:105], v[98:99], v[140:141]
	v_pk_add_f32 v[90:91], v[90:91], v[142:143]
	s_waitcnt vmcnt(0)
	v_pk_fma_f32 v[90:91], v[90:91], v[238:239], v[92:93]
	v_pk_fma_f32 v[92:93], v[104:105], v[236:237], v[102:103]
	v_add_co_u32_e32 v102, vcc, s11, v138
	global_load_dwordx4 v[98:101], v2, s[8:9]
	s_nop 0
	v_addc_co_u32_e32 v103, vcc, 0, v139, vcc
	v_add_co_u32_e32 v106, vcc, s10, v138
	global_load_dwordx4 v[102:105], v[102:103], off
	s_nop 0
	v_addc_co_u32_e32 v107, vcc, 0, v139, vcc
	v_add_co_u32_e32 v110, vcc, s12, v138
	global_load_dwordx4 v[106:109], v[106:107], off
	s_nop 0
	v_addc_co_u32_e32 v111, vcc, 0, v139, vcc
	v_add_co_u32_e32 v114, vcc, s13, v138
	global_load_dwordx4 v[110:113], v[110:111], off
	s_nop 0
	v_addc_co_u32_e32 v115, vcc, 0, v139, vcc
	v_add_co_u32_e32 v118, vcc, s14, v138
	global_load_dwordx4 v[114:117], v[114:115], off
	s_nop 0
	v_addc_co_u32_e32 v119, vcc, 0, v139, vcc
	v_add_co_u32_e32 v122, vcc, s15, v138
	global_load_dwordx4 v[118:121], v[118:119], off
	s_nop 0
	v_addc_co_u32_e32 v123, vcc, 0, v139, vcc
	v_add_co_u32_e32 v126, vcc, s17, v138
	global_load_dwordx4 v[122:125], v[122:123], off
	s_nop 0
	v_addc_co_u32_e32 v127, vcc, 0, v139, vcc
	v_add_co_u32_e32 v130, vcc, s18, v138
	global_load_dwordx4 v[126:129], v[126:127], off
	s_nop 0
	v_addc_co_u32_e32 v131, vcc, 0, v139, vcc
	v_add_co_u32_e32 v134, vcc, s19, v138
	global_load_dwordx4 v[130:133], v[130:131], off
	s_nop 0
	v_addc_co_u32_e32 v135, vcc, 0, v139, vcc
	v_add_co_u32_e32 v138, vcc, s20, v138
	global_load_dwordx4 v[134:137], v[134:135], off
	s_nop 0
	v_addc_co_u32_e32 v139, vcc, 0, v139, vcc
	global_load_dwordx4 v[138:141], v[138:139], off
	v_lshlrev_b32_e32 v2, 4, v68
	s_waitcnt vmcnt(10)
	v_pk_add_f32 v[100:101], v[100:101], 0 op_sel_hi:[1,0]
	v_pk_add_f32 v[98:99], v[98:99], 0 op_sel_hi:[1,0]
	s_waitcnt vmcnt(9)
	v_pk_add_f32 v[100:101], v[100:101], v[104:105]
	v_pk_add_f32 v[98:99], v[98:99], v[102:103]
	s_waitcnt vmcnt(8)
	v_pk_add_f32 v[100:101], v[100:101], v[108:109]
	v_pk_add_f32 v[98:99], v[98:99], v[106:107]
	s_waitcnt vmcnt(7)
	v_pk_add_f32 v[100:101], v[100:101], v[112:113]
	v_pk_add_f32 v[98:99], v[98:99], v[110:111]
	s_waitcnt vmcnt(6)
	v_pk_add_f32 v[100:101], v[100:101], v[116:117]
	v_pk_add_f32 v[98:99], v[98:99], v[114:115]
	s_waitcnt vmcnt(5)
	v_pk_add_f32 v[100:101], v[100:101], v[120:121]
	v_pk_add_f32 v[98:99], v[98:99], v[118:119]
	s_waitcnt vmcnt(4)
	v_pk_add_f32 v[100:101], v[100:101], v[124:125]
	v_pk_add_f32 v[98:99], v[98:99], v[122:123]
	s_waitcnt vmcnt(3)
	v_pk_add_f32 v[100:101], v[100:101], v[128:129]
	v_pk_add_f32 v[98:99], v[98:99], v[126:127]
	s_waitcnt vmcnt(2)
	v_pk_add_f32 v[100:101], v[100:101], v[132:133]
	v_pk_add_f32 v[98:99], v[98:99], v[130:131]
	s_waitcnt vmcnt(1)
	v_pk_add_f32 v[100:101], v[100:101], v[136:137]
	v_pk_add_f32 v[98:99], v[98:99], v[134:135]
	s_waitcnt vmcnt(0)
	v_pk_add_f32 v[102:103], v[100:101], v[140:141]
	v_pk_add_f32 v[104:105], v[98:99], v[138:139]
	v_lshl_add_u64 v[138:139], s[8:9], 0, v[2:3]
	s_waitcnt vmcnt(0)
	v_pk_fma_f32 v[94:95], v[102:103], v[242:243], v[94:95]
	v_add_co_u32_e32 v102, vcc, s11, v138
	v_pk_fma_f32 v[96:97], v[104:105], v[240:241], v[96:97]
	s_nop 0
	v_addc_co_u32_e32 v103, vcc, 0, v139, vcc
	v_add_co_u32_e32 v106, vcc, s10, v138
	global_load_dwordx4 v[98:101], v2, s[8:9]
	s_nop 0
	v_addc_co_u32_e32 v107, vcc, 0, v139, vcc
	v_add_co_u32_e32 v110, vcc, s12, v138
	global_load_dwordx4 v[102:105], v[102:103], off
	s_nop 0
	v_addc_co_u32_e32 v111, vcc, 0, v139, vcc
	v_add_co_u32_e32 v114, vcc, s13, v138
	global_load_dwordx4 v[106:109], v[106:107], off
	s_nop 0
	v_addc_co_u32_e32 v115, vcc, 0, v139, vcc
	v_add_co_u32_e32 v118, vcc, s14, v138
	global_load_dwordx4 v[110:113], v[110:111], off
	s_nop 0
	v_addc_co_u32_e32 v119, vcc, 0, v139, vcc
	v_add_co_u32_e32 v122, vcc, s15, v138
	global_load_dwordx4 v[114:117], v[114:115], off
	s_nop 0
	v_addc_co_u32_e32 v123, vcc, 0, v139, vcc
	v_add_co_u32_e32 v126, vcc, s17, v138
	global_load_dwordx4 v[118:121], v[118:119], off
	s_nop 0
	v_addc_co_u32_e32 v127, vcc, 0, v139, vcc
	v_add_co_u32_e32 v130, vcc, s18, v138
	global_load_dwordx4 v[122:125], v[122:123], off
	s_nop 0
	v_addc_co_u32_e32 v131, vcc, 0, v139, vcc
	v_add_co_u32_e32 v134, vcc, s19, v138
	global_load_dwordx4 v[126:129], v[126:127], off
	s_nop 0
	v_addc_co_u32_e32 v135, vcc, 0, v139, vcc
	global_load_dwordx4 v[130:133], v[130:131], off
	v_add_co_u32_e32 v138, vcc, s20, v138
	global_load_dwordx4 v[134:137], v[134:135], off
	s_nop 0
	v_addc_co_u32_e32 v139, vcc, 0, v139, vcc
	global_load_dwordx4 v[138:141], v[138:139], off
	v_lshlrev_b32_e32 v2, 4, v72
	s_waitcnt vmcnt(10)
	v_pk_add_f32 v[100:101], v[100:101], 0 op_sel_hi:[1,0]
	v_pk_add_f32 v[98:99], v[98:99], 0 op_sel_hi:[1,0]
	s_waitcnt vmcnt(9)
	v_pk_add_f32 v[100:101], v[100:101], v[104:105]
	v_pk_add_f32 v[98:99], v[98:99], v[102:103]
	s_waitcnt vmcnt(8)
	v_pk_add_f32 v[100:101], v[100:101], v[108:109]
	v_pk_add_f32 v[98:99], v[98:99], v[106:107]
	s_waitcnt vmcnt(7)
	v_pk_add_f32 v[100:101], v[100:101], v[112:113]
	v_pk_add_f32 v[98:99], v[98:99], v[110:111]
	s_waitcnt vmcnt(6)
	v_pk_add_f32 v[100:101], v[100:101], v[116:117]
	v_pk_add_f32 v[98:99], v[98:99], v[114:115]
	s_waitcnt vmcnt(5)
	v_pk_add_f32 v[100:101], v[100:101], v[120:121]
	v_pk_add_f32 v[98:99], v[98:99], v[118:119]
	s_waitcnt vmcnt(4)
	v_pk_add_f32 v[100:101], v[100:101], v[124:125]
	v_pk_add_f32 v[98:99], v[98:99], v[122:123]
	s_waitcnt vmcnt(3)
	v_pk_add_f32 v[100:101], v[100:101], v[128:129]
	v_pk_add_f32 v[98:99], v[98:99], v[126:127]
	s_waitcnt vmcnt(2)
	v_pk_add_f32 v[100:101], v[100:101], v[132:133]
	v_pk_add_f32 v[98:99], v[98:99], v[130:131]
	s_waitcnt vmcnt(1)
	v_pk_add_f32 v[100:101], v[100:101], v[136:137]
	v_pk_add_f32 v[98:99], v[98:99], v[134:135]
	s_waitcnt vmcnt(0)
	v_pk_add_f32 v[104:105], v[100:101], v[140:141]
	v_pk_add_f32 v[106:107], v[98:99], v[138:139]
	s_waitcnt vmcnt(0)
	v_pk_fma_f32 v[98:99], v[104:105], v[246:247], v[54:55]
	v_lshl_add_u64 v[102:103], s[8:9], 0, v[2:3]
	v_add_co_u32_e32 v104, vcc, s11, v102
	v_pk_fma_f32 v[100:101], v[106:107], v[244:245], v[52:53]
	s_nop 0
	v_addc_co_u32_e32 v105, vcc, 0, v103, vcc
	v_add_co_u32_e32 v108, vcc, s10, v102
	global_load_dwordx4 v[52:55], v2, s[8:9]
	s_nop 0
	v_addc_co_u32_e32 v109, vcc, 0, v103, vcc
	v_add_co_u32_e32 v112, vcc, s12, v102
	global_load_dwordx4 v[104:107], v[104:105], off
	s_nop 0
	v_addc_co_u32_e32 v113, vcc, 0, v103, vcc
	v_add_co_u32_e32 v116, vcc, s13, v102
	global_load_dwordx4 v[108:111], v[108:109], off
	s_nop 0
	v_addc_co_u32_e32 v117, vcc, 0, v103, vcc
	v_add_co_u32_e32 v120, vcc, s14, v102
	global_load_dwordx4 v[112:115], v[112:113], off
	s_nop 0
	v_addc_co_u32_e32 v121, vcc, 0, v103, vcc
	v_add_co_u32_e32 v124, vcc, s15, v102
	global_load_dwordx4 v[116:119], v[116:117], off
	s_nop 0
	v_addc_co_u32_e32 v125, vcc, 0, v103, vcc
	v_add_co_u32_e32 v128, vcc, s17, v102
	global_load_dwordx4 v[120:123], v[120:121], off
	s_nop 0
	v_addc_co_u32_e32 v129, vcc, 0, v103, vcc
	v_add_co_u32_e32 v132, vcc, s18, v102
	global_load_dwordx4 v[124:127], v[124:125], off
	s_nop 0
	v_addc_co_u32_e32 v133, vcc, 0, v103, vcc
	v_add_co_u32_e32 v136, vcc, s19, v102
	global_load_dwordx4 v[128:131], v[128:129], off
	s_nop 0
	v_addc_co_u32_e32 v137, vcc, 0, v103, vcc
	global_load_dwordx4 v[132:135], v[132:133], off
	v_add_co_u32_e32 v102, vcc, s20, v102
	global_load_dwordx4 v[136:139], v[136:137], off
	s_nop 0
	v_addc_co_u32_e32 v103, vcc, 0, v103, vcc
	global_load_dwordx4 v[140:143], v[102:103], off
	s_waitcnt vmcnt(10)
	v_pk_add_f32 v[54:55], v[54:55], 0 op_sel_hi:[1,0]
	v_pk_add_f32 v[52:53], v[52:53], 0 op_sel_hi:[1,0]
	s_waitcnt vmcnt(9)
	v_pk_add_f32 v[54:55], v[54:55], v[106:107]
	v_pk_add_f32 v[52:53], v[52:53], v[104:105]
	s_waitcnt vmcnt(8)
	v_pk_add_f32 v[54:55], v[54:55], v[110:111]
	v_pk_add_f32 v[52:53], v[52:53], v[108:109]
	s_waitcnt vmcnt(7)
	v_pk_add_f32 v[54:55], v[54:55], v[114:115]
	v_pk_add_f32 v[52:53], v[52:53], v[112:113]
	s_waitcnt vmcnt(6)
	v_pk_add_f32 v[54:55], v[54:55], v[118:119]
	v_pk_add_f32 v[52:53], v[52:53], v[116:117]
	s_waitcnt vmcnt(5)
	v_pk_add_f32 v[54:55], v[54:55], v[122:123]
	v_pk_add_f32 v[52:53], v[52:53], v[120:121]
	s_waitcnt vmcnt(4)
	v_pk_add_f32 v[54:55], v[54:55], v[126:127]
	v_pk_add_f32 v[52:53], v[52:53], v[124:125]
	s_waitcnt vmcnt(3)
	v_pk_add_f32 v[54:55], v[54:55], v[130:131]
	v_pk_add_f32 v[52:53], v[52:53], v[128:129]
	s_waitcnt vmcnt(2)
	v_pk_add_f32 v[54:55], v[54:55], v[134:135]
	v_pk_add_f32 v[52:53], v[52:53], v[132:133]
	v_mov_b32_e32 v134, v1
	s_waitcnt vmcnt(1)
	v_pk_add_f32 v[54:55], v[54:55], v[138:139]
	v_pk_add_f32 v[52:53], v[52:53], v[136:137]
	s_waitcnt vmcnt(0)
	v_pk_add_f32 v[104:105], v[54:55], v[142:143]
	v_pk_add_f32 v[102:103], v[52:53], v[140:141]
	s_waitcnt vmcnt(0)
	v_pk_fma_f32 v[86:87], v[104:105], v[250:251], v[86:87]
	v_pk_fma_f32 v[88:89], v[102:103], v[248:249], v[88:89]
	v_cvt_pk_bf16_f32 v52, v92, v93
	v_cvt_pk_bf16_f32 v53, v90, v91
	v_lshl_add_u64 v[90:91], v[56:57], 0, s[2:3]
	global_store_dwordx2 v[90:91], v[52:53], off
	v_lshlrev_b32_e32 v102, 16, v52
	v_and_b32_e32 v103, 0xffff0000, v52
	v_lshlrev_b32_e32 v92, 16, v53
	v_and_b32_e32 v93, 0xffff0000, v53
	v_cvt_pk_bf16_f32 v52, v96, v97
	v_cvt_pk_bf16_f32 v53, v94, v95
	v_cvt_pk_bf16_f32 v54, v100, v101
	v_cvt_pk_bf16_f32 v55, v98, v99
	v_cvt_pk_bf16_f32 v98, v88, v89
	v_cvt_pk_bf16_f32 v99, v86, v87
	global_store_dwordx2 v[90:91], v[52:53], off offset:512
	v_lshlrev_b32_e32 v96, 16, v52
	v_and_b32_e32 v97, 0xffff0000, v52
	v_lshlrev_b32_e32 v94, 16, v53
	v_and_b32_e32 v95, 0xffff0000, v53
	global_store_dwordx2 v[90:91], v[54:55], off offset:1024
	v_lshlrev_b32_e32 v52, 16, v54
	v_and_b32_e32 v53, 0xffff0000, v54
	v_lshlrev_b32_e32 v54, 16, v55
	v_and_b32_e32 v55, 0xffff0000, v55
	v_lshlrev_b32_e32 v88, 16, v98
	v_and_b32_e32 v89, 0xffff0000, v98
	v_lshlrev_b32_e32 v86, 16, v99
	v_and_b32_e32 v87, 0xffff0000, v99
	global_store_dwordx2 v[90:91], v[98:99], off offset:1536

.LBB0_1263:
	s_min_i32 s2, s38, 0x4000
	s_and_b32 s2, s2, 0xfffff000
	s_add_i32 s2, s2, 0
	s_add_i32 s3, s2, 0xa000
	v_add_u32_e32 v1, s2, v58
	v_add_u32_e32 v2, s3, v58
	ds_read_b128 v[44:47], v1 offset:45056
	ds_read_b128 v[36:39], v1 offset:46080
	ds_read_b128 v[48:51], v2 offset:24576
	ds_read_b128 v[40:43], v2 offset:25600
	ds_read_b128 v[28:31], v1 offset:47104
	ds_read_b128 v[20:23], v1 offset:48128
	ds_read_b128 v[32:35], v2 offset:26624
	ds_read_b128 v[24:27], v2 offset:27648
	s_waitcnt vmcnt(7)
	v_lshlrev_b32_e32 v94, 16, v84
	v_and_b32_e32 v95, 0xffff0000, v84
	v_lshlrev_b32_e32 v84, 16, v85
	v_and_b32_e32 v85, 0xffff0000, v85
	s_waitcnt vmcnt(6)
	v_lshlrev_b32_e32 v88, 16, v82
	v_and_b32_e32 v89, 0xffff0000, v82
	v_lshlrev_b32_e32 v86, 16, v83
	v_and_b32_e32 v87, 0xffff0000, v83
	s_waitcnt vmcnt(5)
	v_lshlrev_b32_e32 v52, 16, v80
	v_and_b32_e32 v53, 0xffff0000, v80
	v_lshlrev_b32_e32 v54, 16, v81
	v_and_b32_e32 v55, 0xffff0000, v81
	s_waitcnt vmcnt(4)
	v_lshlrev_b32_e32 v80, 16, v78
	v_and_b32_e32 v81, 0xffff0000, v78
	v_lshlrev_b32_e32 v78, 16, v79
	s_cmpk_lt_i32 s38, 0x4000
	v_and_b32_e32 v79, 0xffff0000, v79
	s_cbranch_scc1 .LBB0_1245
	global_load_dwordx4 v[236:239], v[62:63], off
	global_load_dwordx4 v[240:243], v[66:67], off
	global_load_dwordx4 v[244:247], v[70:71], off
	global_load_dwordx4 v[248:251], v[74:75], off
	v_readlane_b32 s8, v255, 14
	s_mov_b32 s39, s81
	s_add_i32 s8, s8, s16
	s_mov_b32 s9, s81
	s_lshl_b64 s[2:3], s[38:39], 11
	s_lshl_b64 s[8:9], s[8:9], 2
	s_add_u32 s8, s0, s8
	s_addc_u32 s9, s1, s9
	s_add_u32 s8, s8, 0x420f8000
	s_addc_u32 s9, s9, 0
	v_lshlrev_b32_e32 v2, 4, v0
	v_lshl_add_u64 v[82:83], s[8:9], 0, v[2:3]
	s_mov_b32 s11, 0x400000
	v_add_co_u32_e32 v96, vcc, s11, v82
	s_mov_b32 s10, 0x800000
	s_nop 0
	v_addc_co_u32_e32 v97, vcc, 0, v83, vcc
	v_add_co_u32_e32 v100, vcc, s10, v82
	s_mov_b32 s12, 0xc00000
	s_nop 0
	v_addc_co_u32_e32 v101, vcc, 0, v83, vcc
	v_add_co_u32_e32 v104, vcc, s12, v82
	s_mov_b32 s13, 0x1000000
	s_nop 0
	v_addc_co_u32_e32 v105, vcc, 0, v83, vcc
	v_add_co_u32_e32 v108, vcc, s13, v82
	s_mov_b32 s14, 0x1400000
	s_nop 0
	v_addc_co_u32_e32 v109, vcc, 0, v83, vcc
	v_add_co_u32_e32 v112, vcc, s14, v82
	s_mov_b32 s15, 0x1800000
	s_nop 0
	v_addc_co_u32_e32 v113, vcc, 0, v83, vcc
	global_load_dwordx4 v[90:93], v2, s[8:9]
	v_add_co_u32_e32 v116, vcc, s15, v82
	global_load_dwordx4 v[96:99], v[96:97], off
	s_nop 0
	v_addc_co_u32_e32 v117, vcc, 0, v83, vcc
	s_mov_b32 s17, 0x1c00000
	global_load_dwordx4 v[100:103], v[100:101], off
	v_add_co_u32_e32 v120, vcc, s17, v82
	global_load_dwordx4 v[104:107], v[104:105], off
	s_nop 0
	v_addc_co_u32_e32 v121, vcc, 0, v83, vcc
	s_brev_b32 s18, 64
	global_load_dwordx4 v[108:111], v[108:109], off
	v_add_co_u32_e32 v124, vcc, s18, v82
	global_load_dwordx4 v[112:115], v[112:113], off
	s_nop 0
	v_addc_co_u32_e32 v125, vcc, 0, v83, vcc
	s_mov_b32 s19, 0x2400000
	global_load_dwordx4 v[116:119], v[116:117], off
	v_add_co_u32_e32 v128, vcc, s19, v82
	global_load_dwordx4 v[120:123], v[120:121], off
	s_nop 0
	v_addc_co_u32_e32 v129, vcc, 0, v83, vcc
	s_mov_b32 s20, 0x2800000
	global_load_dwordx4 v[124:127], v[124:125], off
	v_add_co_u32_e32 v82, vcc, s20, v82
	global_load_dwordx4 v[128:131], v[128:129], off
	s_nop 0
	v_addc_co_u32_e32 v83, vcc, 0, v83, vcc
	v_mov_b32_e32 v1, v134
	global_load_dwordx4 v[132:135], v[82:83], off
	v_lshlrev_b32_e32 v2, 4, v64
	s_waitcnt vmcnt(10)
	v_pk_add_f32 v[90:91], v[90:91], 0 op_sel_hi:[1,0]
	v_pk_add_f32 v[82:83], v[92:93], 0 op_sel_hi:[1,0]
	s_waitcnt vmcnt(9)
	v_pk_add_f32 v[90:91], v[90:91], v[96:97]
	v_pk_add_f32 v[82:83], v[82:83], v[98:99]
	s_waitcnt vmcnt(8)
	v_pk_add_f32 v[90:91], v[90:91], v[100:101]
	v_pk_add_f32 v[82:83], v[82:83], v[102:103]
	s_waitcnt vmcnt(7)
	v_pk_add_f32 v[90:91], v[90:91], v[104:105]
	v_pk_add_f32 v[82:83], v[82:83], v[106:107]
	s_waitcnt vmcnt(6)
	v_pk_add_f32 v[90:91], v[90:91], v[108:109]
	v_pk_add_f32 v[82:83], v[82:83], v[110:111]
	s_waitcnt vmcnt(5)
	v_pk_add_f32 v[90:91], v[90:91], v[112:113]
	v_pk_add_f32 v[82:83], v[82:83], v[114:115]
	s_waitcnt vmcnt(4)
	v_pk_add_f32 v[90:91], v[90:91], v[116:117]
	v_pk_add_f32 v[82:83], v[82:83], v[118:119]
	s_waitcnt vmcnt(3)
	v_pk_add_f32 v[90:91], v[90:91], v[120:121]
	v_pk_add_f32 v[82:83], v[82:83], v[122:123]
	s_waitcnt vmcnt(2)
	v_pk_add_f32 v[90:91], v[90:91], v[124:125]
	v_pk_add_f32 v[82:83], v[82:83], v[126:127]
	s_waitcnt vmcnt(1)
	v_pk_add_f32 v[90:91], v[90:91], v[128:129]
	v_pk_add_f32 v[82:83], v[82:83], v[130:131]
	v_lshl_add_u64 v[130:131], s[8:9], 0, v[2:3]
	s_waitcnt vmcnt(0)
	v_pk_add_f32 v[96:97], v[90:91], v[132:133]
	v_pk_add_f32 v[82:83], v[82:83], v[134:135]
	s_waitcnt vmcnt(0)
	v_pk_fma_f32 v[82:83], v[82:83], v[238:239], v[84:85]
	v_pk_fma_f32 v[84:85], v[96:97], v[236:237], v[94:95]
	v_add_co_u32_e32 v94, vcc, s11, v130
	global_load_dwordx4 v[90:93], v2, s[8:9]
	s_nop 0
	v_addc_co_u32_e32 v95, vcc, 0, v131, vcc
	v_add_co_u32_e32 v98, vcc, s10, v130
	global_load_dwordx4 v[94:97], v[94:95], off
	s_nop 0
	v_addc_co_u32_e32 v99, vcc, 0, v131, vcc
	v_add_co_u32_e32 v102, vcc, s12, v130
	global_load_dwordx4 v[98:101], v[98:99], off
	s_nop 0
	v_addc_co_u32_e32 v103, vcc, 0, v131, vcc
	v_add_co_u32_e32 v106, vcc, s13, v130
	global_load_dwordx4 v[102:105], v[102:103], off
	s_nop 0
	v_addc_co_u32_e32 v107, vcc, 0, v131, vcc
	v_add_co_u32_e32 v110, vcc, s14, v130
	global_load_dwordx4 v[106:109], v[106:107], off
	s_nop 0
	v_addc_co_u32_e32 v111, vcc, 0, v131, vcc
	v_add_co_u32_e32 v114, vcc, s15, v130
	global_load_dwordx4 v[110:113], v[110:111], off
	s_nop 0
	v_addc_co_u32_e32 v115, vcc, 0, v131, vcc
	v_add_co_u32_e32 v118, vcc, s17, v130
	global_load_dwordx4 v[114:117], v[114:115], off
	s_nop 0
	v_addc_co_u32_e32 v119, vcc, 0, v131, vcc
	v_add_co_u32_e32 v122, vcc, s18, v130
	global_load_dwordx4 v[118:121], v[118:119], off
	s_nop 0
	v_addc_co_u32_e32 v123, vcc, 0, v131, vcc
	v_add_co_u32_e32 v126, vcc, s19, v130
	global_load_dwordx4 v[122:125], v[122:123], off
	s_nop 0
	v_addc_co_u32_e32 v127, vcc, 0, v131, vcc
	v_add_co_u32_e32 v130, vcc, s20, v130
	global_load_dwordx4 v[126:129], v[126:127], off
	s_nop 0
	v_addc_co_u32_e32 v131, vcc, 0, v131, vcc
	global_load_dwordx4 v[130:133], v[130:131], off
	v_lshlrev_b32_e32 v2, 4, v68
	s_waitcnt vmcnt(10)
	v_pk_add_f32 v[92:93], v[92:93], 0 op_sel_hi:[1,0]
	v_pk_add_f32 v[90:91], v[90:91], 0 op_sel_hi:[1,0]
	s_waitcnt vmcnt(9)
	v_pk_add_f32 v[92:93], v[92:93], v[96:97]
	v_pk_add_f32 v[90:91], v[90:91], v[94:95]
	s_waitcnt vmcnt(8)
	v_pk_add_f32 v[92:93], v[92:93], v[100:101]
	v_pk_add_f32 v[90:91], v[90:91], v[98:99]
	s_waitcnt vmcnt(7)
	v_pk_add_f32 v[92:93], v[92:93], v[104:105]
	v_pk_add_f32 v[90:91], v[90:91], v[102:103]
	s_waitcnt vmcnt(6)
	v_pk_add_f32 v[92:93], v[92:93], v[108:109]
	v_pk_add_f32 v[90:91], v[90:91], v[106:107]
	s_waitcnt vmcnt(5)
	v_pk_add_f32 v[92:93], v[92:93], v[112:113]
	v_pk_add_f32 v[90:91], v[90:91], v[110:111]
	s_waitcnt vmcnt(4)
	v_pk_add_f32 v[92:93], v[92:93], v[116:117]
	v_pk_add_f32 v[90:91], v[90:91], v[114:115]
	s_waitcnt vmcnt(3)
	v_pk_add_f32 v[92:93], v[92:93], v[120:121]
	v_pk_add_f32 v[90:91], v[90:91], v[118:119]
	s_waitcnt vmcnt(2)
	v_pk_add_f32 v[92:93], v[92:93], v[124:125]
	v_pk_add_f32 v[90:91], v[90:91], v[122:123]
	s_waitcnt vmcnt(1)
	v_pk_add_f32 v[92:93], v[92:93], v[128:129]
	v_pk_add_f32 v[90:91], v[90:91], v[126:127]
	s_waitcnt vmcnt(0)
	v_pk_add_f32 v[94:95], v[92:93], v[132:133]
	v_pk_add_f32 v[96:97], v[90:91], v[130:131]
	v_lshl_add_u64 v[130:131], s[8:9], 0, v[2:3]
	s_waitcnt vmcnt(0)
	v_pk_fma_f32 v[86:87], v[94:95], v[242:243], v[86:87]
	v_add_co_u32_e32 v94, vcc, s11, v130
	v_pk_fma_f32 v[88:89], v[96:97], v[240:241], v[88:89]
	s_nop 0
	v_addc_co_u32_e32 v95, vcc, 0, v131, vcc
	v_add_co_u32_e32 v98, vcc, s10, v130
	global_load_dwordx4 v[90:93], v2, s[8:9]
	s_nop 0
	v_addc_co_u32_e32 v99, vcc, 0, v131, vcc
	v_add_co_u32_e32 v102, vcc, s12, v130
	global_load_dwordx4 v[94:97], v[94:95], off
	s_nop 0
	v_addc_co_u32_e32 v103, vcc, 0, v131, vcc
	v_add_co_u32_e32 v106, vcc, s13, v130
	global_load_dwordx4 v[98:101], v[98:99], off
	s_nop 0
	v_addc_co_u32_e32 v107, vcc, 0, v131, vcc
	v_add_co_u32_e32 v110, vcc, s14, v130
	global_load_dwordx4 v[102:105], v[102:103], off
	s_nop 0
	v_addc_co_u32_e32 v111, vcc, 0, v131, vcc
	v_add_co_u32_e32 v114, vcc, s15, v130
	global_load_dwordx4 v[106:109], v[106:107], off
	s_nop 0
	v_addc_co_u32_e32 v115, vcc, 0, v131, vcc
	v_add_co_u32_e32 v118, vcc, s17, v130
	global_load_dwordx4 v[110:113], v[110:111], off
	s_nop 0
	v_addc_co_u32_e32 v119, vcc, 0, v131, vcc
	v_add_co_u32_e32 v122, vcc, s18, v130
	global_load_dwordx4 v[114:117], v[114:115], off
	s_nop 0
	v_addc_co_u32_e32 v123, vcc, 0, v131, vcc
	v_add_co_u32_e32 v126, vcc, s19, v130
	global_load_dwordx4 v[118:121], v[118:119], off
	s_nop 0
	v_addc_co_u32_e32 v127, vcc, 0, v131, vcc
	global_load_dwordx4 v[122:125], v[122:123], off
	v_add_co_u32_e32 v130, vcc, s20, v130
	global_load_dwordx4 v[126:129], v[126:127], off
	s_nop 0
	v_addc_co_u32_e32 v131, vcc, 0, v131, vcc
	global_load_dwordx4 v[130:133], v[130:131], off
	v_lshlrev_b32_e32 v2, 4, v72
	s_waitcnt vmcnt(10)
	v_pk_add_f32 v[92:93], v[92:93], 0 op_sel_hi:[1,0]
	v_pk_add_f32 v[90:91], v[90:91], 0 op_sel_hi:[1,0]
	s_waitcnt vmcnt(9)
	v_pk_add_f32 v[92:93], v[92:93], v[96:97]
	v_pk_add_f32 v[90:91], v[90:91], v[94:95]
	s_waitcnt vmcnt(8)
	v_pk_add_f32 v[92:93], v[92:93], v[100:101]
	v_pk_add_f32 v[90:91], v[90:91], v[98:99]
	s_waitcnt vmcnt(7)
	v_pk_add_f32 v[92:93], v[92:93], v[104:105]
	v_pk_add_f32 v[90:91], v[90:91], v[102:103]
	s_waitcnt vmcnt(6)
	v_pk_add_f32 v[92:93], v[92:93], v[108:109]
	v_pk_add_f32 v[90:91], v[90:91], v[106:107]
	s_waitcnt vmcnt(5)
	v_pk_add_f32 v[92:93], v[92:93], v[112:113]
	v_pk_add_f32 v[90:91], v[90:91], v[110:111]
	s_waitcnt vmcnt(4)
	v_pk_add_f32 v[92:93], v[92:93], v[116:117]
	v_pk_add_f32 v[90:91], v[90:91], v[114:115]
	s_waitcnt vmcnt(3)
	v_pk_add_f32 v[92:93], v[92:93], v[120:121]
	v_pk_add_f32 v[90:91], v[90:91], v[118:119]
	s_waitcnt vmcnt(2)
	v_pk_add_f32 v[92:93], v[92:93], v[124:125]
	v_pk_add_f32 v[90:91], v[90:91], v[122:123]
	s_waitcnt vmcnt(1)
	v_pk_add_f32 v[92:93], v[92:93], v[128:129]
	v_pk_add_f32 v[90:91], v[90:91], v[126:127]
	s_waitcnt vmcnt(0)
	v_pk_add_f32 v[96:97], v[92:93], v[132:133]
	v_pk_add_f32 v[98:99], v[90:91], v[130:131]
	s_waitcnt vmcnt(0)
	v_pk_fma_f32 v[90:91], v[96:97], v[246:247], v[54:55]
	v_lshl_add_u64 v[94:95], s[8:9], 0, v[2:3]
	v_add_co_u32_e32 v96, vcc, s11, v94
	v_pk_fma_f32 v[92:93], v[98:99], v[244:245], v[52:53]
	s_nop 0
	v_addc_co_u32_e32 v97, vcc, 0, v95, vcc
	v_add_co_u32_e32 v100, vcc, s10, v94
	global_load_dwordx4 v[52:55], v2, s[8:9]
	s_nop 0
	v_addc_co_u32_e32 v101, vcc, 0, v95, vcc
	v_add_co_u32_e32 v104, vcc, s12, v94
	global_load_dwordx4 v[96:99], v[96:97], off
	s_nop 0
	v_addc_co_u32_e32 v105, vcc, 0, v95, vcc
	v_add_co_u32_e32 v108, vcc, s13, v94
	global_load_dwordx4 v[100:103], v[100:101], off
	s_nop 0
	v_addc_co_u32_e32 v109, vcc, 0, v95, vcc
	v_add_co_u32_e32 v112, vcc, s14, v94
	global_load_dwordx4 v[104:107], v[104:105], off
	s_nop 0
	v_addc_co_u32_e32 v113, vcc, 0, v95, vcc
	v_add_co_u32_e32 v116, vcc, s15, v94
	global_load_dwordx4 v[108:111], v[108:109], off
	s_nop 0
	v_addc_co_u32_e32 v117, vcc, 0, v95, vcc
	v_add_co_u32_e32 v120, vcc, s17, v94
	global_load_dwordx4 v[112:115], v[112:113], off
	s_nop 0
	v_addc_co_u32_e32 v121, vcc, 0, v95, vcc
	v_add_co_u32_e32 v124, vcc, s18, v94
	global_load_dwordx4 v[116:119], v[116:117], off
	s_nop 0
	v_addc_co_u32_e32 v125, vcc, 0, v95, vcc
	v_add_co_u32_e32 v128, vcc, s19, v94
	global_load_dwordx4 v[120:123], v[120:121], off
	s_nop 0
	v_addc_co_u32_e32 v129, vcc, 0, v95, vcc
	global_load_dwordx4 v[124:127], v[124:125], off
	v_add_co_u32_e32 v94, vcc, s20, v94
	global_load_dwordx4 v[128:131], v[128:129], off
	s_nop 0
	v_addc_co_u32_e32 v95, vcc, 0, v95, vcc
	global_load_dwordx4 v[132:135], v[94:95], off
	s_waitcnt vmcnt(10)
	v_pk_add_f32 v[54:55], v[54:55], 0 op_sel_hi:[1,0]
	v_pk_add_f32 v[52:53], v[52:53], 0 op_sel_hi:[1,0]
	s_waitcnt vmcnt(9)
	v_pk_add_f32 v[54:55], v[54:55], v[98:99]
	v_pk_add_f32 v[52:53], v[52:53], v[96:97]
	s_waitcnt vmcnt(8)
	v_pk_add_f32 v[54:55], v[54:55], v[102:103]
	v_pk_add_f32 v[52:53], v[52:53], v[100:101]
	s_waitcnt vmcnt(7)
	v_pk_add_f32 v[54:55], v[54:55], v[106:107]
	v_pk_add_f32 v[52:53], v[52:53], v[104:105]
	s_waitcnt vmcnt(6)
	v_pk_add_f32 v[54:55], v[54:55], v[110:111]
	v_pk_add_f32 v[52:53], v[52:53], v[108:109]
	s_waitcnt vmcnt(5)
	v_pk_add_f32 v[54:55], v[54:55], v[114:115]
	v_pk_add_f32 v[52:53], v[52:53], v[112:113]
	s_waitcnt vmcnt(4)
	v_pk_add_f32 v[54:55], v[54:55], v[118:119]
	v_pk_add_f32 v[52:53], v[52:53], v[116:117]
	s_waitcnt vmcnt(3)
	v_pk_add_f32 v[54:55], v[54:55], v[122:123]
	v_pk_add_f32 v[52:53], v[52:53], v[120:121]
	s_waitcnt vmcnt(2)
	v_pk_add_f32 v[54:55], v[54:55], v[126:127]
	v_pk_add_f32 v[52:53], v[52:53], v[124:125]
	s_waitcnt vmcnt(1)
	v_pk_add_f32 v[54:55], v[54:55], v[130:131]
	v_pk_add_f32 v[52:53], v[52:53], v[128:129]
	s_waitcnt vmcnt(0)
	v_pk_add_f32 v[96:97], v[54:55], v[134:135]
	v_pk_add_f32 v[94:95], v[52:53], v[132:133]
	v_mov_b32_e32 v134, v1
	s_waitcnt vmcnt(0)
	v_pk_fma_f32 v[78:79], v[96:97], v[250:251], v[78:79]
	v_pk_fma_f32 v[80:81], v[94:95], v[248:249], v[80:81]
	v_cvt_pk_bf16_f32 v52, v84, v85
	v_cvt_pk_bf16_f32 v53, v82, v83
	v_lshl_add_u64 v[82:83], v[56:57], 0, s[2:3]
	global_store_dwordx2 v[82:83], v[52:53], off
	v_lshlrev_b32_e32 v94, 16, v52
	v_and_b32_e32 v95, 0xffff0000, v52
	v_lshlrev_b32_e32 v84, 16, v53
	v_and_b32_e32 v85, 0xffff0000, v53
	v_cvt_pk_bf16_f32 v52, v88, v89
	v_cvt_pk_bf16_f32 v53, v86, v87
	v_cvt_pk_bf16_f32 v54, v92, v93
	v_cvt_pk_bf16_f32 v55, v90, v91
	v_cvt_pk_bf16_f32 v90, v80, v81
	v_cvt_pk_bf16_f32 v91, v78, v79
	global_store_dwordx2 v[82:83], v[52:53], off offset:512
	v_lshlrev_b32_e32 v88, 16, v52
	v_and_b32_e32 v89, 0xffff0000, v52
	v_lshlrev_b32_e32 v86, 16, v53
	v_and_b32_e32 v87, 0xffff0000, v53
	global_store_dwordx2 v[82:83], v[54:55], off offset:1024
	v_lshlrev_b32_e32 v52, 16, v54
	v_and_b32_e32 v53, 0xffff0000, v54
	v_lshlrev_b32_e32 v54, 16, v55
	v_and_b32_e32 v55, 0xffff0000, v55
	v_lshlrev_b32_e32 v80, 16, v90
	v_and_b32_e32 v81, 0xffff0000, v90
	v_lshlrev_b32_e32 v78, 16, v91
	v_and_b32_e32 v79, 0xffff0000, v91
	global_store_dwordx2 v[82:83], v[90:91], off offset:1536
	s_branch .LBB0_1245

.LBB0_2032:
	s_add_i32 s8, s88, s80
	s_cmp_lt_i32 s8, s31
	s_cselect_b64 s[12:13], -1, 0
	s_and_b64 s[0:1], s[12:13], exec
	s_cselect_b32 s0, s8, s80
	s_ashr_i32 s1, s0, 31
	s_lshl_b64 s[0:1], s[0:1], 11
	v_lshl_add_u64 v[4:5], v[54:55], 0, s[0:1]
	v_readlane_b32 s0, v254, 8
	s_add_i32 s18, s0, s80
	s_cmp_lt_i32 s18, s31
	s_cselect_b64 s[2:3], -1, 0
	s_and_b64 s[0:1], s[2:3], exec
	s_cselect_b32 s0, s18, s80
	s_ashr_i32 s1, s0, 31
	s_lshl_b64 s[0:1], s[0:1], 11
	global_load_dwordx2 v[106:107], v[4:5], off
	global_load_dwordx2 v[104:105], v[4:5], off offset:512
	global_load_dwordx2 v[102:103], v[4:5], off offset:1024
	global_load_dwordx2 v[100:101], v[4:5], off offset:1536
	v_lshl_add_u64 v[4:5], v[54:55], 0, s[0:1]
	v_readlane_b32 s0, v255, 10
	s_add_i32 s56, s0, s80
	s_cmp_lt_i32 s56, s31
	s_mov_b32 s0, 0xfbc00000
	s_cselect_b64 s[58:59], -1, 0
	global_load_dwordx2 v[98:99], v[4:5], off
	global_load_dwordx2 v[96:97], v[4:5], off offset:512
	global_load_dwordx2 v[94:95], v[4:5], off offset:1024
	global_load_dwordx2 v[92:93], v[4:5], off offset:1536
	v_add_co_u32_e32 v4, vcc, s0, v74
	s_and_b64 s[0:1], s[58:59], exec
	s_cselect_b32 s0, s56, s80
	s_ashr_i32 s1, s0, 31
	v_addc_co_u32_e32 v5, vcc, -1, v75, vcc
	s_lshl_b64 s[0:1], s[0:1], 11
	global_load_dwordx2 v[110:111], v[4:5], off
	global_load_dwordx2 v[108:109], v[4:5], off offset:-512
	global_load_dwordx2 v[116:117], v[4:5], off offset:-1024
	global_load_dwordx2 v[112:113], v[4:5], off offset:-1536
	v_lshl_add_u64 v[4:5], v[54:55], 0, s[0:1]
	v_readlane_b32 s0, v255, 18
	s_add_i32 s52, s0, s80
	s_cmp_lt_i32 s52, s31
	v_readlane_b32 s1, v255, 19
	s_cselect_b64 s[54:55], -1, 0
	s_and_b64 s[0:1], s[54:55], exec
	s_cselect_b32 s0, s52, s80
	s_ashr_i32 s1, s0, 31
	s_lshl_b64 s[0:1], s[0:1], 11
	global_load_dwordx2 v[90:91], v[4:5], off
	global_load_dwordx2 v[88:89], v[4:5], off offset:512
	global_load_dwordx2 v[86:87], v[4:5], off offset:1024
	global_load_dwordx2 v[84:85], v[4:5], off offset:1536
	v_lshl_add_u64 v[4:5], v[54:55], 0, s[0:1]
	global_load_dwordx2 v[82:83], v[4:5], off
	global_load_dwordx2 v[80:81], v[4:5], off offset:512
	global_load_dwordx2 v[78:79], v[4:5], off offset:1024
	global_load_dwordx2 v[76:77], v[4:5], off offset:1536
	s_min_i32 s0, s80, 0x4000
	s_and_b32 s0, s0, 0xfffff000
	s_add_i32 s0, s0, 0
	s_add_i32 s1, s0, 0xa000
	s_waitcnt vmcnt(23)
	v_add_u32_e32 v12, s1, v56
	v_add_u32_e32 v2, s0, v56
	ds_read_b128 v[44:47], v53 offset:40960
	ds_read_b128 v[32:35], v53 offset:41984
	ds_read_b128 v[40:43], v2 offset:45056
	ds_read_b128 v[28:31], v2 offset:46080
	ds_read_b128 v[48:51], v12 offset:24576
	ds_read_b128 v[36:39], v12 offset:25600
	s_waitcnt vmcnt(21)
	ds_read_b128 v[20:23], v53 offset:43008
	ds_read_b128 v[8:11], v53 offset:44032
	ds_read_b128 v[16:19], v2 offset:47104
	ds_read_b128 v[4:7], v2 offset:48128
	s_waitcnt vmcnt(20)
	ds_read_b128 v[24:27], v12 offset:26624
	ds_read_b128 v[12:15], v12 offset:27648
	s_cmpk_lt_i32 s80, 0x4000
	v_readlane_b32 s10, v255, 53
	s_cselect_b64 s[0:1], -1, 0
	v_readlane_b32 s11, v255, 54
	s_or_b64 s[0:1], s[10:11], s[0:1]
	s_and_b64 vcc, exec, s[0:1]
	s_waitcnt vmcnt(10)
	v_lshlrev_b32_e32 v118, 16, v109
	s_waitcnt vmcnt(9)
	v_lshlrev_b32_e32 v122, 16, v116
	s_waitcnt vmcnt(8)
	v_lshlrev_b32_e32 v114, 16, v112
	v_and_b32_e32 v115, 0xffff0000, v112
	v_lshlrev_b32_e32 v112, 16, v113
	v_and_b32_e32 v113, 0xffff0000, v113
	v_and_b32_e32 v123, 0xffff0000, v116
	v_lshlrev_b32_e32 v120, 16, v117
	v_and_b32_e32 v121, 0xffff0000, v117
	v_lshlrev_b32_e32 v116, 16, v108
	v_and_b32_e32 v117, 0xffff0000, v108
	v_and_b32_e32 v119, 0xffff0000, v109
	v_lshlrev_b32_e32 v108, 16, v110
	v_and_b32_e32 v109, 0xffff0000, v110
	v_lshlrev_b32_e32 v110, 16, v111
	v_and_b32_e32 v111, 0xffff0000, v111
	s_cbranch_vccnz .LBB0_2034
	global_load_dwordx4 v[236:239], v[60:61], off
	global_load_dwordx4 v[240:243], v[64:65], off
	global_load_dwordx4 v[244:247], v[68:69], off
	global_load_dwordx4 v[248:251], v[72:73], off
	s_mov_b32 s51, s81
	s_lshl_b64 s[0:1], s[80:81], 11
	s_lshl_b64 s[10:11], s[50:51], 2
	s_add_u32 s9, s6, s10
	s_addc_u32 s11, s7, s11
	s_add_u32 s10, s9, 0x420f8000
	s_addc_u32 s11, s11, 0
	v_lshlrev_b32_e32 v2, 4, v52
	v_lshl_add_u64 v[132:133], s[10:11], 0, v[2:3]
	s_mov_b32 s9, 0x400000
	v_add_co_u32_e32 v124, vcc, s9, v132
	s_mov_b32 s14, 0x800000
	s_nop 0
	v_addc_co_u32_e32 v125, vcc, 0, v133, vcc
	v_add_co_u32_e32 v128, vcc, s14, v132
	s_mov_b32 s15, 0xc00000
	s_nop 0
	v_addc_co_u32_e32 v129, vcc, 0, v133, vcc
	v_add_co_u32_e32 v132, vcc, s15, v132
	global_load_dwordx4 v[124:127], v[124:125], off
	s_nop 0
	v_addc_co_u32_e32 v133, vcc, 0, v133, vcc
	global_load_dwordx4 v[128:131], v[128:129], off
	v_mov_b32_e32 v57, v134
	global_load_dwordx4 v[132:135], v[132:133], off
	s_nop 0
	global_load_dwordx4 v[136:139], v2, s[10:11]
	v_lshlrev_b32_e32 v2, 4, v62
	s_waitcnt vmcnt(0)
	v_pk_add_f32 v[138:139], v[138:139], 0 op_sel_hi:[1,0]
	v_pk_add_f32 v[136:137], v[136:137], 0 op_sel_hi:[1,0]
	v_pk_add_f32 v[126:127], v[126:127], v[138:139]
	v_pk_add_f32 v[124:125], v[124:125], v[136:137]
	v_pk_add_f32 v[126:127], v[130:131], v[126:127]
	v_pk_add_f32 v[124:125], v[128:129], v[124:125]
	v_pk_add_f32 v[128:129], v[134:135], v[126:127]
	v_pk_add_f32 v[130:131], v[132:133], v[124:125]
	v_lshl_add_u64 v[132:133], s[10:11], 0, v[2:3]
	s_waitcnt vmcnt(0)
	v_pk_fma_f32 v[114:115], v[236:237], v[130:131], v[114:115]
	v_add_co_u32_e32 v124, vcc, s9, v132
	v_pk_fma_f32 v[112:113], v[238:239], v[128:129], v[112:113]
	s_nop 0
	v_addc_co_u32_e32 v125, vcc, 0, v133, vcc
	v_add_co_u32_e32 v128, vcc, s14, v132
	global_load_dwordx4 v[124:127], v[124:125], off
	s_nop 0
	v_addc_co_u32_e32 v129, vcc, 0, v133, vcc
	v_add_co_u32_e32 v132, vcc, s15, v132
	global_load_dwordx4 v[128:131], v[128:129], off
	s_nop 0
	v_addc_co_u32_e32 v133, vcc, 0, v133, vcc
	global_load_dwordx4 v[132:135], v[132:133], off
	s_nop 0
	global_load_dwordx4 v[136:139], v2, s[10:11]
	v_lshlrev_b32_e32 v2, 4, v66
	s_waitcnt vmcnt(0)
	v_pk_add_f32 v[138:139], v[138:139], 0 op_sel_hi:[1,0]
	v_pk_add_f32 v[136:137], v[136:137], 0 op_sel_hi:[1,0]
	v_pk_add_f32 v[126:127], v[126:127], v[138:139]
	v_pk_add_f32 v[124:125], v[124:125], v[136:137]
	v_pk_add_f32 v[126:127], v[130:131], v[126:127]
	v_pk_add_f32 v[124:125], v[128:129], v[124:125]
	v_pk_add_f32 v[128:129], v[134:135], v[126:127]
	v_pk_add_f32 v[130:131], v[132:133], v[124:125]
	v_lshl_add_u64 v[132:133], s[10:11], 0, v[2:3]
	s_waitcnt vmcnt(0)
	v_pk_fma_f32 v[122:123], v[240:241], v[130:131], v[122:123]
	v_add_co_u32_e32 v124, vcc, s9, v132
	v_pk_fma_f32 v[120:121], v[242:243], v[128:129], v[120:121]
	s_nop 0
	v_addc_co_u32_e32 v125, vcc, 0, v133, vcc
	v_add_co_u32_e32 v128, vcc, s14, v132
	global_load_dwordx4 v[124:127], v[124:125], off
	s_nop 0
	v_addc_co_u32_e32 v129, vcc, 0, v133, vcc
	v_add_co_u32_e32 v132, vcc, s15, v132
	global_load_dwordx4 v[128:131], v[128:129], off
	s_nop 0
	v_addc_co_u32_e32 v133, vcc, 0, v133, vcc
	global_load_dwordx4 v[132:135], v[132:133], off
	s_nop 0
	global_load_dwordx4 v[136:139], v2, s[10:11]
	v_lshlrev_b32_e32 v2, 4, v70
	s_waitcnt vmcnt(0)
	v_pk_add_f32 v[138:139], v[138:139], 0 op_sel_hi:[1,0]
	v_pk_add_f32 v[136:137], v[136:137], 0 op_sel_hi:[1,0]
	v_pk_add_f32 v[126:127], v[126:127], v[138:139]
	v_pk_add_f32 v[124:125], v[124:125], v[136:137]
	v_pk_add_f32 v[126:127], v[130:131], v[126:127]
	v_pk_add_f32 v[124:125], v[128:129], v[124:125]
	v_pk_add_f32 v[128:129], v[134:135], v[126:127]
	v_pk_add_f32 v[130:131], v[132:133], v[124:125]
	v_lshl_add_u64 v[132:133], s[10:11], 0, v[2:3]
	s_waitcnt vmcnt(0)
	v_pk_fma_f32 v[116:117], v[244:245], v[130:131], v[116:117]
	v_add_co_u32_e32 v124, vcc, s9, v132
	v_pk_fma_f32 v[118:119], v[246:247], v[128:129], v[118:119]
	s_nop 0
	v_addc_co_u32_e32 v125, vcc, 0, v133, vcc
	v_add_co_u32_e32 v128, vcc, s14, v132
	global_load_dwordx4 v[124:127], v[124:125], off
	s_nop 0
	v_addc_co_u32_e32 v129, vcc, 0, v133, vcc
	v_add_co_u32_e32 v132, vcc, s15, v132
	global_load_dwordx4 v[128:131], v[128:129], off
	s_nop 0
	v_addc_co_u32_e32 v133, vcc, 0, v133, vcc
	global_load_dwordx4 v[132:135], v[132:133], off
	s_nop 0
	global_load_dwordx4 v[136:139], v2, s[10:11]
	s_waitcnt vmcnt(0)
	v_pk_add_f32 v[138:139], v[138:139], 0 op_sel_hi:[1,0]
	v_pk_add_f32 v[136:137], v[136:137], 0 op_sel_hi:[1,0]
	v_pk_add_f32 v[126:127], v[126:127], v[138:139]
	v_pk_add_f32 v[124:125], v[124:125], v[136:137]
	v_pk_add_f32 v[126:127], v[130:131], v[126:127]
	v_pk_add_f32 v[124:125], v[128:129], v[124:125]
	v_pk_add_f32 v[128:129], v[134:135], v[126:127]
	v_pk_add_f32 v[130:131], v[132:133], v[124:125]
	v_mov_b32_e32 v134, v57
	s_waitcnt vmcnt(0)
	v_pk_fma_f32 v[110:111], v[250:251], v[128:129], v[110:111]
	v_pk_fma_f32 v[108:109], v[248:249], v[130:131], v[108:109]
	v_cvt_pk_bf16_f32 v124, v114, v115
	v_cvt_pk_bf16_f32 v125, v112, v113
	v_lshl_add_u64 v[126:127], v[54:55], 0, s[0:1]
	global_store_dwordx2 v[126:127], v[124:125], off
	v_lshlrev_b32_e32 v114, 16, v124
	v_and_b32_e32 v115, 0xffff0000, v124
	v_lshlrev_b32_e32 v112, 16, v125
	v_and_b32_e32 v113, 0xffff0000, v125
	v_cvt_pk_bf16_f32 v124, v122, v123
	v_cvt_pk_bf16_f32 v125, v120, v121
	global_store_dwordx2 v[126:127], v[124:125], off offset:512
	v_lshlrev_b32_e32 v122, 16, v124
	v_and_b32_e32 v123, 0xffff0000, v124
	v_lshlrev_b32_e32 v120, 16, v125
	v_and_b32_e32 v121, 0xffff0000, v125
	v_cvt_pk_bf16_f32 v124, v116, v117
	v_cvt_pk_bf16_f32 v125, v118, v119
	global_store_dwordx2 v[126:127], v[124:125], off offset:1024
	v_lshlrev_b32_e32 v116, 16, v124
	v_and_b32_e32 v117, 0xffff0000, v124
	v_lshlrev_b32_e32 v118, 16, v125
	v_and_b32_e32 v119, 0xffff0000, v125
	v_cvt_pk_bf16_f32 v124, v108, v109
	v_cvt_pk_bf16_f32 v125, v110, v111
	v_lshlrev_b32_e32 v108, 16, v124
	v_and_b32_e32 v109, 0xffff0000, v124
	v_lshlrev_b32_e32 v110, 16, v125
	v_and_b32_e32 v111, 0xffff0000, v125
	global_store_dwordx2 v[126:127], v[124:125], off offset:1536
	s_branch .LBB0_2035

.LBB0_2040:
	s_min_i32 s0, s52, 0x4000
	s_and_b32 s0, s0, 0xfffff000
	s_add_i32 s0, s0, 0
	s_add_i32 s1, s0, 0xa000
	v_add_u32_e32 v12, s1, v56
	v_add_u32_e32 v2, s0, v56
	ds_read_b128 v[44:47], v53 offset:40960
	ds_read_b128 v[32:35], v53 offset:41984
	ds_read_b128 v[40:43], v2 offset:45056
	ds_read_b128 v[28:31], v2 offset:46080
	ds_read_b128 v[48:51], v12 offset:24576
	ds_read_b128 v[36:39], v12 offset:25600
	ds_read_b128 v[20:23], v53 offset:43008
	ds_read_b128 v[8:11], v53 offset:44032
	ds_read_b128 v[16:19], v2 offset:47104
	ds_read_b128 v[4:7], v2 offset:48128
	ds_read_b128 v[24:27], v12 offset:26624
	ds_read_b128 v[12:15], v12 offset:27648
	s_cmpk_lt_i32 s52, 0x4000
	v_readlane_b32 s2, v255, 53
	s_cselect_b64 s[0:1], -1, 0
	v_readlane_b32 s3, v255, 54
	s_or_b64 s[0:1], s[2:3], s[0:1]
	s_waitcnt vmcnt(7)
	v_lshlrev_b32_e32 v92, 16, v82
	v_and_b32_e32 v93, 0xffff0000, v82
	v_lshlrev_b32_e32 v82, 16, v83
	v_and_b32_e32 v83, 0xffff0000, v83
	s_waitcnt vmcnt(6)
	v_lshlrev_b32_e32 v90, 16, v80
	v_and_b32_e32 v91, 0xffff0000, v80
	v_lshlrev_b32_e32 v88, 16, v81
	v_and_b32_e32 v89, 0xffff0000, v81
	s_waitcnt vmcnt(5)
	v_lshlrev_b32_e32 v84, 16, v78
	v_and_b32_e32 v85, 0xffff0000, v78
	v_lshlrev_b32_e32 v86, 16, v79
	v_and_b32_e32 v87, 0xffff0000, v79
	s_waitcnt vmcnt(4)
	v_lshlrev_b32_e32 v78, 16, v76
	v_and_b32_e32 v79, 0xffff0000, v76
	v_lshlrev_b32_e32 v76, 16, v77
	v_and_b32_e32 v77, 0xffff0000, v77
	s_and_b64 vcc, exec, s[0:1]
	s_cbranch_vccnz .LBB0_2042
	global_load_dwordx4 v[236:239], v[60:61], off
	global_load_dwordx4 v[240:243], v[64:65], off
	global_load_dwordx4 v[244:247], v[68:69], off
	global_load_dwordx4 v[248:251], v[72:73], off
	v_readlane_b32 s2, v255, 14
	s_mov_b32 s53, s81
	s_add_i32 s2, s2, s50
	s_mov_b32 s3, s81
	s_lshl_b64 s[0:1], s[52:53], 11
	s_lshl_b64 s[2:3], s[2:3], 2
	s_add_u32 s2, s6, s2
	s_addc_u32 s3, s7, s3
	s_add_u32 s2, s2, 0x420f8000
	s_addc_u32 s3, s3, 0
	v_lshlrev_b32_e32 v2, 4, v52
	v_lshl_add_u64 v[80:81], s[2:3], 0, v[2:3]
	s_mov_b32 s9, 0x400000
	v_add_co_u32_e32 v94, vcc, s9, v80
	s_mov_b32 s8, 0x800000
	s_nop 0
	v_addc_co_u32_e32 v95, vcc, 0, v81, vcc
	v_add_co_u32_e32 v98, vcc, s8, v80
	s_mov_b32 s10, 0xc00000
	s_nop 0
	v_addc_co_u32_e32 v99, vcc, 0, v81, vcc
	v_add_co_u32_e32 v80, vcc, s10, v80
	global_load_dwordx4 v[94:97], v[94:95], off
	s_nop 0
	v_addc_co_u32_e32 v81, vcc, 0, v81, vcc
	global_load_dwordx4 v[98:101], v[98:99], off
	s_nop 0
	global_load_dwordx4 v[102:105], v[80:81], off
	global_load_dwordx4 v[106:109], v2, s[2:3]
	v_lshlrev_b32_e32 v2, 4, v62
	s_waitcnt vmcnt(0)
	v_pk_add_f32 v[106:107], v[106:107], 0 op_sel_hi:[1,0]
	s_nop 0
	v_pk_add_f32 v[94:95], v[94:95], v[106:107]
	v_pk_add_f32 v[80:81], v[108:109], 0 op_sel_hi:[1,0]
	v_pk_add_f32 v[94:95], v[98:99], v[94:95]
	v_pk_add_f32 v[80:81], v[96:97], v[80:81]
	v_pk_add_f32 v[98:99], v[102:103], v[94:95]
	v_pk_add_f32 v[80:81], v[100:101], v[80:81]
	v_lshl_add_u64 v[100:101], s[2:3], 0, v[2:3]
	v_pk_add_f32 v[80:81], v[104:105], v[80:81]
	s_waitcnt vmcnt(0)
	v_pk_fma_f32 v[80:81], v[238:239], v[80:81], v[82:83]
	v_pk_fma_f32 v[82:83], v[236:237], v[98:99], v[92:93]
	v_add_co_u32_e32 v92, vcc, s9, v100
	v_cvt_pk_bf16_f32 v82, v82, v83
	s_nop 0
	v_addc_co_u32_e32 v93, vcc, 0, v101, vcc
	v_add_co_u32_e32 v96, vcc, s8, v100
	global_load_dwordx4 v[92:95], v[92:93], off
	s_nop 0
	v_addc_co_u32_e32 v97, vcc, 0, v101, vcc
	v_add_co_u32_e32 v100, vcc, s10, v100
	global_load_dwordx4 v[96:99], v[96:97], off
	s_nop 0
	v_addc_co_u32_e32 v101, vcc, 0, v101, vcc
	global_load_dwordx4 v[100:103], v[100:101], off
	s_nop 0
	global_load_dwordx4 v[104:107], v2, s[2:3]
	v_lshlrev_b32_e32 v2, 4, v66
	v_cvt_pk_bf16_f32 v83, v80, v81
	v_lshl_add_u64 v[80:81], v[54:55], 0, s[0:1]
	s_waitcnt vmcnt(0)
	v_pk_add_f32 v[106:107], v[106:107], 0 op_sel_hi:[1,0]
	v_pk_add_f32 v[104:105], v[104:105], 0 op_sel_hi:[1,0]
	v_pk_add_f32 v[94:95], v[94:95], v[106:107]
	v_pk_add_f32 v[92:93], v[92:93], v[104:105]
	v_pk_add_f32 v[94:95], v[98:99], v[94:95]
	v_pk_add_f32 v[92:93], v[96:97], v[92:93]
	v_pk_add_f32 v[96:97], v[102:103], v[94:95]
	v_pk_add_f32 v[98:99], v[100:101], v[92:93]
	v_lshl_add_u64 v[100:101], s[2:3], 0, v[2:3]
	s_waitcnt vmcnt(0)
	v_pk_fma_f32 v[90:91], v[240:241], v[98:99], v[90:91]
	v_add_co_u32_e32 v92, vcc, s9, v100
	v_pk_fma_f32 v[88:89], v[242:243], v[96:97], v[88:89]
	s_nop 0
	v_addc_co_u32_e32 v93, vcc, 0, v101, vcc
	v_add_co_u32_e32 v96, vcc, s8, v100
	global_load_dwordx4 v[92:95], v[92:93], off
	s_nop 0
	v_addc_co_u32_e32 v97, vcc, 0, v101, vcc
	v_add_co_u32_e32 v100, vcc, s10, v100
	global_load_dwordx4 v[96:99], v[96:97], off
	s_nop 0
	v_addc_co_u32_e32 v101, vcc, 0, v101, vcc
	global_load_dwordx4 v[100:103], v[100:101], off
	s_nop 0
	global_load_dwordx4 v[104:107], v2, s[2:3]
	v_lshlrev_b32_e32 v2, 4, v70
	s_waitcnt vmcnt(0)
	v_pk_add_f32 v[106:107], v[106:107], 0 op_sel_hi:[1,0]
	v_pk_add_f32 v[104:105], v[104:105], 0 op_sel_hi:[1,0]
	v_pk_add_f32 v[94:95], v[94:95], v[106:107]
	v_pk_add_f32 v[92:93], v[92:93], v[104:105]
	v_pk_add_f32 v[94:95], v[98:99], v[94:95]
	v_pk_add_f32 v[92:93], v[96:97], v[92:93]
	v_pk_add_f32 v[96:97], v[102:103], v[94:95]
	v_pk_add_f32 v[98:99], v[100:101], v[92:93]
	v_lshl_add_u64 v[100:101], s[2:3], 0, v[2:3]
	s_waitcnt vmcnt(0)
	v_pk_fma_f32 v[84:85], v[244:245], v[98:99], v[84:85]
	v_add_co_u32_e32 v92, vcc, s9, v100
	v_pk_fma_f32 v[86:87], v[246:247], v[96:97], v[86:87]
	s_nop 0
	v_addc_co_u32_e32 v93, vcc, 0, v101, vcc
	v_add_co_u32_e32 v96, vcc, s8, v100
	global_load_dwordx4 v[92:95], v[92:93], off
	s_nop 0
	v_addc_co_u32_e32 v97, vcc, 0, v101, vcc
	v_add_co_u32_e32 v100, vcc, s10, v100
	global_load_dwordx4 v[96:99], v[96:97], off
	s_nop 0
	v_addc_co_u32_e32 v101, vcc, 0, v101, vcc
	global_load_dwordx4 v[100:103], v[100:101], off
	s_nop 0
	global_load_dwordx4 v[104:107], v2, s[2:3]
	s_waitcnt vmcnt(0)
	v_pk_add_f32 v[106:107], v[106:107], 0 op_sel_hi:[1,0]
	v_pk_add_f32 v[104:105], v[104:105], 0 op_sel_hi:[1,0]
	v_pk_add_f32 v[94:95], v[94:95], v[106:107]
	v_pk_add_f32 v[92:93], v[92:93], v[104:105]
	v_pk_add_f32 v[94:95], v[98:99], v[94:95]
	v_pk_add_f32 v[92:93], v[96:97], v[92:93]
	v_pk_add_f32 v[96:97], v[102:103], v[94:95]
	v_pk_add_f32 v[98:99], v[100:101], v[92:93]
	s_waitcnt vmcnt(0)
	v_pk_fma_f32 v[76:77], v[250:251], v[96:97], v[76:77]
	v_cvt_pk_bf16_f32 v94, v90, v91
	v_cvt_pk_bf16_f32 v95, v88, v89
	v_pk_fma_f32 v[78:79], v[248:249], v[98:99], v[78:79]
	global_store_dwordx2 v[80:81], v[94:95], off offset:512
	v_lshlrev_b32_e32 v90, 16, v94
	v_and_b32_e32 v91, 0xffff0000, v94
	v_lshlrev_b32_e32 v88, 16, v95
	v_and_b32_e32 v89, 0xffff0000, v95
	v_cvt_pk_bf16_f32 v94, v84, v85
	v_cvt_pk_bf16_f32 v95, v86, v87
	global_store_dwordx2 v[80:81], v[94:95], off offset:1024
	v_lshlrev_b32_e32 v84, 16, v94
	v_and_b32_e32 v85, 0xffff0000, v94
	v_lshlrev_b32_e32 v86, 16, v95
	v_and_b32_e32 v87, 0xffff0000, v95
	v_cvt_pk_bf16_f32 v94, v78, v79
	v_cvt_pk_bf16_f32 v95, v76, v77
	global_store_dwordx2 v[80:81], v[82:83], off
	v_lshlrev_b32_e32 v92, 16, v82
	v_and_b32_e32 v93, 0xffff0000, v82
	v_lshlrev_b32_e32 v82, 16, v83
	v_and_b32_e32 v83, 0xffff0000, v83
	v_lshlrev_b32_e32 v78, 16, v94
	v_and_b32_e32 v79, 0xffff0000, v94
	v_lshlrev_b32_e32 v76, 16, v95
	v_and_b32_e32 v77, 0xffff0000, v95
	global_store_dwordx2 v[80:81], v[94:95], off offset:1536

.LBB0_2053:
	s_min_i32 s0, s8, 0x4000
	s_and_b32 s0, s0, 0xfffff000
	s_add_i32 s0, s0, 0
	s_add_i32 s1, s0, 0xa000
	v_add_u32_e32 v12, s1, v56
	v_add_u32_e32 v2, s0, v56
	ds_read_b128 v[44:47], v53 offset:40960
	ds_read_b128 v[32:35], v53 offset:41984
	ds_read_b128 v[40:43], v2 offset:45056
	ds_read_b128 v[28:31], v2 offset:46080
	ds_read_b128 v[48:51], v12 offset:24576
	ds_read_b128 v[36:39], v12 offset:25600
	ds_read_b128 v[20:23], v53 offset:43008
	ds_read_b128 v[8:11], v53 offset:44032
	ds_read_b128 v[16:19], v2 offset:47104
	ds_read_b128 v[4:7], v2 offset:48128
	ds_read_b128 v[24:27], v12 offset:26624
	ds_read_b128 v[12:15], v12 offset:27648
	s_cmpk_lt_i32 s8, 0x4000
	v_readlane_b32 s10, v255, 53
	s_cselect_b64 s[0:1], -1, 0
	v_readlane_b32 s11, v255, 54
	s_or_b64 s[0:1], s[10:11], s[0:1]
	v_lshlrev_b32_e32 v116, 16, v106
	v_and_b32_e32 v117, 0xffff0000, v106
	v_lshlrev_b32_e32 v106, 16, v107
	v_and_b32_e32 v107, 0xffff0000, v107
	v_lshlrev_b32_e32 v114, 16, v104
	v_and_b32_e32 v115, 0xffff0000, v104
	v_lshlrev_b32_e32 v112, 16, v105
	v_and_b32_e32 v113, 0xffff0000, v105
	v_lshlrev_b32_e32 v108, 16, v102
	v_and_b32_e32 v109, 0xffff0000, v102
	v_lshlrev_b32_e32 v110, 16, v103
	v_and_b32_e32 v111, 0xffff0000, v103
	v_lshlrev_b32_e32 v102, 16, v100
	v_and_b32_e32 v103, 0xffff0000, v100
	v_lshlrev_b32_e32 v100, 16, v101
	v_and_b32_e32 v101, 0xffff0000, v101
	s_and_b64 vcc, exec, s[0:1]
	s_cbranch_vccnz .LBB0_2055
	global_load_dwordx4 v[236:239], v[60:61], off
	global_load_dwordx4 v[240:243], v[64:65], off
	global_load_dwordx4 v[244:247], v[68:69], off
	global_load_dwordx4 v[248:251], v[72:73], off
	s_mov_b32 s9, s81
	s_lshl_b64 s[0:1], s[8:9], 11
	v_readlane_b32 s9, v255, 15
	s_add_i32 s10, s9, s50
	s_mov_b32 s11, s81
	s_lshl_b64 s[10:11], s[10:11], 2
	s_add_u32 s9, s6, s10
	s_addc_u32 s11, s7, s11
	s_add_u32 s10, s9, 0x420f8000
	s_addc_u32 s11, s11, 0
	v_lshlrev_b32_e32 v2, 4, v52
	v_lshl_add_u64 v[104:105], s[10:11], 0, v[2:3]
	s_mov_b32 s12, 0x400000
	v_add_co_u32_e32 v118, vcc, s12, v104
	s_mov_b32 s9, 0x800000
	s_nop 0
	v_addc_co_u32_e32 v119, vcc, 0, v105, vcc
	v_add_co_u32_e32 v122, vcc, s9, v104
	s_mov_b32 s13, 0xc00000
	s_nop 0
	v_addc_co_u32_e32 v123, vcc, 0, v105, vcc
	v_add_co_u32_e32 v104, vcc, s13, v104
	global_load_dwordx4 v[118:121], v[118:119], off
	s_nop 0
	v_addc_co_u32_e32 v105, vcc, 0, v105, vcc
	global_load_dwordx4 v[122:125], v[122:123], off
	s_nop 0
	global_load_dwordx4 v[126:129], v[104:105], off
	global_load_dwordx4 v[130:133], v2, s[10:11]
	v_lshlrev_b32_e32 v2, 4, v62
	s_waitcnt vmcnt(0)
	v_pk_add_f32 v[130:131], v[130:131], 0 op_sel_hi:[1,0]
	s_nop 0
	v_pk_add_f32 v[118:119], v[118:119], v[130:131]
	v_pk_add_f32 v[104:105], v[132:133], 0 op_sel_hi:[1,0]
	v_pk_add_f32 v[118:119], v[122:123], v[118:119]
	v_pk_add_f32 v[104:105], v[120:121], v[104:105]
	v_pk_add_f32 v[122:123], v[126:127], v[118:119]
	v_pk_add_f32 v[104:105], v[124:125], v[104:105]
	v_lshl_add_u64 v[124:125], s[10:11], 0, v[2:3]
	v_pk_add_f32 v[104:105], v[128:129], v[104:105]
	s_waitcnt vmcnt(0)
	v_pk_fma_f32 v[104:105], v[238:239], v[104:105], v[106:107]
	v_pk_fma_f32 v[106:107], v[236:237], v[122:123], v[116:117]
	v_add_co_u32_e32 v116, vcc, s12, v124
	v_cvt_pk_bf16_f32 v106, v106, v107
	s_nop 0
	v_addc_co_u32_e32 v117, vcc, 0, v125, vcc
	v_add_co_u32_e32 v120, vcc, s9, v124
	global_load_dwordx4 v[116:119], v[116:117], off
	s_nop 0
	v_addc_co_u32_e32 v121, vcc, 0, v125, vcc
	v_add_co_u32_e32 v124, vcc, s13, v124
	global_load_dwordx4 v[120:123], v[120:121], off
	s_nop 0
	v_addc_co_u32_e32 v125, vcc, 0, v125, vcc
	global_load_dwordx4 v[124:127], v[124:125], off
	s_nop 0
	global_load_dwordx4 v[128:131], v2, s[10:11]
	v_lshlrev_b32_e32 v2, 4, v66
	v_cvt_pk_bf16_f32 v107, v104, v105
	v_lshl_add_u64 v[104:105], v[54:55], 0, s[0:1]
	s_waitcnt vmcnt(0)
	v_pk_add_f32 v[130:131], v[130:131], 0 op_sel_hi:[1,0]
	v_pk_add_f32 v[128:129], v[128:129], 0 op_sel_hi:[1,0]
	v_pk_add_f32 v[118:119], v[118:119], v[130:131]
	v_pk_add_f32 v[116:117], v[116:117], v[128:129]
	v_pk_add_f32 v[118:119], v[122:123], v[118:119]
	v_pk_add_f32 v[116:117], v[120:121], v[116:117]
	v_pk_add_f32 v[120:121], v[126:127], v[118:119]
	v_pk_add_f32 v[122:123], v[124:125], v[116:117]
	v_lshl_add_u64 v[124:125], s[10:11], 0, v[2:3]
	s_waitcnt vmcnt(0)
	v_pk_fma_f32 v[114:115], v[240:241], v[122:123], v[114:115]
	v_add_co_u32_e32 v116, vcc, s12, v124
	v_pk_fma_f32 v[112:113], v[242:243], v[120:121], v[112:113]
	s_nop 0
	v_addc_co_u32_e32 v117, vcc, 0, v125, vcc
	v_add_co_u32_e32 v120, vcc, s9, v124
	global_load_dwordx4 v[116:119], v[116:117], off
	s_nop 0
	v_addc_co_u32_e32 v121, vcc, 0, v125, vcc
	v_add_co_u32_e32 v124, vcc, s13, v124
	global_load_dwordx4 v[120:123], v[120:121], off
	s_nop 0
	v_addc_co_u32_e32 v125, vcc, 0, v125, vcc
	global_load_dwordx4 v[124:127], v[124:125], off
	s_nop 0
	global_load_dwordx4 v[128:131], v2, s[10:11]
	v_lshlrev_b32_e32 v2, 4, v70
	s_waitcnt vmcnt(0)
	v_pk_add_f32 v[130:131], v[130:131], 0 op_sel_hi:[1,0]
	v_pk_add_f32 v[128:129], v[128:129], 0 op_sel_hi:[1,0]
	v_pk_add_f32 v[118:119], v[118:119], v[130:131]
	v_pk_add_f32 v[116:117], v[116:117], v[128:129]
	v_pk_add_f32 v[118:119], v[122:123], v[118:119]
	v_pk_add_f32 v[116:117], v[120:121], v[116:117]
	v_pk_add_f32 v[120:121], v[126:127], v[118:119]
	v_pk_add_f32 v[122:123], v[124:125], v[116:117]
	v_lshl_add_u64 v[124:125], s[10:11], 0, v[2:3]
	s_waitcnt vmcnt(0)
	v_pk_fma_f32 v[108:109], v[244:245], v[122:123], v[108:109]
	v_add_co_u32_e32 v116, vcc, s12, v124
	v_pk_fma_f32 v[110:111], v[246:247], v[120:121], v[110:111]
	s_nop 0
	v_addc_co_u32_e32 v117, vcc, 0, v125, vcc
	v_add_co_u32_e32 v120, vcc, s9, v124
	global_load_dwordx4 v[116:119], v[116:117], off
	s_nop 0
	v_addc_co_u32_e32 v121, vcc, 0, v125, vcc
	v_add_co_u32_e32 v124, vcc, s13, v124
	global_load_dwordx4 v[120:123], v[120:121], off
	s_nop 0
	v_addc_co_u32_e32 v125, vcc, 0, v125, vcc
	global_load_dwordx4 v[124:127], v[124:125], off
	s_nop 0
	global_load_dwordx4 v[128:131], v2, s[10:11]
	s_waitcnt vmcnt(0)
	v_pk_add_f32 v[130:131], v[130:131], 0 op_sel_hi:[1,0]
	v_pk_add_f32 v[128:129], v[128:129], 0 op_sel_hi:[1,0]
	v_pk_add_f32 v[118:119], v[118:119], v[130:131]
	v_pk_add_f32 v[116:117], v[116:117], v[128:129]
	v_pk_add_f32 v[118:119], v[122:123], v[118:119]
	v_pk_add_f32 v[116:117], v[120:121], v[116:117]
	v_pk_add_f32 v[120:121], v[126:127], v[118:119]
	v_pk_add_f32 v[122:123], v[124:125], v[116:117]
	s_waitcnt vmcnt(0)
	v_pk_fma_f32 v[100:101], v[250:251], v[120:121], v[100:101]
	v_cvt_pk_bf16_f32 v118, v114, v115
	v_cvt_pk_bf16_f32 v119, v112, v113
	v_pk_fma_f32 v[102:103], v[248:249], v[122:123], v[102:103]
	global_store_dwordx2 v[104:105], v[118:119], off offset:512
	v_lshlrev_b32_e32 v114, 16, v118
	v_and_b32_e32 v115, 0xffff0000, v118
	v_lshlrev_b32_e32 v112, 16, v119
	v_and_b32_e32 v113, 0xffff0000, v119
	v_cvt_pk_bf16_f32 v118, v108, v109
	v_cvt_pk_bf16_f32 v119, v110, v111
	global_store_dwordx2 v[104:105], v[118:119], off offset:1024
	v_lshlrev_b32_e32 v108, 16, v118
	v_and_b32_e32 v109, 0xffff0000, v118
	v_lshlrev_b32_e32 v110, 16, v119
	v_and_b32_e32 v111, 0xffff0000, v119
	v_cvt_pk_bf16_f32 v118, v102, v103
	v_cvt_pk_bf16_f32 v119, v100, v101
	global_store_dwordx2 v[104:105], v[106:107], off
	v_lshlrev_b32_e32 v116, 16, v106
	v_and_b32_e32 v117, 0xffff0000, v106
	v_lshlrev_b32_e32 v106, 16, v107
	v_and_b32_e32 v107, 0xffff0000, v107
	v_lshlrev_b32_e32 v102, 16, v118
	v_and_b32_e32 v103, 0xffff0000, v118
	v_lshlrev_b32_e32 v100, 16, v119
	v_and_b32_e32 v101, 0xffff0000, v119
	global_store_dwordx2 v[104:105], v[118:119], off offset:1536

.LBB0_2062:
	s_min_i32 s0, s18, 0x4000
	s_and_b32 s0, s0, 0xfffff000
	s_add_i32 s0, s0, 0
	s_add_i32 s1, s0, 0xa000
	v_add_u32_e32 v12, s1, v56
	v_add_u32_e32 v2, s0, v56
	ds_read_b128 v[44:47], v53 offset:40960
	ds_read_b128 v[32:35], v53 offset:41984
	ds_read_b128 v[40:43], v2 offset:45056
	ds_read_b128 v[28:31], v2 offset:46080
	ds_read_b128 v[48:51], v12 offset:24576
	ds_read_b128 v[36:39], v12 offset:25600
	ds_read_b128 v[20:23], v53 offset:43008
	ds_read_b128 v[8:11], v53 offset:44032
	ds_read_b128 v[16:19], v2 offset:47104
	ds_read_b128 v[4:7], v2 offset:48128
	ds_read_b128 v[24:27], v12 offset:26624
	ds_read_b128 v[12:15], v12 offset:27648
	s_cmpk_lt_i32 s18, 0x4000
	v_readlane_b32 s2, v255, 53
	s_cselect_b64 s[0:1], -1, 0
	v_readlane_b32 s3, v255, 54
	s_or_b64 s[0:1], s[2:3], s[0:1]
	v_lshlrev_b32_e32 v108, 16, v98
	v_and_b32_e32 v109, 0xffff0000, v98
	v_lshlrev_b32_e32 v98, 16, v99
	v_and_b32_e32 v99, 0xffff0000, v99
	v_lshlrev_b32_e32 v106, 16, v96
	v_and_b32_e32 v107, 0xffff0000, v96
	v_lshlrev_b32_e32 v104, 16, v97
	v_and_b32_e32 v105, 0xffff0000, v97
	v_lshlrev_b32_e32 v100, 16, v94
	v_and_b32_e32 v101, 0xffff0000, v94
	v_lshlrev_b32_e32 v102, 16, v95
	v_and_b32_e32 v103, 0xffff0000, v95
	v_lshlrev_b32_e32 v94, 16, v92
	v_and_b32_e32 v95, 0xffff0000, v92
	v_lshlrev_b32_e32 v92, 16, v93
	v_and_b32_e32 v93, 0xffff0000, v93
	s_and_b64 vcc, exec, s[0:1]
	s_cbranch_vccnz .LBB0_2064
	global_load_dwordx4 v[236:239], v[60:61], off
	global_load_dwordx4 v[240:243], v[64:65], off
	global_load_dwordx4 v[244:247], v[68:69], off
	global_load_dwordx4 v[248:251], v[72:73], off
	v_readlane_b32 s2, v255, 12
	s_mov_b32 s19, s81
	s_add_i32 s2, s2, s50
	s_mov_b32 s3, s81
	s_lshl_b64 s[0:1], s[18:19], 11
	s_lshl_b64 s[2:3], s[2:3], 2
	s_add_u32 s2, s6, s2
	s_addc_u32 s3, s7, s3
	s_add_u32 s2, s2, 0x420f8000
	s_addc_u32 s3, s3, 0
	v_lshlrev_b32_e32 v2, 4, v52
	v_lshl_add_u64 v[96:97], s[2:3], 0, v[2:3]
	s_mov_b32 s9, 0x400000
	v_add_co_u32_e32 v110, vcc, s9, v96
	s_mov_b32 s8, 0x800000
	s_nop 0
	v_addc_co_u32_e32 v111, vcc, 0, v97, vcc
	v_add_co_u32_e32 v114, vcc, s8, v96
	s_mov_b32 s10, 0xc00000
	s_nop 0
	v_addc_co_u32_e32 v115, vcc, 0, v97, vcc
	v_add_co_u32_e32 v96, vcc, s10, v96
	global_load_dwordx4 v[110:113], v[110:111], off
	s_nop 0
	v_addc_co_u32_e32 v97, vcc, 0, v97, vcc
	global_load_dwordx4 v[114:117], v[114:115], off
	s_nop 0
	global_load_dwordx4 v[118:121], v[96:97], off
	global_load_dwordx4 v[122:125], v2, s[2:3]
	v_lshlrev_b32_e32 v2, 4, v62
	s_waitcnt vmcnt(0)
	v_pk_add_f32 v[122:123], v[122:123], 0 op_sel_hi:[1,0]
	s_nop 0
	v_pk_add_f32 v[110:111], v[110:111], v[122:123]
	v_pk_add_f32 v[96:97], v[124:125], 0 op_sel_hi:[1,0]
	v_pk_add_f32 v[110:111], v[114:115], v[110:111]
	v_pk_add_f32 v[96:97], v[112:113], v[96:97]
	v_pk_add_f32 v[114:115], v[118:119], v[110:111]
	v_pk_add_f32 v[96:97], v[116:117], v[96:97]
	v_lshl_add_u64 v[116:117], s[2:3], 0, v[2:3]
	v_pk_add_f32 v[96:97], v[120:121], v[96:97]
	s_waitcnt vmcnt(0)
	v_pk_fma_f32 v[96:97], v[238:239], v[96:97], v[98:99]
	v_pk_fma_f32 v[98:99], v[236:237], v[114:115], v[108:109]
	v_add_co_u32_e32 v108, vcc, s9, v116
	v_cvt_pk_bf16_f32 v98, v98, v99
	s_nop 0
	v_addc_co_u32_e32 v109, vcc, 0, v117, vcc
	v_add_co_u32_e32 v112, vcc, s8, v116
	global_load_dwordx4 v[108:111], v[108:109], off
	s_nop 0
	v_addc_co_u32_e32 v113, vcc, 0, v117, vcc
	v_add_co_u32_e32 v116, vcc, s10, v116
	global_load_dwordx4 v[112:115], v[112:113], off
	s_nop 0
	v_addc_co_u32_e32 v117, vcc, 0, v117, vcc
	global_load_dwordx4 v[116:119], v[116:117], off
	s_nop 0
	global_load_dwordx4 v[120:123], v2, s[2:3]
	v_lshlrev_b32_e32 v2, 4, v66
	v_cvt_pk_bf16_f32 v99, v96, v97
	v_lshl_add_u64 v[96:97], v[54:55], 0, s[0:1]
	s_waitcnt vmcnt(0)
	v_pk_add_f32 v[122:123], v[122:123], 0 op_sel_hi:[1,0]
	v_pk_add_f32 v[120:121], v[120:121], 0 op_sel_hi:[1,0]
	v_pk_add_f32 v[110:111], v[110:111], v[122:123]
	v_pk_add_f32 v[108:109], v[108:109], v[120:121]
	v_pk_add_f32 v[110:111], v[114:115], v[110:111]
	v_pk_add_f32 v[108:109], v[112:113], v[108:109]
	v_pk_add_f32 v[112:113], v[118:119], v[110:111]
	v_pk_add_f32 v[114:115], v[116:117], v[108:109]
	v_lshl_add_u64 v[116:117], s[2:3], 0, v[2:3]
	s_waitcnt vmcnt(0)
	v_pk_fma_f32 v[106:107], v[240:241], v[114:115], v[106:107]
	v_add_co_u32_e32 v108, vcc, s9, v116
	v_pk_fma_f32 v[104:105], v[242:243], v[112:113], v[104:105]
	s_nop 0
	v_addc_co_u32_e32 v109, vcc, 0, v117, vcc
	v_add_co_u32_e32 v112, vcc, s8, v116
	global_load_dwordx4 v[108:111], v[108:109], off
	s_nop 0
	v_addc_co_u32_e32 v113, vcc, 0, v117, vcc
	v_add_co_u32_e32 v116, vcc, s10, v116
	global_load_dwordx4 v[112:115], v[112:113], off
	s_nop 0
	v_addc_co_u32_e32 v117, vcc, 0, v117, vcc
	global_load_dwordx4 v[116:119], v[116:117], off
	s_nop 0
	global_load_dwordx4 v[120:123], v2, s[2:3]
	v_lshlrev_b32_e32 v2, 4, v70
	s_waitcnt vmcnt(0)
	v_pk_add_f32 v[122:123], v[122:123], 0 op_sel_hi:[1,0]
	v_pk_add_f32 v[120:121], v[120:121], 0 op_sel_hi:[1,0]
	v_pk_add_f32 v[110:111], v[110:111], v[122:123]
	v_pk_add_f32 v[108:109], v[108:109], v[120:121]
	v_pk_add_f32 v[110:111], v[114:115], v[110:111]
	v_pk_add_f32 v[108:109], v[112:113], v[108:109]
	v_pk_add_f32 v[112:113], v[118:119], v[110:111]
	v_pk_add_f32 v[114:115], v[116:117], v[108:109]
	v_lshl_add_u64 v[116:117], s[2:3], 0, v[2:3]
	s_waitcnt vmcnt(0)
	v_pk_fma_f32 v[100:101], v[244:245], v[114:115], v[100:101]
	v_add_co_u32_e32 v108, vcc, s9, v116
	v_pk_fma_f32 v[102:103], v[246:247], v[112:113], v[102:103]
	s_nop 0
	v_addc_co_u32_e32 v109, vcc, 0, v117, vcc
	v_add_co_u32_e32 v112, vcc, s8, v116
	global_load_dwordx4 v[108:111], v[108:109], off
	s_nop 0
	v_addc_co_u32_e32 v113, vcc, 0, v117, vcc
	v_add_co_u32_e32 v116, vcc, s10, v116
	global_load_dwordx4 v[112:115], v[112:113], off
	s_nop 0
	v_addc_co_u32_e32 v117, vcc, 0, v117, vcc
	global_load_dwordx4 v[116:119], v[116:117], off
	s_nop 0
	global_load_dwordx4 v[120:123], v2, s[2:3]
	s_waitcnt vmcnt(0)
	v_pk_add_f32 v[122:123], v[122:123], 0 op_sel_hi:[1,0]
	v_pk_add_f32 v[120:121], v[120:121], 0 op_sel_hi:[1,0]
	v_pk_add_f32 v[110:111], v[110:111], v[122:123]
	v_pk_add_f32 v[108:109], v[108:109], v[120:121]
	v_pk_add_f32 v[110:111], v[114:115], v[110:111]
	v_pk_add_f32 v[108:109], v[112:113], v[108:109]
	v_pk_add_f32 v[112:113], v[118:119], v[110:111]
	v_pk_add_f32 v[114:115], v[116:117], v[108:109]
	s_waitcnt vmcnt(0)
	v_pk_fma_f32 v[92:93], v[250:251], v[112:113], v[92:93]
	v_cvt_pk_bf16_f32 v110, v106, v107
	v_cvt_pk_bf16_f32 v111, v104, v105
	v_pk_fma_f32 v[94:95], v[248:249], v[114:115], v[94:95]
	global_store_dwordx2 v[96:97], v[110:111], off offset:512
	v_lshlrev_b32_e32 v106, 16, v110
	v_and_b32_e32 v107, 0xffff0000, v110
	v_lshlrev_b32_e32 v104, 16, v111
	v_and_b32_e32 v105, 0xffff0000, v111
	v_cvt_pk_bf16_f32 v110, v100, v101
	v_cvt_pk_bf16_f32 v111, v102, v103
	global_store_dwordx2 v[96:97], v[110:111], off offset:1024
	v_lshlrev_b32_e32 v100, 16, v110
	v_and_b32_e32 v101, 0xffff0000, v110
	v_lshlrev_b32_e32 v102, 16, v111
	v_and_b32_e32 v103, 0xffff0000, v111
	v_cvt_pk_bf16_f32 v110, v94, v95
	v_cvt_pk_bf16_f32 v111, v92, v93
	global_store_dwordx2 v[96:97], v[98:99], off
	v_lshlrev_b32_e32 v108, 16, v98
	v_and_b32_e32 v109, 0xffff0000, v98
	v_lshlrev_b32_e32 v98, 16, v99
	v_and_b32_e32 v99, 0xffff0000, v99
	v_lshlrev_b32_e32 v94, 16, v110
	v_and_b32_e32 v95, 0xffff0000, v110
	v_lshlrev_b32_e32 v92, 16, v111
	v_and_b32_e32 v93, 0xffff0000, v111
	global_store_dwordx2 v[96:97], v[110:111], off offset:1536

.LBB0_2071:
	s_min_i32 s0, s56, 0x4000
	s_and_b32 s0, s0, 0xfffff000
	s_add_i32 s0, s0, 0
	s_add_i32 s1, s0, 0xa000
	v_add_u32_e32 v12, s1, v56
	v_add_u32_e32 v2, s0, v56
	ds_read_b128 v[44:47], v53 offset:40960
	ds_read_b128 v[32:35], v53 offset:41984
	ds_read_b128 v[40:43], v2 offset:45056
	ds_read_b128 v[28:31], v2 offset:46080
	ds_read_b128 v[48:51], v12 offset:24576
	ds_read_b128 v[36:39], v12 offset:25600
	ds_read_b128 v[20:23], v53 offset:43008
	ds_read_b128 v[8:11], v53 offset:44032
	ds_read_b128 v[16:19], v2 offset:47104
	ds_read_b128 v[4:7], v2 offset:48128
	ds_read_b128 v[24:27], v12 offset:26624
	ds_read_b128 v[12:15], v12 offset:27648
	s_cmpk_lt_i32 s56, 0x4000
	v_readlane_b32 s2, v255, 53
	s_cselect_b64 s[0:1], -1, 0
	v_readlane_b32 s3, v255, 54
	s_or_b64 s[0:1], s[2:3], s[0:1]
	s_waitcnt vmcnt(11)
	v_lshlrev_b32_e32 v100, 16, v90
	v_and_b32_e32 v101, 0xffff0000, v90
	v_lshlrev_b32_e32 v90, 16, v91
	v_and_b32_e32 v91, 0xffff0000, v91
	s_waitcnt vmcnt(10)
	v_lshlrev_b32_e32 v98, 16, v88
	v_and_b32_e32 v99, 0xffff0000, v88
	v_lshlrev_b32_e32 v96, 16, v89
	v_and_b32_e32 v97, 0xffff0000, v89
	s_waitcnt vmcnt(9)
	v_lshlrev_b32_e32 v92, 16, v86
	v_and_b32_e32 v93, 0xffff0000, v86
	v_lshlrev_b32_e32 v94, 16, v87
	v_and_b32_e32 v95, 0xffff0000, v87
	s_waitcnt vmcnt(8)
	v_lshlrev_b32_e32 v86, 16, v84
	v_and_b32_e32 v87, 0xffff0000, v84
	v_lshlrev_b32_e32 v84, 16, v85
	v_and_b32_e32 v85, 0xffff0000, v85
	s_and_b64 vcc, exec, s[0:1]
	s_cbranch_vccnz .LBB0_2073
	global_load_dwordx4 v[236:239], v[60:61], off
	global_load_dwordx4 v[240:243], v[64:65], off
	global_load_dwordx4 v[244:247], v[68:69], off
	global_load_dwordx4 v[248:251], v[72:73], off
	v_readlane_b32 s2, v255, 13
	s_mov_b32 s57, s81
	s_add_i32 s2, s2, s50
	s_mov_b32 s3, s81
	s_lshl_b64 s[0:1], s[56:57], 11
	s_lshl_b64 s[2:3], s[2:3], 2
	s_add_u32 s2, s6, s2
	s_addc_u32 s3, s7, s3
	s_add_u32 s2, s2, 0x420f8000
	s_addc_u32 s3, s3, 0
	v_lshlrev_b32_e32 v2, 4, v52
	v_lshl_add_u64 v[88:89], s[2:3], 0, v[2:3]
	s_mov_b32 s9, 0x400000
	v_add_co_u32_e32 v102, vcc, s9, v88
	s_mov_b32 s8, 0x800000
	s_nop 0
	v_addc_co_u32_e32 v103, vcc, 0, v89, vcc
	v_add_co_u32_e32 v106, vcc, s8, v88
	s_mov_b32 s10, 0xc00000
	s_nop 0
	v_addc_co_u32_e32 v107, vcc, 0, v89, vcc
	v_add_co_u32_e32 v88, vcc, s10, v88
	global_load_dwordx4 v[102:105], v[102:103], off
	s_nop 0
	v_addc_co_u32_e32 v89, vcc, 0, v89, vcc
	global_load_dwordx4 v[106:109], v[106:107], off
	s_nop 0
	global_load_dwordx4 v[110:113], v[88:89], off
	global_load_dwordx4 v[114:117], v2, s[2:3]
	v_lshlrev_b32_e32 v2, 4, v62
	s_waitcnt vmcnt(0)
	v_pk_add_f32 v[114:115], v[114:115], 0 op_sel_hi:[1,0]
	s_nop 0
	v_pk_add_f32 v[102:103], v[102:103], v[114:115]
	v_pk_add_f32 v[88:89], v[116:117], 0 op_sel_hi:[1,0]
	v_pk_add_f32 v[102:103], v[106:107], v[102:103]
	v_pk_add_f32 v[88:89], v[104:105], v[88:89]
	v_pk_add_f32 v[106:107], v[110:111], v[102:103]
	v_pk_add_f32 v[88:89], v[108:109], v[88:89]
	v_lshl_add_u64 v[108:109], s[2:3], 0, v[2:3]
	v_pk_add_f32 v[88:89], v[112:113], v[88:89]
	s_waitcnt vmcnt(0)
	v_pk_fma_f32 v[88:89], v[238:239], v[88:89], v[90:91]
	v_pk_fma_f32 v[90:91], v[236:237], v[106:107], v[100:101]
	v_add_co_u32_e32 v100, vcc, s9, v108
	v_cvt_pk_bf16_f32 v90, v90, v91
	s_nop 0
	v_addc_co_u32_e32 v101, vcc, 0, v109, vcc
	v_add_co_u32_e32 v104, vcc, s8, v108
	global_load_dwordx4 v[100:103], v[100:101], off
	s_nop 0
	v_addc_co_u32_e32 v105, vcc, 0, v109, vcc
	v_add_co_u32_e32 v108, vcc, s10, v108
	global_load_dwordx4 v[104:107], v[104:105], off
	s_nop 0
	v_addc_co_u32_e32 v109, vcc, 0, v109, vcc
	global_load_dwordx4 v[108:111], v[108:109], off
	s_nop 0
	global_load_dwordx4 v[112:115], v2, s[2:3]
	v_lshlrev_b32_e32 v2, 4, v66
	v_cvt_pk_bf16_f32 v91, v88, v89
	v_lshl_add_u64 v[88:89], v[54:55], 0, s[0:1]
	s_waitcnt vmcnt(0)
	v_pk_add_f32 v[114:115], v[114:115], 0 op_sel_hi:[1,0]
	v_pk_add_f32 v[112:113], v[112:113], 0 op_sel_hi:[1,0]
	v_pk_add_f32 v[102:103], v[102:103], v[114:115]
	v_pk_add_f32 v[100:101], v[100:101], v[112:113]
	v_pk_add_f32 v[102:103], v[106:107], v[102:103]
	v_pk_add_f32 v[100:101], v[104:105], v[100:101]
	v_pk_add_f32 v[104:105], v[110:111], v[102:103]
	v_pk_add_f32 v[106:107], v[108:109], v[100:101]
	v_lshl_add_u64 v[108:109], s[2:3], 0, v[2:3]
	s_waitcnt vmcnt(0)
	v_pk_fma_f32 v[98:99], v[240:241], v[106:107], v[98:99]
	v_add_co_u32_e32 v100, vcc, s9, v108
	v_pk_fma_f32 v[96:97], v[242:243], v[104:105], v[96:97]
	s_nop 0
	v_addc_co_u32_e32 v101, vcc, 0, v109, vcc
	v_add_co_u32_e32 v104, vcc, s8, v108
	global_load_dwordx4 v[100:103], v[100:101], off
	s_nop 0
	v_addc_co_u32_e32 v105, vcc, 0, v109, vcc
	v_add_co_u32_e32 v108, vcc, s10, v108
	global_load_dwordx4 v[104:107], v[104:105], off
	s_nop 0
	v_addc_co_u32_e32 v109, vcc, 0, v109, vcc
	global_load_dwordx4 v[108:111], v[108:109], off
	s_nop 0
	global_load_dwordx4 v[112:115], v2, s[2:3]
	v_lshlrev_b32_e32 v2, 4, v70
	s_waitcnt vmcnt(0)
	v_pk_add_f32 v[114:115], v[114:115], 0 op_sel_hi:[1,0]
	v_pk_add_f32 v[112:113], v[112:113], 0 op_sel_hi:[1,0]
	v_pk_add_f32 v[102:103], v[102:103], v[114:115]
	v_pk_add_f32 v[100:101], v[100:101], v[112:113]
	v_pk_add_f32 v[102:103], v[106:107], v[102:103]
	v_pk_add_f32 v[100:101], v[104:105], v[100:101]
	v_pk_add_f32 v[104:105], v[110:111], v[102:103]
	v_pk_add_f32 v[106:107], v[108:109], v[100:101]
	v_lshl_add_u64 v[108:109], s[2:3], 0, v[2:3]
	s_waitcnt vmcnt(0)
	v_pk_fma_f32 v[92:93], v[244:245], v[106:107], v[92:93]
	v_add_co_u32_e32 v100, vcc, s9, v108
	v_pk_fma_f32 v[94:95], v[246:247], v[104:105], v[94:95]
	s_nop 0
	v_addc_co_u32_e32 v101, vcc, 0, v109, vcc
	v_add_co_u32_e32 v104, vcc, s8, v108
	global_load_dwordx4 v[100:103], v[100:101], off
	s_nop 0
	v_addc_co_u32_e32 v105, vcc, 0, v109, vcc
	v_add_co_u32_e32 v108, vcc, s10, v108
	global_load_dwordx4 v[104:107], v[104:105], off
	s_nop 0
	v_addc_co_u32_e32 v109, vcc, 0, v109, vcc
	global_load_dwordx4 v[108:111], v[108:109], off
	s_nop 0
	global_load_dwordx4 v[112:115], v2, s[2:3]
	s_waitcnt vmcnt(0)
	v_pk_add_f32 v[114:115], v[114:115], 0 op_sel_hi:[1,0]
	v_pk_add_f32 v[112:113], v[112:113], 0 op_sel_hi:[1,0]
	v_pk_add_f32 v[102:103], v[102:103], v[114:115]
	v_pk_add_f32 v[100:101], v[100:101], v[112:113]
	v_pk_add_f32 v[102:103], v[106:107], v[102:103]
	v_pk_add_f32 v[100:101], v[104:105], v[100:101]
	v_pk_add_f32 v[104:105], v[110:111], v[102:103]
	v_pk_add_f32 v[106:107], v[108:109], v[100:101]
	s_waitcnt vmcnt(0)
	v_pk_fma_f32 v[84:85], v[250:251], v[104:105], v[84:85]
	v_cvt_pk_bf16_f32 v102, v98, v99
	v_cvt_pk_bf16_f32 v103, v96, v97
	v_pk_fma_f32 v[86:87], v[248:249], v[106:107], v[86:87]
	global_store_dwordx2 v[88:89], v[102:103], off offset:512
	v_lshlrev_b32_e32 v98, 16, v102
	v_and_b32_e32 v99, 0xffff0000, v102
	v_lshlrev_b32_e32 v96, 16, v103
	v_and_b32_e32 v97, 0xffff0000, v103
	v_cvt_pk_bf16_f32 v102, v92, v93
	v_cvt_pk_bf16_f32 v103, v94, v95
	global_store_dwordx2 v[88:89], v[102:103], off offset:1024
	v_lshlrev_b32_e32 v92, 16, v102
	v_and_b32_e32 v93, 0xffff0000, v102
	v_lshlrev_b32_e32 v94, 16, v103
	v_and_b32_e32 v95, 0xffff0000, v103
	v_cvt_pk_bf16_f32 v102, v86, v87
	v_cvt_pk_bf16_f32 v103, v84, v85
	global_store_dwordx2 v[88:89], v[90:91], off
	v_lshlrev_b32_e32 v100, 16, v90
	v_and_b32_e32 v101, 0xffff0000, v90
	v_lshlrev_b32_e32 v90, 16, v91
	v_and_b32_e32 v91, 0xffff0000, v91
	v_lshlrev_b32_e32 v86, 16, v102
	v_and_b32_e32 v87, 0xffff0000, v102
	v_lshlrev_b32_e32 v84, 16, v103
	v_and_b32_e32 v85, 0xffff0000, v103
	global_store_dwordx2 v[88:89], v[102:103], off offset:1536
